# GEMM mainloops: serpentine order inside MFMA pairs (swap every second pair) so consecutive MFMAs share one source operand
# baseline (speedup 1.0000x reference)
.LBB0_378:
	s_add_u32 s28, s36, 0xfff80080
	s_addc_u32 s29, s37, -1
	s_add_i32 s42, 0, 0x10000
	s_cmp_eq_u32 vcc_hi, 28
	s_cselect_b32 s53, s11, s29
	s_cselect_b32 s52, s21, s28
	s_cselect_b32 s51, s41, s79
	s_cselect_b32 s50, vcc_lo, s78
	s_add_i32 s43, 0, 0x14000
	v_add_u32_e32 v140, s42, v169
	v_add_u32_e32 v173, s43, v169
	ds_read_b128 v[128:131], v140
	ds_read_b128 v[132:135], v140 offset:1024
	ds_read_b128 v[136:139], v140 offset:2048
	ds_read_b128 v[140:143], v140 offset:3072
	ds_read_b128 v[156:159], v173
	ds_read_b128 v[160:163], v173 offset:1024
	ds_read_b128 v[164:167], v173 offset:2048
	ds_read_b128 v[174:177], v173 offset:3072
	v_lshl_add_u64 v[182:183], s[36:37], 0, v[152:153]
	s_add_i32 m0, s88, 0xc000
	ds_read_b128 v[178:181], v172
	ds_read_b128 v[194:197], v172 offset:1024
	ds_read_b128 v[198:201], v172 offset:2048
	ds_read_b128 v[202:205], v172 offset:3072
	ds_read_b128 v[206:209], v172 offset:4096
	ds_read_b128 v[224:227], v172 offset:5120
	ds_read_b128 v[228:231], v172 offset:6144
	ds_read_b128 v[232:235], v172 offset:7168
	global_load_lds_dwordx4 v[182:183], off
	v_lshl_add_u64 v[182:183], s[36:37], 0, v[154:155]
	s_add_i32 m0, s88, 0xe000
	s_nop 0
	global_load_lds_dwordx4 v[182:183], off
	s_waitcnt vmcnt(8)
	s_waitcnt lgkmcnt(0)
	s_barrier
	s_setprio 1
	s_waitcnt lgkmcnt(0)
	v_mfma_f32_16x16x32_bf16 v[124:127], v[128:131], v[178:181], v[124:127]
	v_mfma_f32_16x16x32_bf16 v[120:123], v[136:139], v[178:181], v[120:123]
	v_mfma_f32_16x16x32_bf16 v[108:111], v[136:139], v[198:201], v[108:111]
	v_mfma_f32_16x16x32_bf16 v[116:119], v[128:131], v[198:201], v[116:119]
	v_mfma_f32_16x16x32_bf16 v[100:103], v[128:131], v[206:209], v[100:103]
	v_mfma_f32_16x16x32_bf16 v[92:95], v[136:139], v[206:209], v[92:95]
	v_mfma_f32_16x16x32_bf16 v[76:79], v[136:139], v[228:231], v[76:79]
	v_mfma_f32_16x16x32_bf16 v[84:87], v[128:131], v[228:231], v[84:87]
	v_mfma_f32_16x16x32_bf16 v[124:127], v[132:135], v[194:197], v[124:127]
	v_mfma_f32_16x16x32_bf16 v[120:123], v[140:143], v[194:197], v[120:123]
	v_mfma_f32_16x16x32_bf16 v[108:111], v[140:143], v[202:205], v[108:111]
	v_mfma_f32_16x16x32_bf16 v[116:119], v[132:135], v[202:205], v[116:119]
	v_mfma_f32_16x16x32_bf16 v[100:103], v[132:135], v[224:227], v[100:103]
	v_mfma_f32_16x16x32_bf16 v[92:95], v[140:143], v[224:227], v[92:95]
	v_mfma_f32_16x16x32_bf16 v[76:79], v[140:143], v[232:235], v[76:79]
	v_mfma_f32_16x16x32_bf16 v[84:87], v[132:135], v[232:235], v[84:87]
	s_setprio 0
	s_setprio 1
	v_mfma_f32_16x16x32_bf16 v[112:115], v[156:159], v[178:181], v[112:115]
	v_mfma_f32_16x16x32_bf16 v[104:107], v[164:167], v[178:181], v[104:107]
	v_mfma_f32_16x16x32_bf16 v[88:91], v[164:167], v[198:201], v[88:91]
	v_mfma_f32_16x16x32_bf16 v[96:99], v[156:159], v[198:201], v[96:99]
	v_mfma_f32_16x16x32_bf16 v[80:83], v[156:159], v[206:209], v[80:83]
	v_mfma_f32_16x16x32_bf16 v[72:75], v[164:167], v[206:209], v[72:75]
	v_mfma_f32_16x16x32_bf16 v[64:67], v[164:167], v[228:231], v[64:67]
	v_mfma_f32_16x16x32_bf16 v[68:71], v[156:159], v[228:231], v[68:71]
	v_mfma_f32_16x16x32_bf16 v[112:115], v[160:163], v[194:197], v[112:115]
	v_mfma_f32_16x16x32_bf16 v[104:107], v[174:177], v[194:197], v[104:107]
	v_mfma_f32_16x16x32_bf16 v[88:91], v[174:177], v[202:205], v[88:91]
	v_mfma_f32_16x16x32_bf16 v[96:99], v[160:163], v[202:205], v[96:99]
	v_mfma_f32_16x16x32_bf16 v[80:83], v[160:163], v[224:227], v[80:83]
	v_mfma_f32_16x16x32_bf16 v[72:75], v[174:177], v[224:227], v[72:75]
	v_mfma_f32_16x16x32_bf16 v[64:67], v[174:177], v[232:235], v[64:67]
	v_mfma_f32_16x16x32_bf16 v[68:71], v[160:163], v[232:235], v[68:71]
	s_setprio 0
	s_barrier
	s_add_i32 s28, s42, s62
	v_lshl_add_u64 v[182:183], s[50:51], 0, v[146:147]
	s_mov_b32 m0, s28
	ds_read_b128 v[178:181], v172 offset:16384
	ds_read_b128 v[194:197], v172 offset:17408
	ds_read_b128 v[198:201], v172 offset:18432
	ds_read_b128 v[202:205], v172 offset:19456
	ds_read_b128 v[206:209], v172 offset:20480
	ds_read_b128 v[224:227], v172 offset:21504
	ds_read_b128 v[228:231], v172 offset:22528
	ds_read_b128 v[232:235], v172 offset:23552
	global_load_lds_dwordx4 v[182:183], off
	s_add_i32 m0, s28, 0x2000
	s_add_u32 s28, s50, 0x80000
	v_lshl_add_u64 v[210:211], s[50:51], 0, v[150:151]
	s_addc_u32 s29, s51, 0
	s_add_i32 s42, s43, s62
	global_load_lds_dwordx4 v[210:211], off
	v_lshl_add_u64 v[236:237], s[28:29], 0, v[146:147]
	s_mov_b32 m0, s42
	v_lshl_add_u64 v[238:239], s[52:53], 0, v[148:149]
	global_load_lds_dwordx4 v[236:237], off
	v_lshl_add_u64 v[236:237], s[28:29], 0, v[150:151]
	s_add_i32 m0, s42, 0x2000
	s_nop 0
	global_load_lds_dwordx4 v[236:237], off
	v_lshl_add_u64 v[236:237], s[52:53], 0, v[144:145]
	s_mov_b32 m0, s88
	s_nop 0
	global_load_lds_dwordx4 v[236:237], off
	s_mov_b32 m0, s89
	s_nop 0
	global_load_lds_dwordx4 v[238:239], off
	s_waitcnt vmcnt(8)
	s_waitcnt lgkmcnt(0)
	s_barrier
	s_setprio 1
	s_waitcnt lgkmcnt(0)
	v_mfma_f32_16x16x32_bf16 v[60:63], v[128:131], v[178:181], v[60:63]
	v_mfma_f32_16x16x32_bf16 v[56:59], v[136:139], v[178:181], v[56:59]
	v_mfma_f32_16x16x32_bf16 v[44:47], v[136:139], v[198:201], v[44:47]
	v_mfma_f32_16x16x32_bf16 v[52:55], v[128:131], v[198:201], v[52:55]
	v_mfma_f32_16x16x32_bf16 v[36:39], v[128:131], v[206:209], v[36:39]
	v_mfma_f32_16x16x32_bf16 v[28:31], v[136:139], v[206:209], v[28:31]
	v_mfma_f32_16x16x32_bf16 v[12:15], v[136:139], v[228:231], v[12:15]
	v_mfma_f32_16x16x32_bf16 v[20:23], v[128:131], v[228:231], v[20:23]
	v_mfma_f32_16x16x32_bf16 v[60:63], v[132:135], v[194:197], v[60:63]
	v_mfma_f32_16x16x32_bf16 v[56:59], v[140:143], v[194:197], v[56:59]
	v_mfma_f32_16x16x32_bf16 v[44:47], v[140:143], v[202:205], v[44:47]
	v_mfma_f32_16x16x32_bf16 v[52:55], v[132:135], v[202:205], v[52:55]
	v_mfma_f32_16x16x32_bf16 v[36:39], v[132:135], v[224:227], v[36:39]
	v_mfma_f32_16x16x32_bf16 v[28:31], v[140:143], v[224:227], v[28:31]
	v_mfma_f32_16x16x32_bf16 v[12:15], v[140:143], v[232:235], v[12:15]
	v_mfma_f32_16x16x32_bf16 v[20:23], v[132:135], v[232:235], v[20:23]
	s_setprio 0
	s_setprio 1
	v_mfma_f32_16x16x32_bf16 v[48:51], v[156:159], v[178:181], v[48:51]
	v_mfma_f32_16x16x32_bf16 v[40:43], v[164:167], v[178:181], v[40:43]
	v_mfma_f32_16x16x32_bf16 v[24:27], v[164:167], v[198:201], v[24:27]
	v_mfma_f32_16x16x32_bf16 v[32:35], v[156:159], v[198:201], v[32:35]
	v_mfma_f32_16x16x32_bf16 v[16:19], v[156:159], v[206:209], v[16:19]
	v_mfma_f32_16x16x32_bf16 v[8:11], v[164:167], v[206:209], v[8:11]
	v_mfma_f32_16x16x32_bf16 v[0:3], v[164:167], v[228:231], v[0:3]
	v_mfma_f32_16x16x32_bf16 v[4:7], v[156:159], v[228:231], v[4:7]
	v_mfma_f32_16x16x32_bf16 v[48:51], v[160:163], v[194:197], v[48:51]
	v_mfma_f32_16x16x32_bf16 v[40:43], v[174:177], v[194:197], v[40:43]
	v_mfma_f32_16x16x32_bf16 v[24:27], v[174:177], v[202:205], v[24:27]
	v_mfma_f32_16x16x32_bf16 v[32:35], v[160:163], v[202:205], v[32:35]
	v_mfma_f32_16x16x32_bf16 v[16:19], v[160:163], v[224:227], v[16:19]
	v_mfma_f32_16x16x32_bf16 v[8:11], v[174:177], v[224:227], v[8:11]
	v_mfma_f32_16x16x32_bf16 v[0:3], v[174:177], v[232:235], v[0:3]
	v_mfma_f32_16x16x32_bf16 v[4:7], v[160:163], v[232:235], v[4:7]
	s_setprio 0
	s_barrier
	s_add_i32 s42, 0, 0x18000
	s_add_i32 s43, 0, 0x1c000
	v_add_u32_e32 v140, s42, v169
	v_add_u32_e32 v173, s43, v169
	ds_read_b128 v[128:131], v140
	ds_read_b128 v[132:135], v140 offset:1024
	ds_read_b128 v[136:139], v140 offset:2048
	ds_read_b128 v[140:143], v140 offset:3072
	ds_read_b128 v[156:159], v173
	ds_read_b128 v[160:163], v173 offset:1024
	ds_read_b128 v[164:167], v173 offset:2048
	ds_read_b128 v[174:177], v173 offset:3072
	s_add_u32 s28, s52, 0x80000
	s_addc_u32 s29, s53, 0
	s_mov_b32 m0, s26
	v_lshl_add_u64 v[240:241], s[28:29], 0, v[144:145]
	ds_read_b128 v[178:181], v172 offset:32768
	ds_read_b128 v[194:197], v172 offset:33792
	ds_read_b128 v[198:201], v172 offset:34816
	ds_read_b128 v[202:205], v172 offset:35840
	ds_read_b128 v[206:209], v172 offset:36864
	ds_read_b128 v[224:227], v172 offset:37888
	ds_read_b128 v[228:231], v172 offset:38912
	ds_read_b128 v[232:235], v172 offset:39936
	global_load_lds_dwordx4 v[240:241], off
	v_lshl_add_u64 v[240:241], s[28:29], 0, v[148:149]
	s_mov_b32 m0, s27
	s_nop 0
	global_load_lds_dwordx4 v[240:241], off
	s_waitcnt vmcnt(8)
	s_waitcnt lgkmcnt(0)
	s_barrier
	s_setprio 1
	s_waitcnt lgkmcnt(0)
	v_mfma_f32_16x16x32_bf16 v[124:127], v[128:131], v[178:181], v[124:127]
	v_mfma_f32_16x16x32_bf16 v[120:123], v[136:139], v[178:181], v[120:123]
	v_mfma_f32_16x16x32_bf16 v[108:111], v[136:139], v[198:201], v[108:111]
	v_mfma_f32_16x16x32_bf16 v[116:119], v[128:131], v[198:201], v[116:119]
	v_mfma_f32_16x16x32_bf16 v[100:103], v[128:131], v[206:209], v[100:103]
	v_mfma_f32_16x16x32_bf16 v[92:95], v[136:139], v[206:209], v[92:95]
	v_mfma_f32_16x16x32_bf16 v[76:79], v[136:139], v[228:231], v[76:79]
	v_mfma_f32_16x16x32_bf16 v[84:87], v[128:131], v[228:231], v[84:87]
	v_mfma_f32_16x16x32_bf16 v[124:127], v[132:135], v[194:197], v[124:127]
	v_mfma_f32_16x16x32_bf16 v[120:123], v[140:143], v[194:197], v[120:123]
	v_mfma_f32_16x16x32_bf16 v[108:111], v[140:143], v[202:205], v[108:111]
	v_mfma_f32_16x16x32_bf16 v[116:119], v[132:135], v[202:205], v[116:119]
	v_mfma_f32_16x16x32_bf16 v[100:103], v[132:135], v[224:227], v[100:103]
	v_mfma_f32_16x16x32_bf16 v[92:95], v[140:143], v[224:227], v[92:95]
	v_mfma_f32_16x16x32_bf16 v[76:79], v[140:143], v[232:235], v[76:79]
	v_mfma_f32_16x16x32_bf16 v[84:87], v[132:135], v[232:235], v[84:87]
	s_setprio 0
	s_setprio 1
	v_mfma_f32_16x16x32_bf16 v[112:115], v[156:159], v[178:181], v[112:115]
	v_mfma_f32_16x16x32_bf16 v[104:107], v[164:167], v[178:181], v[104:107]
	v_mfma_f32_16x16x32_bf16 v[88:91], v[164:167], v[198:201], v[88:91]
	v_mfma_f32_16x16x32_bf16 v[96:99], v[156:159], v[198:201], v[96:99]
	v_mfma_f32_16x16x32_bf16 v[80:83], v[156:159], v[206:209], v[80:83]
	v_mfma_f32_16x16x32_bf16 v[72:75], v[164:167], v[206:209], v[72:75]
	v_mfma_f32_16x16x32_bf16 v[64:67], v[164:167], v[228:231], v[64:67]
	v_mfma_f32_16x16x32_bf16 v[68:71], v[156:159], v[228:231], v[68:71]
	v_mfma_f32_16x16x32_bf16 v[112:115], v[160:163], v[194:197], v[112:115]
	v_mfma_f32_16x16x32_bf16 v[104:107], v[174:177], v[194:197], v[104:107]
	v_mfma_f32_16x16x32_bf16 v[88:91], v[174:177], v[202:205], v[88:91]
	v_mfma_f32_16x16x32_bf16 v[96:99], v[160:163], v[202:205], v[96:99]
	v_mfma_f32_16x16x32_bf16 v[80:83], v[160:163], v[224:227], v[80:83]
	v_mfma_f32_16x16x32_bf16 v[72:75], v[174:177], v[224:227], v[72:75]
	v_mfma_f32_16x16x32_bf16 v[64:67], v[174:177], v[232:235], v[64:67]
	v_mfma_f32_16x16x32_bf16 v[68:71], v[160:163], v[232:235], v[68:71]
	s_setprio 0
	s_barrier
	s_add_i32 s28, s42, s62
	v_lshl_add_u64 v[182:183], v[182:183], 0, s[68:69]
	s_mov_b32 m0, s28
	ds_read_b128 v[178:181], v172 offset:49152
	ds_read_b128 v[194:197], v172 offset:50176
	ds_read_b128 v[198:201], v172 offset:51200
	ds_read_b128 v[202:205], v172 offset:52224
	ds_read_b128 v[206:209], v172 offset:53248
	ds_read_b128 v[224:227], v172 offset:54272
	ds_read_b128 v[228:231], v172 offset:55296
	ds_read_b128 v[232:235], v172 offset:56320
	global_load_lds_dwordx4 v[182:183], off
	s_add_i32 m0, s28, 0x2000
	s_add_u32 s28, s50, 0x80080
	v_lshl_add_u64 v[182:183], v[210:211], 0, s[68:69]
	s_addc_u32 s29, s51, 0
	s_add_i32 s42, s43, s62
	global_load_lds_dwordx4 v[182:183], off
	v_lshl_add_u64 v[182:183], s[28:29], 0, v[146:147]
	s_mov_b32 m0, s42
	s_nop 0
	global_load_lds_dwordx4 v[182:183], off
	v_lshl_add_u64 v[182:183], s[28:29], 0, v[150:151]
	s_add_i32 m0, s42, 0x2000
	s_nop 0
	global_load_lds_dwordx4 v[182:183], off
	v_lshl_add_u64 v[182:183], v[236:237], 0, s[68:69]
	s_mov_b32 m0, s94
	s_nop 0
	global_load_lds_dwordx4 v[182:183], off
	v_lshl_add_u64 v[182:183], v[238:239], 0, s[68:69]
	s_mov_b32 m0, s95
	s_nop 0
	global_load_lds_dwordx4 v[182:183], off
	s_waitcnt vmcnt(8)
	s_waitcnt lgkmcnt(0)
	s_barrier
	s_setprio 1
	s_waitcnt lgkmcnt(0)
	v_mfma_f32_16x16x32_bf16 v[60:63], v[128:131], v[178:181], v[60:63]
	v_mfma_f32_16x16x32_bf16 v[56:59], v[136:139], v[178:181], v[56:59]
	v_mfma_f32_16x16x32_bf16 v[44:47], v[136:139], v[198:201], v[44:47]
	v_mfma_f32_16x16x32_bf16 v[52:55], v[128:131], v[198:201], v[52:55]
	v_mfma_f32_16x16x32_bf16 v[36:39], v[128:131], v[206:209], v[36:39]
	v_mfma_f32_16x16x32_bf16 v[28:31], v[136:139], v[206:209], v[28:31]
	v_mfma_f32_16x16x32_bf16 v[12:15], v[136:139], v[228:231], v[12:15]
	v_mfma_f32_16x16x32_bf16 v[20:23], v[128:131], v[228:231], v[20:23]
	v_mfma_f32_16x16x32_bf16 v[60:63], v[132:135], v[194:197], v[60:63]
	v_mfma_f32_16x16x32_bf16 v[56:59], v[140:143], v[194:197], v[56:59]
	v_mfma_f32_16x16x32_bf16 v[44:47], v[140:143], v[202:205], v[44:47]
	v_mfma_f32_16x16x32_bf16 v[52:55], v[132:135], v[202:205], v[52:55]
	v_mfma_f32_16x16x32_bf16 v[36:39], v[132:135], v[224:227], v[36:39]
	v_mfma_f32_16x16x32_bf16 v[28:31], v[140:143], v[224:227], v[28:31]
	v_mfma_f32_16x16x32_bf16 v[12:15], v[140:143], v[232:235], v[12:15]
	v_mfma_f32_16x16x32_bf16 v[20:23], v[132:135], v[232:235], v[20:23]
	s_setprio 0
	s_setprio 1
	v_mfma_f32_16x16x32_bf16 v[48:51], v[156:159], v[178:181], v[48:51]
	v_mfma_f32_16x16x32_bf16 v[40:43], v[164:167], v[178:181], v[40:43]
	v_mfma_f32_16x16x32_bf16 v[24:27], v[164:167], v[198:201], v[24:27]
	v_mfma_f32_16x16x32_bf16 v[32:35], v[156:159], v[198:201], v[32:35]
	v_mfma_f32_16x16x32_bf16 v[16:19], v[156:159], v[206:209], v[16:19]
	v_mfma_f32_16x16x32_bf16 v[8:11], v[164:167], v[206:209], v[8:11]
	v_mfma_f32_16x16x32_bf16 v[0:3], v[164:167], v[228:231], v[0:3]
	v_mfma_f32_16x16x32_bf16 v[4:7], v[156:159], v[228:231], v[4:7]
	v_mfma_f32_16x16x32_bf16 v[48:51], v[160:163], v[194:197], v[48:51]
	v_mfma_f32_16x16x32_bf16 v[40:43], v[174:177], v[194:197], v[40:43]
	v_mfma_f32_16x16x32_bf16 v[24:27], v[174:177], v[202:205], v[24:27]
	v_mfma_f32_16x16x32_bf16 v[32:35], v[160:163], v[202:205], v[32:35]
	v_mfma_f32_16x16x32_bf16 v[16:19], v[160:163], v[224:227], v[16:19]
	v_mfma_f32_16x16x32_bf16 v[8:11], v[174:177], v[224:227], v[8:11]
	v_mfma_f32_16x16x32_bf16 v[0:3], v[174:177], v[232:235], v[0:3]
	v_mfma_f32_16x16x32_bf16 v[4:7], v[160:163], v[232:235], v[4:7]
	s_setprio 0
	s_barrier
	s_add_i32 vcc_hi, vcc_hi, 2
	s_add_u32 s36, s36, 0x100
	s_addc_u32 s37, s37, 0
	s_add_u32 s78, s78, 0x100
	s_addc_u32 s79, s79, 0
	s_cmp_gt_u32 vcc_hi, 29
	s_cbranch_scc0 .LBB0_378
	s_and_b64 vcc, exec, s[14:15]
	s_cbranch_vccz .LBB0_381
	s_barrier

.LBB0_514:
	s_add_u32 s42, s30, s44
	s_addc_u32 s43, s31, 0
	s_add_u32 s40, s42, 0x100
	s_addc_u32 s41, s43, 0
	s_and_b64 s[28:29], s[38:39], exec
	s_cselect_b32 s41, s9, s41
	s_cselect_b32 s40, s63, s40
	s_add_u32 s28, s18, s44
	s_addc_u32 s29, s19, 0
	s_add_u32 s44, s28, 0x100
	s_addc_u32 s45, s29, 0
	s_add_i32 s76, 0, 0x10000
	s_and_b64 s[28:29], s[38:39], exec
	s_cselect_b32 s44, s79, s44
	s_cselect_b32 s45, s78, s45
	s_add_i32 s85, 0, 0x14000
	v_add_u32_e32 v158, s76, v136
	v_add_u32_e32 v174, s85, v136
	ds_read_b128 v[146:149], v158
	ds_read_b128 v[150:153], v158 offset:1024
	ds_read_b128 v[154:157], v158 offset:2048
	ds_read_b128 v[158:161], v158 offset:3072
	ds_read_b128 v[162:165], v174
	ds_read_b128 v[166:169], v174 offset:1024
	ds_read_b128 v[170:173], v174 offset:2048
	ds_read_b128 v[174:177], v174 offset:3072
	s_add_u32 s46, s42, 0x10080
	s_addc_u32 s47, s43, 0
	s_add_i32 s29, s76, s4
	s_add_i32 s43, s85, s4
	s_add_i32 m0, s20, 0xc000
	s_add_i32 s90, s20, 0xe000
	s_add_i32 s49, s29, 0x2000
	s_add_i32 s42, s43, 0x2000
	s_add_i32 s48, 0, 0x18000
	s_add_i32 s28, 0, 0x1c000
	s_add_u32 s38, s40, 0x10000
	s_addc_u32 s39, s41, 0
	s_add_i32 s88, s48, s4
	s_add_i32 s76, s28, s4
	s_add_i32 s89, s88, 0x2000
	s_add_i32 s85, s76, 0x2000
	v_lshl_add_u64 v[182:183], s[46:47], 0, v[134:135]
	ds_read_b128 v[178:181], v145
	ds_read_b128 v[194:197], v145 offset:1024
	ds_read_b128 v[198:201], v145 offset:2048
	ds_read_b128 v[202:205], v145 offset:3072
	ds_read_b128 v[206:209], v145 offset:4096
	ds_read_b128 v[224:227], v145 offset:5120
	ds_read_b128 v[228:231], v145 offset:6144
	ds_read_b128 v[232:235], v145 offset:7168
	global_load_lds_dwordx4 v[182:183], off
	v_lshl_add_u64 v[182:183], s[46:47], 0, v[130:131]
	s_mov_b32 m0, s90
	s_nop 0
	global_load_lds_dwordx4 v[182:183], off
	s_waitcnt vmcnt(8)
	s_waitcnt lgkmcnt(0)
	s_barrier
	s_setprio 1
	s_waitcnt lgkmcnt(0)
	v_mfma_f32_16x16x32_bf16 v[124:127], v[146:149], v[178:181], v[124:127]
	v_mfma_f32_16x16x32_bf16 v[120:123], v[154:157], v[178:181], v[120:123]
	v_mfma_f32_16x16x32_bf16 v[104:107], v[154:157], v[198:201], v[104:107]
	v_mfma_f32_16x16x32_bf16 v[112:115], v[146:149], v[198:201], v[112:115]
	v_mfma_f32_16x16x32_bf16 v[96:99], v[146:149], v[206:209], v[96:99]
	v_mfma_f32_16x16x32_bf16 v[88:91], v[154:157], v[206:209], v[88:91]
	v_mfma_f32_16x16x32_bf16 v[72:75], v[154:157], v[228:231], v[72:75]
	v_mfma_f32_16x16x32_bf16 v[80:83], v[146:149], v[228:231], v[80:83]
	v_mfma_f32_16x16x32_bf16 v[124:127], v[150:153], v[194:197], v[124:127]
	v_mfma_f32_16x16x32_bf16 v[120:123], v[158:161], v[194:197], v[120:123]
	v_mfma_f32_16x16x32_bf16 v[104:107], v[158:161], v[202:205], v[104:107]
	v_mfma_f32_16x16x32_bf16 v[112:115], v[150:153], v[202:205], v[112:115]
	v_mfma_f32_16x16x32_bf16 v[96:99], v[150:153], v[224:227], v[96:99]
	v_mfma_f32_16x16x32_bf16 v[88:91], v[158:161], v[224:227], v[88:91]
	v_mfma_f32_16x16x32_bf16 v[72:75], v[158:161], v[232:235], v[72:75]
	v_mfma_f32_16x16x32_bf16 v[80:83], v[150:153], v[232:235], v[80:83]
	s_setprio 0
	s_setprio 1
	v_mfma_f32_16x16x32_bf16 v[116:119], v[162:165], v[178:181], v[116:119]
	v_mfma_f32_16x16x32_bf16 v[108:111], v[170:173], v[178:181], v[108:111]
	v_mfma_f32_16x16x32_bf16 v[92:95], v[170:173], v[198:201], v[92:95]
	v_mfma_f32_16x16x32_bf16 v[100:103], v[162:165], v[198:201], v[100:103]
	v_mfma_f32_16x16x32_bf16 v[84:87], v[162:165], v[206:209], v[84:87]
	v_mfma_f32_16x16x32_bf16 v[76:79], v[170:173], v[206:209], v[76:79]
	v_mfma_f32_16x16x32_bf16 v[64:67], v[170:173], v[228:231], v[64:67]
	v_mfma_f32_16x16x32_bf16 v[68:71], v[162:165], v[228:231], v[68:71]
	v_mfma_f32_16x16x32_bf16 v[116:119], v[166:169], v[194:197], v[116:119]
	v_mfma_f32_16x16x32_bf16 v[108:111], v[174:177], v[194:197], v[108:111]
	v_mfma_f32_16x16x32_bf16 v[92:95], v[174:177], v[202:205], v[92:95]
	v_mfma_f32_16x16x32_bf16 v[100:103], v[166:169], v[202:205], v[100:103]
	v_mfma_f32_16x16x32_bf16 v[84:87], v[166:169], v[224:227], v[84:87]
	v_mfma_f32_16x16x32_bf16 v[76:79], v[174:177], v[224:227], v[76:79]
	v_mfma_f32_16x16x32_bf16 v[64:67], v[174:177], v[232:235], v[64:67]
	v_mfma_f32_16x16x32_bf16 v[68:71], v[166:169], v[232:235], v[68:71]
	s_setprio 0
	s_barrier
	s_mov_b32 m0, s29
	v_lshl_add_u64 v[182:183], s[44:45], 0, v[132:133]
	ds_read_b128 v[178:181], v145 offset:16384
	ds_read_b128 v[194:197], v145 offset:17408
	ds_read_b128 v[198:201], v145 offset:18432
	ds_read_b128 v[202:205], v145 offset:19456
	ds_read_b128 v[206:209], v145 offset:20480
	ds_read_b128 v[224:227], v145 offset:21504
	ds_read_b128 v[228:231], v145 offset:22528
	ds_read_b128 v[232:235], v145 offset:23552
	global_load_lds_dwordx4 v[182:183], off
	v_lshl_add_u64 v[210:211], s[44:45], 0, v[128:129]
	s_mov_b32 m0, s49
	v_lshl_add_u64 v[236:237], v[182:183], 0, s[70:71]
	global_load_lds_dwordx4 v[210:211], off
	s_mov_b32 m0, s43
	v_lshl_add_u64 v[238:239], s[40:41], 0, v[130:131]
	global_load_lds_dwordx4 v[236:237], off
	v_lshl_add_u64 v[236:237], v[210:211], 0, s[70:71]
	s_mov_b32 m0, s42
	s_nop 0
	global_load_lds_dwordx4 v[236:237], off
	v_lshl_add_u64 v[236:237], s[40:41], 0, v[134:135]
	s_mov_b32 m0, s20
	s_nop 0
	global_load_lds_dwordx4 v[236:237], off
	s_mov_b32 m0, s21
	s_nop 0
	global_load_lds_dwordx4 v[238:239], off
	s_waitcnt vmcnt(8)
	s_waitcnt lgkmcnt(0)
	s_barrier
	s_setprio 1
	s_waitcnt lgkmcnt(0)
	v_mfma_f32_16x16x32_bf16 v[60:63], v[146:149], v[178:181], v[60:63]
	v_mfma_f32_16x16x32_bf16 v[56:59], v[154:157], v[178:181], v[56:59]
	v_mfma_f32_16x16x32_bf16 v[40:43], v[154:157], v[198:201], v[40:43]
	v_mfma_f32_16x16x32_bf16 v[48:51], v[146:149], v[198:201], v[48:51]
	v_mfma_f32_16x16x32_bf16 v[32:35], v[146:149], v[206:209], v[32:35]
	v_mfma_f32_16x16x32_bf16 v[24:27], v[154:157], v[206:209], v[24:27]
	v_mfma_f32_16x16x32_bf16 v[8:11], v[154:157], v[228:231], v[8:11]
	v_mfma_f32_16x16x32_bf16 v[16:19], v[146:149], v[228:231], v[16:19]
	v_mfma_f32_16x16x32_bf16 v[60:63], v[150:153], v[194:197], v[60:63]
	v_mfma_f32_16x16x32_bf16 v[56:59], v[158:161], v[194:197], v[56:59]
	v_mfma_f32_16x16x32_bf16 v[40:43], v[158:161], v[202:205], v[40:43]
	v_mfma_f32_16x16x32_bf16 v[48:51], v[150:153], v[202:205], v[48:51]
	v_mfma_f32_16x16x32_bf16 v[32:35], v[150:153], v[224:227], v[32:35]
	v_mfma_f32_16x16x32_bf16 v[24:27], v[158:161], v[224:227], v[24:27]
	v_mfma_f32_16x16x32_bf16 v[8:11], v[158:161], v[232:235], v[8:11]
	v_mfma_f32_16x16x32_bf16 v[16:19], v[150:153], v[232:235], v[16:19]
	s_setprio 0
	s_setprio 1
	v_mfma_f32_16x16x32_bf16 v[52:55], v[162:165], v[178:181], v[52:55]
	v_mfma_f32_16x16x32_bf16 v[44:47], v[170:173], v[178:181], v[44:47]
	v_mfma_f32_16x16x32_bf16 v[28:31], v[170:173], v[198:201], v[28:31]
	v_mfma_f32_16x16x32_bf16 v[36:39], v[162:165], v[198:201], v[36:39]
	v_mfma_f32_16x16x32_bf16 v[20:23], v[162:165], v[206:209], v[20:23]
	v_mfma_f32_16x16x32_bf16 v[12:15], v[170:173], v[206:209], v[12:15]
	v_mfma_f32_16x16x32_bf16 v[0:3], v[170:173], v[228:231], v[0:3]
	v_mfma_f32_16x16x32_bf16 v[4:7], v[162:165], v[228:231], v[4:7]
	v_mfma_f32_16x16x32_bf16 v[52:55], v[166:169], v[194:197], v[52:55]
	v_mfma_f32_16x16x32_bf16 v[44:47], v[174:177], v[194:197], v[44:47]
	v_mfma_f32_16x16x32_bf16 v[28:31], v[174:177], v[202:205], v[28:31]
	v_mfma_f32_16x16x32_bf16 v[36:39], v[166:169], v[202:205], v[36:39]
	v_mfma_f32_16x16x32_bf16 v[20:23], v[166:169], v[224:227], v[20:23]
	v_mfma_f32_16x16x32_bf16 v[12:15], v[174:177], v[224:227], v[12:15]
	v_mfma_f32_16x16x32_bf16 v[0:3], v[174:177], v[232:235], v[0:3]
	v_mfma_f32_16x16x32_bf16 v[4:7], v[166:169], v[232:235], v[4:7]
	s_setprio 0
	s_barrier
	v_add_u32_e32 v158, s48, v136
	v_add_u32_e32 v174, s28, v136
	ds_read_b128 v[146:149], v158
	ds_read_b128 v[150:153], v158 offset:1024
	ds_read_b128 v[154:157], v158 offset:2048
	ds_read_b128 v[158:161], v158 offset:3072
	ds_read_b128 v[162:165], v174
	ds_read_b128 v[166:169], v174 offset:1024
	ds_read_b128 v[170:173], v174 offset:2048
	ds_read_b128 v[174:177], v174 offset:3072
	s_mov_b32 m0, s26
	v_lshl_add_u64 v[240:241], s[38:39], 0, v[134:135]
	ds_read_b128 v[178:181], v145 offset:32768
	ds_read_b128 v[194:197], v145 offset:33792
	ds_read_b128 v[198:201], v145 offset:34816
	ds_read_b128 v[202:205], v145 offset:35840
	ds_read_b128 v[206:209], v145 offset:36864
	ds_read_b128 v[224:227], v145 offset:37888
	ds_read_b128 v[228:231], v145 offset:38912
	ds_read_b128 v[232:235], v145 offset:39936
	global_load_lds_dwordx4 v[240:241], off
	v_lshl_add_u64 v[240:241], s[38:39], 0, v[130:131]
	s_mov_b32 m0, s27
	s_nop 0
	global_load_lds_dwordx4 v[240:241], off
	s_waitcnt vmcnt(8)
	s_waitcnt lgkmcnt(0)
	s_barrier
	s_setprio 1
	s_waitcnt lgkmcnt(0)
	v_mfma_f32_16x16x32_bf16 v[124:127], v[146:149], v[178:181], v[124:127]
	v_mfma_f32_16x16x32_bf16 v[120:123], v[154:157], v[178:181], v[120:123]
	v_mfma_f32_16x16x32_bf16 v[104:107], v[154:157], v[198:201], v[104:107]
	v_mfma_f32_16x16x32_bf16 v[112:115], v[146:149], v[198:201], v[112:115]
	v_mfma_f32_16x16x32_bf16 v[96:99], v[146:149], v[206:209], v[96:99]
	v_mfma_f32_16x16x32_bf16 v[88:91], v[154:157], v[206:209], v[88:91]
	v_mfma_f32_16x16x32_bf16 v[72:75], v[154:157], v[228:231], v[72:75]
	v_mfma_f32_16x16x32_bf16 v[80:83], v[146:149], v[228:231], v[80:83]
	v_mfma_f32_16x16x32_bf16 v[124:127], v[150:153], v[194:197], v[124:127]
	v_mfma_f32_16x16x32_bf16 v[120:123], v[158:161], v[194:197], v[120:123]
	v_mfma_f32_16x16x32_bf16 v[104:107], v[158:161], v[202:205], v[104:107]
	v_mfma_f32_16x16x32_bf16 v[112:115], v[150:153], v[202:205], v[112:115]
	v_mfma_f32_16x16x32_bf16 v[96:99], v[150:153], v[224:227], v[96:99]
	v_mfma_f32_16x16x32_bf16 v[88:91], v[158:161], v[224:227], v[88:91]
	v_mfma_f32_16x16x32_bf16 v[72:75], v[158:161], v[232:235], v[72:75]
	v_mfma_f32_16x16x32_bf16 v[80:83], v[150:153], v[232:235], v[80:83]
	s_setprio 0
	s_setprio 1
	v_mfma_f32_16x16x32_bf16 v[116:119], v[162:165], v[178:181], v[116:119]
	v_mfma_f32_16x16x32_bf16 v[108:111], v[170:173], v[178:181], v[108:111]
	v_mfma_f32_16x16x32_bf16 v[92:95], v[170:173], v[198:201], v[92:95]
	v_mfma_f32_16x16x32_bf16 v[100:103], v[162:165], v[198:201], v[100:103]
	v_mfma_f32_16x16x32_bf16 v[84:87], v[162:165], v[206:209], v[84:87]
	v_mfma_f32_16x16x32_bf16 v[76:79], v[170:173], v[206:209], v[76:79]
	v_mfma_f32_16x16x32_bf16 v[64:67], v[170:173], v[228:231], v[64:67]
	v_mfma_f32_16x16x32_bf16 v[68:71], v[162:165], v[228:231], v[68:71]
	v_mfma_f32_16x16x32_bf16 v[116:119], v[166:169], v[194:197], v[116:119]
	v_mfma_f32_16x16x32_bf16 v[108:111], v[174:177], v[194:197], v[108:111]
	v_mfma_f32_16x16x32_bf16 v[92:95], v[174:177], v[202:205], v[92:95]
	v_mfma_f32_16x16x32_bf16 v[100:103], v[166:169], v[202:205], v[100:103]
	v_mfma_f32_16x16x32_bf16 v[84:87], v[166:169], v[224:227], v[84:87]
	v_mfma_f32_16x16x32_bf16 v[76:79], v[174:177], v[224:227], v[76:79]
	v_mfma_f32_16x16x32_bf16 v[64:67], v[174:177], v[232:235], v[64:67]
	v_mfma_f32_16x16x32_bf16 v[68:71], v[166:169], v[232:235], v[68:71]
	s_setprio 0
	s_barrier
	s_mov_b32 m0, s88
	v_lshl_add_u64 v[240:241], v[182:183], 0, s[68:69]
	ds_read_b128 v[178:181], v145 offset:49152
	ds_read_b128 v[194:197], v145 offset:50176
	ds_read_b128 v[198:201], v145 offset:51200
	ds_read_b128 v[202:205], v145 offset:52224
	ds_read_b128 v[206:209], v145 offset:53248
	ds_read_b128 v[224:227], v145 offset:54272
	ds_read_b128 v[228:231], v145 offset:55296
	ds_read_b128 v[232:235], v145 offset:56320
	global_load_lds_dwordx4 v[240:241], off
	v_lshl_add_u64 v[240:241], v[210:211], 0, s[68:69]
	s_mov_b32 m0, s89
	v_lshl_add_u64 v[182:183], v[182:183], 0, s[54:55]
	global_load_lds_dwordx4 v[240:241], off
	s_mov_b32 m0, s76
	s_nop 0
	global_load_lds_dwordx4 v[182:183], off
	v_lshl_add_u64 v[182:183], v[210:211], 0, s[54:55]
	s_mov_b32 m0, s85
	s_nop 0
	global_load_lds_dwordx4 v[182:183], off
	v_lshl_add_u64 v[182:183], v[236:237], 0, s[68:69]
	s_mov_b32 m0, s50
	s_nop 0
	global_load_lds_dwordx4 v[182:183], off
	v_lshl_add_u64 v[182:183], v[238:239], 0, s[68:69]
	s_mov_b32 m0, s51
	s_nop 0
	global_load_lds_dwordx4 v[182:183], off
	s_waitcnt vmcnt(8)
	s_waitcnt lgkmcnt(0)
	s_barrier
	s_setprio 1
	s_waitcnt lgkmcnt(0)
	v_mfma_f32_16x16x32_bf16 v[60:63], v[146:149], v[178:181], v[60:63]
	v_mfma_f32_16x16x32_bf16 v[56:59], v[154:157], v[178:181], v[56:59]
	v_mfma_f32_16x16x32_bf16 v[40:43], v[154:157], v[198:201], v[40:43]
	v_mfma_f32_16x16x32_bf16 v[48:51], v[146:149], v[198:201], v[48:51]
	v_mfma_f32_16x16x32_bf16 v[32:35], v[146:149], v[206:209], v[32:35]
	v_mfma_f32_16x16x32_bf16 v[24:27], v[154:157], v[206:209], v[24:27]
	v_mfma_f32_16x16x32_bf16 v[8:11], v[154:157], v[228:231], v[8:11]
	v_mfma_f32_16x16x32_bf16 v[16:19], v[146:149], v[228:231], v[16:19]
	v_mfma_f32_16x16x32_bf16 v[60:63], v[150:153], v[194:197], v[60:63]
	v_mfma_f32_16x16x32_bf16 v[56:59], v[158:161], v[194:197], v[56:59]
	v_mfma_f32_16x16x32_bf16 v[40:43], v[158:161], v[202:205], v[40:43]
	v_mfma_f32_16x16x32_bf16 v[48:51], v[150:153], v[202:205], v[48:51]
	v_mfma_f32_16x16x32_bf16 v[32:35], v[150:153], v[224:227], v[32:35]
	v_mfma_f32_16x16x32_bf16 v[24:27], v[158:161], v[224:227], v[24:27]
	v_mfma_f32_16x16x32_bf16 v[8:11], v[158:161], v[232:235], v[8:11]
	v_mfma_f32_16x16x32_bf16 v[16:19], v[150:153], v[232:235], v[16:19]
	s_setprio 0
	s_setprio 1
	v_mfma_f32_16x16x32_bf16 v[52:55], v[162:165], v[178:181], v[52:55]
	v_mfma_f32_16x16x32_bf16 v[44:47], v[170:173], v[178:181], v[44:47]
	v_mfma_f32_16x16x32_bf16 v[28:31], v[170:173], v[198:201], v[28:31]
	v_mfma_f32_16x16x32_bf16 v[36:39], v[162:165], v[198:201], v[36:39]
	v_mfma_f32_16x16x32_bf16 v[20:23], v[162:165], v[206:209], v[20:23]
	v_mfma_f32_16x16x32_bf16 v[12:15], v[170:173], v[206:209], v[12:15]
	v_mfma_f32_16x16x32_bf16 v[0:3], v[170:173], v[228:231], v[0:3]
	v_mfma_f32_16x16x32_bf16 v[4:7], v[162:165], v[228:231], v[4:7]
	v_mfma_f32_16x16x32_bf16 v[52:55], v[166:169], v[194:197], v[52:55]
	v_mfma_f32_16x16x32_bf16 v[44:47], v[174:177], v[194:197], v[44:47]
	v_mfma_f32_16x16x32_bf16 v[28:31], v[174:177], v[202:205], v[28:31]
	v_mfma_f32_16x16x32_bf16 v[36:39], v[166:169], v[202:205], v[36:39]
	v_mfma_f32_16x16x32_bf16 v[20:23], v[166:169], v[224:227], v[20:23]
	v_mfma_f32_16x16x32_bf16 v[12:15], v[174:177], v[224:227], v[12:15]
	v_mfma_f32_16x16x32_bf16 v[0:3], v[174:177], v[232:235], v[0:3]
	v_mfma_f32_16x16x32_bf16 v[4:7], v[166:169], v[232:235], v[4:7]
	s_setprio 0
	s_barrier
	s_movk_i32 s44, 0x100
	s_andn2_b64 vcc, exec, s[36:37]
	s_mov_b64 s[38:39], -1
	s_mov_b64 s[36:37], 0
	s_cbranch_vccz .LBB0_514
	s_and_b64 vcc, exec, s[6:7]
	s_cbranch_vccz .LBB0_517
	s_barrier

.LBB0_531:
	s_add_u32 s39, s18, s38
	s_addc_u32 s42, s19, 0
	s_add_u32 s40, s39, 0x100
	s_addc_u32 s41, s42, 0
	s_and_b64 s[28:29], s[36:37], exec
	s_cselect_b32 s41, s78, s41
	s_cselect_b32 s40, s79, s40
	s_add_u32 s28, s16, s38
	s_addc_u32 s29, s17, 0
	s_add_u32 s38, s28, 0x100
	s_addc_u32 s43, s29, 0
	s_add_i32 s76, 0, 0x10000
	s_and_b64 s[28:29], s[36:37], exec
	s_cselect_b32 s45, s88, s43
	s_cselect_b32 s44, s89, s38
	s_add_i32 s29, 0, 0x14000
	s_add_u32 s50, s39, 0x10080
	s_addc_u32 s51, s42, 0
	s_add_i32 s43, s76, s4
	s_add_i32 m0, s20, 0xc000
	s_add_i32 s85, s20, 0xe000
	s_add_i32 s48, s43, 0x2000
	v_add_u32_e32 v136, s76, v139
	s_add_u32 s46, s44, 0x40000
	ds_read_b128 v[142:145], v136
	ds_read_b128 v[146:149], v136 offset:1024
	ds_read_b128 v[150:153], v136 offset:2048
	ds_read_b128 v[154:157], v136 offset:3072
	v_add_u32_e32 v136, s29, v139
	s_addc_u32 s47, s45, 0
	s_add_i32 s42, s29, s4
	ds_read_b128 v[158:161], v136
	ds_read_b128 v[162:165], v136 offset:1024
	ds_read_b128 v[166:169], v136 offset:2048
	ds_read_b128 v[170:173], v136 offset:3072
	s_add_i32 s49, s42, 0x2000
	s_add_i32 s28, 0, 0x18000
	s_add_i32 s94, 0, 0x1c000
	s_add_u32 s38, s40, 0x10000
	s_addc_u32 s39, s41, 0
	s_add_i32 s93, s28, s4
	s_add_i32 s92, s93, 0x2000
	s_add_u32 s36, s44, 0x40080
	s_addc_u32 s37, s45, 0
	s_add_i32 s76, s94, s4
	s_add_i32 s29, s76, 0x2000
	v_lshl_add_u64 v[136:137], s[50:51], 0, v[134:135]
	ds_read_b128 v[174:177], v140
	ds_read_b128 v[178:181], v140 offset:1024
	ds_read_b128 v[194:197], v140 offset:2048
	ds_read_b128 v[198:201], v140 offset:3072
	ds_read_b128 v[202:205], v140 offset:4096
	ds_read_b128 v[206:209], v140 offset:5120
	ds_read_b128 v[224:227], v140 offset:6144
	ds_read_b128 v[228:231], v140 offset:7168
	global_load_lds_dwordx4 v[136:137], off
	v_lshl_add_u64 v[136:137], s[50:51], 0, v[130:131]
	s_mov_b32 m0, s85
	s_nop 0
	global_load_lds_dwordx4 v[136:137], off
	s_waitcnt vmcnt(8)
	s_waitcnt lgkmcnt(0)
	s_barrier
	s_setprio 1
	s_waitcnt lgkmcnt(0)
	v_mfma_f32_16x16x32_bf16 v[124:127], v[142:145], v[174:177], v[124:127]
	v_mfma_f32_16x16x32_bf16 v[120:123], v[150:153], v[174:177], v[120:123]
	v_mfma_f32_16x16x32_bf16 v[108:111], v[150:153], v[194:197], v[108:111]
	v_mfma_f32_16x16x32_bf16 v[116:119], v[142:145], v[194:197], v[116:119]
	v_mfma_f32_16x16x32_bf16 v[100:103], v[142:145], v[202:205], v[100:103]
	v_mfma_f32_16x16x32_bf16 v[92:95], v[150:153], v[202:205], v[92:95]
	v_mfma_f32_16x16x32_bf16 v[76:79], v[150:153], v[224:227], v[76:79]
	v_mfma_f32_16x16x32_bf16 v[84:87], v[142:145], v[224:227], v[84:87]
	v_mfma_f32_16x16x32_bf16 v[124:127], v[146:149], v[178:181], v[124:127]
	v_mfma_f32_16x16x32_bf16 v[120:123], v[154:157], v[178:181], v[120:123]
	v_mfma_f32_16x16x32_bf16 v[108:111], v[154:157], v[198:201], v[108:111]
	v_mfma_f32_16x16x32_bf16 v[116:119], v[146:149], v[198:201], v[116:119]
	v_mfma_f32_16x16x32_bf16 v[100:103], v[146:149], v[206:209], v[100:103]
	v_mfma_f32_16x16x32_bf16 v[92:95], v[154:157], v[206:209], v[92:95]
	v_mfma_f32_16x16x32_bf16 v[76:79], v[154:157], v[228:231], v[76:79]
	v_mfma_f32_16x16x32_bf16 v[84:87], v[146:149], v[228:231], v[84:87]
	s_setprio 0
	s_setprio 1
	v_mfma_f32_16x16x32_bf16 v[112:115], v[158:161], v[174:177], v[112:115]
	v_mfma_f32_16x16x32_bf16 v[104:107], v[166:169], v[174:177], v[104:107]
	v_mfma_f32_16x16x32_bf16 v[88:91], v[166:169], v[194:197], v[88:91]
	v_mfma_f32_16x16x32_bf16 v[96:99], v[158:161], v[194:197], v[96:99]
	v_mfma_f32_16x16x32_bf16 v[80:83], v[158:161], v[202:205], v[80:83]
	v_mfma_f32_16x16x32_bf16 v[72:75], v[166:169], v[202:205], v[72:75]
	v_mfma_f32_16x16x32_bf16 v[64:67], v[166:169], v[224:227], v[64:67]
	v_mfma_f32_16x16x32_bf16 v[68:71], v[158:161], v[224:227], v[68:71]
	v_mfma_f32_16x16x32_bf16 v[112:115], v[162:165], v[178:181], v[112:115]
	v_mfma_f32_16x16x32_bf16 v[104:107], v[170:173], v[178:181], v[104:107]
	v_mfma_f32_16x16x32_bf16 v[88:91], v[170:173], v[198:201], v[88:91]
	v_mfma_f32_16x16x32_bf16 v[96:99], v[162:165], v[198:201], v[96:99]
	v_mfma_f32_16x16x32_bf16 v[80:83], v[162:165], v[206:209], v[80:83]
	v_mfma_f32_16x16x32_bf16 v[72:75], v[170:173], v[206:209], v[72:75]
	v_mfma_f32_16x16x32_bf16 v[64:67], v[170:173], v[228:231], v[64:67]
	v_mfma_f32_16x16x32_bf16 v[68:71], v[162:165], v[228:231], v[68:71]
	s_setprio 0
	s_barrier
	s_mov_b32 m0, s43
	v_lshl_add_u64 v[136:137], s[44:45], 0, v[132:133]
	ds_read_b128 v[174:177], v140 offset:16384
	ds_read_b128 v[178:181], v140 offset:17408
	ds_read_b128 v[194:197], v140 offset:18432
	ds_read_b128 v[198:201], v140 offset:19456
	ds_read_b128 v[202:205], v140 offset:20480
	ds_read_b128 v[206:209], v140 offset:21504
	ds_read_b128 v[224:227], v140 offset:22528
	ds_read_b128 v[228:231], v140 offset:23552
	global_load_lds_dwordx4 v[136:137], off
	v_lshl_add_u64 v[182:183], s[44:45], 0, v[128:129]
	s_mov_b32 m0, s48
	v_lshl_add_u64 v[210:211], s[46:47], 0, v[132:133]
	global_load_lds_dwordx4 v[182:183], off
	s_mov_b32 m0, s42
	v_lshl_add_u64 v[232:233], s[40:41], 0, v[130:131]
	global_load_lds_dwordx4 v[210:211], off
	v_lshl_add_u64 v[210:211], s[46:47], 0, v[128:129]
	s_mov_b32 m0, s49
	s_nop 0
	global_load_lds_dwordx4 v[210:211], off
	v_lshl_add_u64 v[210:211], s[40:41], 0, v[134:135]
	s_mov_b32 m0, s20
	s_nop 0
	global_load_lds_dwordx4 v[210:211], off
	s_mov_b32 m0, s21
	s_nop 0
	global_load_lds_dwordx4 v[232:233], off
	s_waitcnt vmcnt(8)
	s_waitcnt lgkmcnt(0)
	s_barrier
	s_setprio 1
	s_waitcnt lgkmcnt(0)
	v_mfma_f32_16x16x32_bf16 v[60:63], v[142:145], v[174:177], v[60:63]
	v_mfma_f32_16x16x32_bf16 v[56:59], v[150:153], v[174:177], v[56:59]
	v_mfma_f32_16x16x32_bf16 v[44:47], v[150:153], v[194:197], v[44:47]
	v_mfma_f32_16x16x32_bf16 v[52:55], v[142:145], v[194:197], v[52:55]
	v_mfma_f32_16x16x32_bf16 v[36:39], v[142:145], v[202:205], v[36:39]
	v_mfma_f32_16x16x32_bf16 v[28:31], v[150:153], v[202:205], v[28:31]
	v_mfma_f32_16x16x32_bf16 v[12:15], v[150:153], v[224:227], v[12:15]
	v_mfma_f32_16x16x32_bf16 v[20:23], v[142:145], v[224:227], v[20:23]
	v_mfma_f32_16x16x32_bf16 v[60:63], v[146:149], v[178:181], v[60:63]
	v_mfma_f32_16x16x32_bf16 v[56:59], v[154:157], v[178:181], v[56:59]
	v_mfma_f32_16x16x32_bf16 v[44:47], v[154:157], v[198:201], v[44:47]
	v_mfma_f32_16x16x32_bf16 v[52:55], v[146:149], v[198:201], v[52:55]
	v_mfma_f32_16x16x32_bf16 v[36:39], v[146:149], v[206:209], v[36:39]
	v_mfma_f32_16x16x32_bf16 v[28:31], v[154:157], v[206:209], v[28:31]
	v_mfma_f32_16x16x32_bf16 v[12:15], v[154:157], v[228:231], v[12:15]
	v_mfma_f32_16x16x32_bf16 v[20:23], v[146:149], v[228:231], v[20:23]
	s_setprio 0
	s_setprio 1
	v_mfma_f32_16x16x32_bf16 v[48:51], v[158:161], v[174:177], v[48:51]
	v_mfma_f32_16x16x32_bf16 v[40:43], v[166:169], v[174:177], v[40:43]
	v_mfma_f32_16x16x32_bf16 v[24:27], v[166:169], v[194:197], v[24:27]
	v_mfma_f32_16x16x32_bf16 v[32:35], v[158:161], v[194:197], v[32:35]
	v_mfma_f32_16x16x32_bf16 v[16:19], v[158:161], v[202:205], v[16:19]
	v_mfma_f32_16x16x32_bf16 v[8:11], v[166:169], v[202:205], v[8:11]
	v_mfma_f32_16x16x32_bf16 v[0:3], v[166:169], v[224:227], v[0:3]
	v_mfma_f32_16x16x32_bf16 v[4:7], v[158:161], v[224:227], v[4:7]
	v_mfma_f32_16x16x32_bf16 v[48:51], v[162:165], v[178:181], v[48:51]
	v_mfma_f32_16x16x32_bf16 v[40:43], v[170:173], v[178:181], v[40:43]
	v_mfma_f32_16x16x32_bf16 v[24:27], v[170:173], v[198:201], v[24:27]
	v_mfma_f32_16x16x32_bf16 v[32:35], v[162:165], v[198:201], v[32:35]
	v_mfma_f32_16x16x32_bf16 v[16:19], v[162:165], v[206:209], v[16:19]
	v_mfma_f32_16x16x32_bf16 v[8:11], v[170:173], v[206:209], v[8:11]
	v_mfma_f32_16x16x32_bf16 v[0:3], v[170:173], v[228:231], v[0:3]
	v_mfma_f32_16x16x32_bf16 v[4:7], v[162:165], v[228:231], v[4:7]
	s_setprio 0
	s_barrier
	v_add_u32_e32 v141, s28, v139
	ds_read_b128 v[142:145], v141
	ds_read_b128 v[146:149], v141 offset:1024
	ds_read_b128 v[150:153], v141 offset:2048
	ds_read_b128 v[154:157], v141 offset:3072
	v_add_u32_e32 v141, s94, v139
	ds_read_b128 v[158:161], v141
	ds_read_b128 v[162:165], v141 offset:1024
	ds_read_b128 v[166:169], v141 offset:2048
	ds_read_b128 v[170:173], v141 offset:3072
	s_mov_b32 m0, s26
	v_lshl_add_u64 v[234:235], s[38:39], 0, v[134:135]
	ds_read_b128 v[174:177], v140 offset:32768
	ds_read_b128 v[178:181], v140 offset:33792
	ds_read_b128 v[194:197], v140 offset:34816
	ds_read_b128 v[198:201], v140 offset:35840
	ds_read_b128 v[202:205], v140 offset:36864
	ds_read_b128 v[206:209], v140 offset:37888
	ds_read_b128 v[224:227], v140 offset:38912
	ds_read_b128 v[228:231], v140 offset:39936
	global_load_lds_dwordx4 v[234:235], off
	v_lshl_add_u64 v[234:235], s[38:39], 0, v[130:131]
	s_mov_b32 m0, s27
	s_nop 0
	global_load_lds_dwordx4 v[234:235], off
	s_waitcnt vmcnt(8)
	s_waitcnt lgkmcnt(0)
	s_barrier
	s_setprio 1
	s_waitcnt lgkmcnt(0)
	v_mfma_f32_16x16x32_bf16 v[124:127], v[142:145], v[174:177], v[124:127]
	v_mfma_f32_16x16x32_bf16 v[120:123], v[150:153], v[174:177], v[120:123]
	v_mfma_f32_16x16x32_bf16 v[108:111], v[150:153], v[194:197], v[108:111]
	v_mfma_f32_16x16x32_bf16 v[116:119], v[142:145], v[194:197], v[116:119]
	v_mfma_f32_16x16x32_bf16 v[100:103], v[142:145], v[202:205], v[100:103]
	v_mfma_f32_16x16x32_bf16 v[92:95], v[150:153], v[202:205], v[92:95]
	v_mfma_f32_16x16x32_bf16 v[76:79], v[150:153], v[224:227], v[76:79]
	v_mfma_f32_16x16x32_bf16 v[84:87], v[142:145], v[224:227], v[84:87]
	v_mfma_f32_16x16x32_bf16 v[124:127], v[146:149], v[178:181], v[124:127]
	v_mfma_f32_16x16x32_bf16 v[120:123], v[154:157], v[178:181], v[120:123]
	v_mfma_f32_16x16x32_bf16 v[108:111], v[154:157], v[198:201], v[108:111]
	v_mfma_f32_16x16x32_bf16 v[116:119], v[146:149], v[198:201], v[116:119]
	v_mfma_f32_16x16x32_bf16 v[100:103], v[146:149], v[206:209], v[100:103]
	v_mfma_f32_16x16x32_bf16 v[92:95], v[154:157], v[206:209], v[92:95]
	v_mfma_f32_16x16x32_bf16 v[76:79], v[154:157], v[228:231], v[76:79]
	v_mfma_f32_16x16x32_bf16 v[84:87], v[146:149], v[228:231], v[84:87]
	s_setprio 0
	s_setprio 1
	v_mfma_f32_16x16x32_bf16 v[112:115], v[158:161], v[174:177], v[112:115]
	v_mfma_f32_16x16x32_bf16 v[104:107], v[166:169], v[174:177], v[104:107]
	v_mfma_f32_16x16x32_bf16 v[88:91], v[166:169], v[194:197], v[88:91]
	v_mfma_f32_16x16x32_bf16 v[96:99], v[158:161], v[194:197], v[96:99]
	v_mfma_f32_16x16x32_bf16 v[80:83], v[158:161], v[202:205], v[80:83]
	v_mfma_f32_16x16x32_bf16 v[72:75], v[166:169], v[202:205], v[72:75]
	v_mfma_f32_16x16x32_bf16 v[64:67], v[166:169], v[224:227], v[64:67]
	v_mfma_f32_16x16x32_bf16 v[68:71], v[158:161], v[224:227], v[68:71]
	v_mfma_f32_16x16x32_bf16 v[112:115], v[162:165], v[178:181], v[112:115]
	v_mfma_f32_16x16x32_bf16 v[104:107], v[170:173], v[178:181], v[104:107]
	v_mfma_f32_16x16x32_bf16 v[88:91], v[170:173], v[198:201], v[88:91]
	v_mfma_f32_16x16x32_bf16 v[96:99], v[162:165], v[198:201], v[96:99]
	v_mfma_f32_16x16x32_bf16 v[80:83], v[162:165], v[206:209], v[80:83]
	v_mfma_f32_16x16x32_bf16 v[72:75], v[170:173], v[206:209], v[72:75]
	v_mfma_f32_16x16x32_bf16 v[64:67], v[170:173], v[228:231], v[64:67]
	v_mfma_f32_16x16x32_bf16 v[68:71], v[162:165], v[228:231], v[68:71]
	s_setprio 0
	s_barrier
	s_mov_b32 m0, s93
	v_lshl_add_u64 v[136:137], v[136:137], 0, s[68:69]
	ds_read_b128 v[174:177], v140 offset:49152
	ds_read_b128 v[178:181], v140 offset:50176
	ds_read_b128 v[194:197], v140 offset:51200
	ds_read_b128 v[198:201], v140 offset:52224
	ds_read_b128 v[202:205], v140 offset:53248
	ds_read_b128 v[206:209], v140 offset:54272
	ds_read_b128 v[224:227], v140 offset:55296
	ds_read_b128 v[228:231], v140 offset:56320
	global_load_lds_dwordx4 v[136:137], off
	v_lshl_add_u64 v[136:137], v[182:183], 0, s[68:69]
	s_mov_b32 m0, s92
	s_nop 0
	global_load_lds_dwordx4 v[136:137], off
	v_lshl_add_u64 v[136:137], s[36:37], 0, v[132:133]
	s_mov_b32 m0, s76
	s_nop 0
	global_load_lds_dwordx4 v[136:137], off
	v_lshl_add_u64 v[136:137], s[36:37], 0, v[128:129]
	s_mov_b32 m0, s29
	s_nop 0
	global_load_lds_dwordx4 v[136:137], off
	v_lshl_add_u64 v[136:137], v[210:211], 0, s[68:69]
	s_mov_b32 m0, s52
	s_nop 0
	global_load_lds_dwordx4 v[136:137], off
	v_lshl_add_u64 v[136:137], v[232:233], 0, s[68:69]
	s_mov_b32 m0, s53
	s_nop 0
	global_load_lds_dwordx4 v[136:137], off
	s_waitcnt vmcnt(8)
	s_waitcnt lgkmcnt(0)
	s_barrier
	s_setprio 1
	s_waitcnt lgkmcnt(0)
	v_mfma_f32_16x16x32_bf16 v[60:63], v[142:145], v[174:177], v[60:63]
	v_mfma_f32_16x16x32_bf16 v[56:59], v[150:153], v[174:177], v[56:59]
	v_mfma_f32_16x16x32_bf16 v[44:47], v[150:153], v[194:197], v[44:47]
	v_mfma_f32_16x16x32_bf16 v[52:55], v[142:145], v[194:197], v[52:55]
	v_mfma_f32_16x16x32_bf16 v[36:39], v[142:145], v[202:205], v[36:39]
	v_mfma_f32_16x16x32_bf16 v[28:31], v[150:153], v[202:205], v[28:31]
	v_mfma_f32_16x16x32_bf16 v[12:15], v[150:153], v[224:227], v[12:15]
	v_mfma_f32_16x16x32_bf16 v[20:23], v[142:145], v[224:227], v[20:23]
	v_mfma_f32_16x16x32_bf16 v[60:63], v[146:149], v[178:181], v[60:63]
	v_mfma_f32_16x16x32_bf16 v[56:59], v[154:157], v[178:181], v[56:59]
	v_mfma_f32_16x16x32_bf16 v[44:47], v[154:157], v[198:201], v[44:47]
	v_mfma_f32_16x16x32_bf16 v[52:55], v[146:149], v[198:201], v[52:55]
	v_mfma_f32_16x16x32_bf16 v[36:39], v[146:149], v[206:209], v[36:39]
	v_mfma_f32_16x16x32_bf16 v[28:31], v[154:157], v[206:209], v[28:31]
	v_mfma_f32_16x16x32_bf16 v[12:15], v[154:157], v[228:231], v[12:15]
	v_mfma_f32_16x16x32_bf16 v[20:23], v[146:149], v[228:231], v[20:23]
	s_setprio 0
	s_setprio 1
	v_mfma_f32_16x16x32_bf16 v[48:51], v[158:161], v[174:177], v[48:51]
	v_mfma_f32_16x16x32_bf16 v[40:43], v[166:169], v[174:177], v[40:43]
	v_mfma_f32_16x16x32_bf16 v[24:27], v[166:169], v[194:197], v[24:27]
	v_mfma_f32_16x16x32_bf16 v[32:35], v[158:161], v[194:197], v[32:35]
	v_mfma_f32_16x16x32_bf16 v[16:19], v[158:161], v[202:205], v[16:19]
	v_mfma_f32_16x16x32_bf16 v[8:11], v[166:169], v[202:205], v[8:11]
	v_mfma_f32_16x16x32_bf16 v[0:3], v[166:169], v[224:227], v[0:3]
	v_mfma_f32_16x16x32_bf16 v[4:7], v[158:161], v[224:227], v[4:7]
	v_mfma_f32_16x16x32_bf16 v[48:51], v[162:165], v[178:181], v[48:51]
	v_mfma_f32_16x16x32_bf16 v[40:43], v[170:173], v[178:181], v[40:43]
	v_mfma_f32_16x16x32_bf16 v[24:27], v[170:173], v[198:201], v[24:27]
	v_mfma_f32_16x16x32_bf16 v[32:35], v[162:165], v[198:201], v[32:35]
	v_mfma_f32_16x16x32_bf16 v[16:19], v[162:165], v[206:209], v[16:19]
	v_mfma_f32_16x16x32_bf16 v[8:11], v[170:173], v[206:209], v[8:11]
	v_mfma_f32_16x16x32_bf16 v[0:3], v[170:173], v[228:231], v[0:3]
	v_mfma_f32_16x16x32_bf16 v[4:7], v[162:165], v[228:231], v[4:7]
	s_setprio 0
	s_barrier
	s_movk_i32 s38, 0x100
	s_andn2_b64 vcc, exec, s[30:31]
	s_mov_b64 s[36:37], -1
	s_mov_b64 s[30:31], 0
	s_cbranch_vccz .LBB0_531
	s_and_b64 vcc, exec, s[6:7]
	s_cbranch_vccz .LBB0_534
	s_barrier

.LBB0_599:
	s_add_i32 s37, s36, 0x100
	s_and_b64 s[28:29], s[30:31], exec
	s_cselect_b32 s29, 0, s37
	s_cselect_b32 s28, 0, 0
	s_add_u32 s38, s34, s29
	s_addc_u32 s39, s35, s28
	s_add_u32 s28, s16, s36
	s_addc_u32 s29, s17, 0
	s_add_u32 s37, s28, 0x100
	s_addc_u32 s40, s29, 0
	s_add_i32 s43, 0, 0x10000
	s_and_b64 s[28:29], s[30:31], exec
	s_cselect_b32 s41, s9, s40
	s_cselect_b32 s40, s58, s37
	s_add_i32 s29, 0, 0x14000
	s_add_u32 s46, s56, s36
	s_addc_u32 s47, s57, 0
	s_add_i32 s42, s43, s4
	s_add_i32 m0, s20, 0xc000
	s_add_i32 s63, s20, 0xe000
	s_add_i32 s48, s42, 0x2000
	s_add_u32 s44, s40, 0x10000
	v_add_u32_e32 v156, s43, v145
	v_add_u32_e32 v172, s29, v145
	s_addc_u32 s45, s41, 0
	s_add_i32 s62, s29, s4
	ds_read_b128 v[136:139], v156
	ds_read_b128 v[140:143], v156 offset:1024
	ds_read_b128 v[152:155], v156 offset:2048
	ds_read_b128 v[156:159], v156 offset:3072
	ds_read_b128 v[160:163], v172
	ds_read_b128 v[164:167], v172 offset:1024
	ds_read_b128 v[168:171], v172 offset:2048
	ds_read_b128 v[172:175], v172 offset:3072
	s_add_i32 s49, s62, 0x2000
	s_add_i32 s28, 0, 0x18000
	s_add_i32 s61, 0, 0x1c000
	s_add_u32 s36, s38, 0x10000
	s_addc_u32 s37, s39, 0
	s_add_i32 s60, s28, s4
	s_add_i32 s59, s60, 0x2000
	s_add_u32 s30, s40, 0x10080
	s_addc_u32 s31, s41, 0
	s_add_i32 s43, s61, s4
	s_add_i32 s29, s43, 0x2000
	v_lshl_add_u64 v[210:211], s[46:47], 0, v[132:133]
	v_lshl_add_u64 v[210:211], v[210:211], 0, s[68:69]
	ds_read_b128 v[176:179], v151
	ds_read_b128 v[180:183], v151 offset:1024
	ds_read_b128 v[194:197], v151 offset:2048
	ds_read_b128 v[198:201], v151 offset:3072
	ds_read_b128 v[202:205], v151 offset:4096
	ds_read_b128 v[206:209], v151 offset:5120
	ds_read_b128 v[224:227], v151 offset:6144
	ds_read_b128 v[228:231], v151 offset:7168
	global_load_lds_dwordx4 v[210:211], off
	v_lshl_add_u64 v[210:211], s[46:47], 0, v[130:131]
	v_lshl_add_u64 v[210:211], v[210:211], 0, s[68:69]
	s_mov_b32 m0, s63
	s_nop 0
	global_load_lds_dwordx4 v[210:211], off
	s_waitcnt vmcnt(8)
	s_waitcnt lgkmcnt(0)
	s_barrier
	s_setprio 1
	s_waitcnt lgkmcnt(0)
	v_mfma_f32_16x16x32_bf16 v[124:127], v[136:139], v[176:179], v[124:127]
	v_mfma_f32_16x16x32_bf16 v[116:119], v[152:155], v[176:179], v[116:119]
	v_mfma_f32_16x16x32_bf16 v[84:87], v[152:155], v[194:197], v[84:87]
	v_mfma_f32_16x16x32_bf16 v[92:95], v[136:139], v[194:197], v[92:95]
	v_mfma_f32_16x16x32_bf16 v[60:63], v[136:139], v[202:205], v[60:63]
	v_mfma_f32_16x16x32_bf16 v[52:55], v[152:155], v[202:205], v[52:55]
	v_mfma_f32_16x16x32_bf16 v[20:23], v[152:155], v[224:227], v[20:23]
	v_mfma_f32_16x16x32_bf16 v[28:31], v[136:139], v[224:227], v[28:31]
	v_mfma_f32_16x16x32_bf16 v[124:127], v[140:143], v[180:183], v[124:127]
	v_mfma_f32_16x16x32_bf16 v[116:119], v[156:159], v[180:183], v[116:119]
	v_mfma_f32_16x16x32_bf16 v[84:87], v[156:159], v[198:201], v[84:87]
	v_mfma_f32_16x16x32_bf16 v[92:95], v[140:143], v[198:201], v[92:95]
	v_mfma_f32_16x16x32_bf16 v[60:63], v[140:143], v[206:209], v[60:63]
	v_mfma_f32_16x16x32_bf16 v[52:55], v[156:159], v[206:209], v[52:55]
	v_mfma_f32_16x16x32_bf16 v[20:23], v[156:159], v[228:231], v[20:23]
	v_mfma_f32_16x16x32_bf16 v[28:31], v[140:143], v[228:231], v[28:31]
	s_setprio 0
	s_setprio 1
	v_mfma_f32_16x16x32_bf16 v[108:111], v[160:163], v[176:179], v[108:111]
	v_mfma_f32_16x16x32_bf16 v[104:107], v[168:171], v[176:179], v[104:107]
	v_mfma_f32_16x16x32_bf16 v[72:75], v[168:171], v[194:197], v[72:75]
	v_mfma_f32_16x16x32_bf16 v[76:79], v[160:163], v[194:197], v[76:79]
	v_mfma_f32_16x16x32_bf16 v[44:47], v[160:163], v[202:205], v[44:47]
	v_mfma_f32_16x16x32_bf16 v[40:43], v[168:171], v[202:205], v[40:43]
	v_mfma_f32_16x16x32_bf16 v[8:11], v[168:171], v[224:227], v[8:11]
	v_mfma_f32_16x16x32_bf16 v[12:15], v[160:163], v[224:227], v[12:15]
	v_mfma_f32_16x16x32_bf16 v[108:111], v[164:167], v[180:183], v[108:111]
	v_mfma_f32_16x16x32_bf16 v[104:107], v[172:175], v[180:183], v[104:107]
	v_mfma_f32_16x16x32_bf16 v[72:75], v[172:175], v[198:201], v[72:75]
	v_mfma_f32_16x16x32_bf16 v[76:79], v[164:167], v[198:201], v[76:79]
	v_mfma_f32_16x16x32_bf16 v[44:47], v[164:167], v[206:209], v[44:47]
	v_mfma_f32_16x16x32_bf16 v[40:43], v[172:175], v[206:209], v[40:43]
	v_mfma_f32_16x16x32_bf16 v[8:11], v[172:175], v[228:231], v[8:11]
	v_mfma_f32_16x16x32_bf16 v[12:15], v[164:167], v[228:231], v[12:15]
	s_setprio 0
	s_barrier
	s_mov_b32 m0, s42
	v_lshl_add_u64 v[210:211], s[40:41], 0, v[184:185]
	ds_read_b128 v[176:179], v151 offset:16384
	ds_read_b128 v[180:183], v151 offset:17408
	ds_read_b128 v[194:197], v151 offset:18432
	ds_read_b128 v[198:201], v151 offset:19456
	ds_read_b128 v[202:205], v151 offset:20480
	ds_read_b128 v[206:209], v151 offset:21504
	ds_read_b128 v[224:227], v151 offset:22528
	ds_read_b128 v[228:231], v151 offset:23552
	global_load_lds_dwordx4 v[210:211], off
	v_lshl_add_u64 v[232:233], s[40:41], 0, v[128:129]
	s_mov_b32 m0, s48
	v_lshl_add_u64 v[234:235], s[44:45], 0, v[184:185]
	global_load_lds_dwordx4 v[232:233], off
	s_mov_b32 m0, s62
	v_lshl_add_u64 v[236:237], s[38:39], 0, v[130:131]
	global_load_lds_dwordx4 v[234:235], off
	v_lshl_add_u64 v[234:235], s[44:45], 0, v[128:129]
	s_mov_b32 m0, s49
	s_nop 0
	global_load_lds_dwordx4 v[234:235], off
	v_lshl_add_u64 v[234:235], s[38:39], 0, v[132:133]
	s_mov_b32 m0, s20
	s_nop 0
	global_load_lds_dwordx4 v[234:235], off
	s_mov_b32 m0, s21
	s_nop 0
	global_load_lds_dwordx4 v[236:237], off
	s_waitcnt vmcnt(8)
	s_waitcnt lgkmcnt(0)
	s_barrier
	s_setprio 1
	s_waitcnt lgkmcnt(0)
	v_mfma_f32_16x16x32_bf16 v[120:123], v[136:139], v[176:179], v[120:123]
	v_mfma_f32_16x16x32_bf16 v[112:115], v[152:155], v[176:179], v[112:115]
	v_mfma_f32_16x16x32_bf16 v[80:83], v[152:155], v[194:197], v[80:83]
	v_mfma_f32_16x16x32_bf16 v[88:91], v[136:139], v[194:197], v[88:91]
	v_mfma_f32_16x16x32_bf16 v[56:59], v[136:139], v[202:205], v[56:59]
	v_mfma_f32_16x16x32_bf16 v[48:51], v[152:155], v[202:205], v[48:51]
	v_mfma_f32_16x16x32_bf16 v[16:19], v[152:155], v[224:227], v[16:19]
	v_mfma_f32_16x16x32_bf16 v[24:27], v[136:139], v[224:227], v[24:27]
	v_mfma_f32_16x16x32_bf16 v[120:123], v[140:143], v[180:183], v[120:123]
	v_mfma_f32_16x16x32_bf16 v[112:115], v[156:159], v[180:183], v[112:115]
	v_mfma_f32_16x16x32_bf16 v[80:83], v[156:159], v[198:201], v[80:83]
	v_mfma_f32_16x16x32_bf16 v[88:91], v[140:143], v[198:201], v[88:91]
	v_mfma_f32_16x16x32_bf16 v[56:59], v[140:143], v[206:209], v[56:59]
	v_mfma_f32_16x16x32_bf16 v[48:51], v[156:159], v[206:209], v[48:51]
	v_mfma_f32_16x16x32_bf16 v[16:19], v[156:159], v[228:231], v[16:19]
	v_mfma_f32_16x16x32_bf16 v[24:27], v[140:143], v[228:231], v[24:27]
	s_setprio 0
	s_setprio 1
	v_mfma_f32_16x16x32_bf16 v[100:103], v[160:163], v[176:179], v[100:103]
	v_mfma_f32_16x16x32_bf16 v[96:99], v[168:171], v[176:179], v[96:99]
	v_mfma_f32_16x16x32_bf16 v[64:67], v[168:171], v[194:197], v[64:67]
	v_mfma_f32_16x16x32_bf16 v[68:71], v[160:163], v[194:197], v[68:71]
	v_mfma_f32_16x16x32_bf16 v[36:39], v[160:163], v[202:205], v[36:39]
	v_mfma_f32_16x16x32_bf16 v[32:35], v[168:171], v[202:205], v[32:35]
	v_mfma_f32_16x16x32_bf16 v[0:3], v[168:171], v[224:227], v[0:3]
	v_mfma_f32_16x16x32_bf16 v[4:7], v[160:163], v[224:227], v[4:7]
	v_mfma_f32_16x16x32_bf16 v[100:103], v[164:167], v[180:183], v[100:103]
	v_mfma_f32_16x16x32_bf16 v[96:99], v[172:175], v[180:183], v[96:99]
	v_mfma_f32_16x16x32_bf16 v[64:67], v[172:175], v[198:201], v[64:67]
	v_mfma_f32_16x16x32_bf16 v[68:71], v[164:167], v[198:201], v[68:71]
	v_mfma_f32_16x16x32_bf16 v[36:39], v[164:167], v[206:209], v[36:39]
	v_mfma_f32_16x16x32_bf16 v[32:35], v[172:175], v[206:209], v[32:35]
	v_mfma_f32_16x16x32_bf16 v[0:3], v[172:175], v[228:231], v[0:3]
	v_mfma_f32_16x16x32_bf16 v[4:7], v[164:167], v[228:231], v[4:7]
	s_setprio 0
	s_barrier
	v_add_u32_e32 v156, s28, v145
	v_add_u32_e32 v172, s61, v145
	ds_read_b128 v[136:139], v156
	ds_read_b128 v[140:143], v156 offset:1024
	ds_read_b128 v[152:155], v156 offset:2048
	ds_read_b128 v[156:159], v156 offset:3072
	ds_read_b128 v[160:163], v172
	ds_read_b128 v[164:167], v172 offset:1024
	ds_read_b128 v[168:171], v172 offset:2048
	ds_read_b128 v[172:175], v172 offset:3072
	s_mov_b32 m0, s26
	v_lshl_add_u64 v[238:239], s[36:37], 0, v[132:133]
	ds_read_b128 v[176:179], v151 offset:32768
	ds_read_b128 v[180:183], v151 offset:33792
	ds_read_b128 v[194:197], v151 offset:34816
	ds_read_b128 v[198:201], v151 offset:35840
	ds_read_b128 v[202:205], v151 offset:36864
	ds_read_b128 v[206:209], v151 offset:37888
	ds_read_b128 v[224:227], v151 offset:38912
	ds_read_b128 v[228:231], v151 offset:39936
	global_load_lds_dwordx4 v[238:239], off
	v_lshl_add_u64 v[238:239], s[36:37], 0, v[130:131]
	s_mov_b32 m0, s27
	s_nop 0
	global_load_lds_dwordx4 v[238:239], off
	s_waitcnt vmcnt(8)
	s_waitcnt lgkmcnt(0)
	s_barrier
	s_setprio 1
	s_waitcnt lgkmcnt(0)
	v_mfma_f32_16x16x32_bf16 v[124:127], v[136:139], v[176:179], v[124:127]
	v_mfma_f32_16x16x32_bf16 v[116:119], v[152:155], v[176:179], v[116:119]
	v_mfma_f32_16x16x32_bf16 v[84:87], v[152:155], v[194:197], v[84:87]
	v_mfma_f32_16x16x32_bf16 v[92:95], v[136:139], v[194:197], v[92:95]
	v_mfma_f32_16x16x32_bf16 v[60:63], v[136:139], v[202:205], v[60:63]
	v_mfma_f32_16x16x32_bf16 v[52:55], v[152:155], v[202:205], v[52:55]
	v_mfma_f32_16x16x32_bf16 v[20:23], v[152:155], v[224:227], v[20:23]
	v_mfma_f32_16x16x32_bf16 v[28:31], v[136:139], v[224:227], v[28:31]
	v_mfma_f32_16x16x32_bf16 v[124:127], v[140:143], v[180:183], v[124:127]
	v_mfma_f32_16x16x32_bf16 v[116:119], v[156:159], v[180:183], v[116:119]
	v_mfma_f32_16x16x32_bf16 v[84:87], v[156:159], v[198:201], v[84:87]
	v_mfma_f32_16x16x32_bf16 v[92:95], v[140:143], v[198:201], v[92:95]
	v_mfma_f32_16x16x32_bf16 v[60:63], v[140:143], v[206:209], v[60:63]
	v_mfma_f32_16x16x32_bf16 v[52:55], v[156:159], v[206:209], v[52:55]
	v_mfma_f32_16x16x32_bf16 v[20:23], v[156:159], v[228:231], v[20:23]
	v_mfma_f32_16x16x32_bf16 v[28:31], v[140:143], v[228:231], v[28:31]
	s_setprio 0
	s_setprio 1
	v_mfma_f32_16x16x32_bf16 v[108:111], v[160:163], v[176:179], v[108:111]
	v_mfma_f32_16x16x32_bf16 v[104:107], v[168:171], v[176:179], v[104:107]
	v_mfma_f32_16x16x32_bf16 v[72:75], v[168:171], v[194:197], v[72:75]
	v_mfma_f32_16x16x32_bf16 v[76:79], v[160:163], v[194:197], v[76:79]
	v_mfma_f32_16x16x32_bf16 v[44:47], v[160:163], v[202:205], v[44:47]
	v_mfma_f32_16x16x32_bf16 v[40:43], v[168:171], v[202:205], v[40:43]
	v_mfma_f32_16x16x32_bf16 v[8:11], v[168:171], v[224:227], v[8:11]
	v_mfma_f32_16x16x32_bf16 v[12:15], v[160:163], v[224:227], v[12:15]
	v_mfma_f32_16x16x32_bf16 v[108:111], v[164:167], v[180:183], v[108:111]
	v_mfma_f32_16x16x32_bf16 v[104:107], v[172:175], v[180:183], v[104:107]
	v_mfma_f32_16x16x32_bf16 v[72:75], v[172:175], v[198:201], v[72:75]
	v_mfma_f32_16x16x32_bf16 v[76:79], v[164:167], v[198:201], v[76:79]
	v_mfma_f32_16x16x32_bf16 v[44:47], v[164:167], v[206:209], v[44:47]
	v_mfma_f32_16x16x32_bf16 v[40:43], v[172:175], v[206:209], v[40:43]
	v_mfma_f32_16x16x32_bf16 v[8:11], v[172:175], v[228:231], v[8:11]
	v_mfma_f32_16x16x32_bf16 v[12:15], v[164:167], v[228:231], v[12:15]
	s_setprio 0
	s_barrier
	s_mov_b32 m0, s60
	v_lshl_add_u64 v[210:211], v[210:211], 0, s[68:69]
	ds_read_b128 v[176:179], v151 offset:49152
	ds_read_b128 v[180:183], v151 offset:50176
	ds_read_b128 v[194:197], v151 offset:51200
	ds_read_b128 v[198:201], v151 offset:52224
	ds_read_b128 v[202:205], v151 offset:53248
	ds_read_b128 v[206:209], v151 offset:54272
	ds_read_b128 v[224:227], v151 offset:55296
	ds_read_b128 v[228:231], v151 offset:56320
	global_load_lds_dwordx4 v[210:211], off
	v_lshl_add_u64 v[210:211], v[232:233], 0, s[68:69]
	s_mov_b32 m0, s59
	s_nop 0
	global_load_lds_dwordx4 v[210:211], off
	v_lshl_add_u64 v[210:211], s[30:31], 0, v[184:185]
	s_mov_b32 m0, s43
	s_nop 0
	global_load_lds_dwordx4 v[210:211], off
	v_lshl_add_u64 v[210:211], s[30:31], 0, v[128:129]
	s_mov_b32 m0, s29
	s_nop 0
	global_load_lds_dwordx4 v[210:211], off
	v_lshl_add_u64 v[210:211], v[234:235], 0, s[68:69]
	s_mov_b32 m0, s50
	s_nop 0
	global_load_lds_dwordx4 v[210:211], off
	v_lshl_add_u64 v[210:211], v[236:237], 0, s[68:69]
	s_mov_b32 m0, s51
	s_nop 0
	global_load_lds_dwordx4 v[210:211], off
	s_waitcnt vmcnt(8)
	s_waitcnt lgkmcnt(0)
	s_barrier
	s_setprio 1
	s_waitcnt lgkmcnt(0)
	v_mfma_f32_16x16x32_bf16 v[120:123], v[136:139], v[176:179], v[120:123]
	v_mfma_f32_16x16x32_bf16 v[112:115], v[152:155], v[176:179], v[112:115]
	v_mfma_f32_16x16x32_bf16 v[80:83], v[152:155], v[194:197], v[80:83]
	v_mfma_f32_16x16x32_bf16 v[88:91], v[136:139], v[194:197], v[88:91]
	v_mfma_f32_16x16x32_bf16 v[56:59], v[136:139], v[202:205], v[56:59]
	v_mfma_f32_16x16x32_bf16 v[48:51], v[152:155], v[202:205], v[48:51]
	v_mfma_f32_16x16x32_bf16 v[16:19], v[152:155], v[224:227], v[16:19]
	v_mfma_f32_16x16x32_bf16 v[24:27], v[136:139], v[224:227], v[24:27]
	v_mfma_f32_16x16x32_bf16 v[120:123], v[140:143], v[180:183], v[120:123]
	v_mfma_f32_16x16x32_bf16 v[112:115], v[156:159], v[180:183], v[112:115]
	v_mfma_f32_16x16x32_bf16 v[80:83], v[156:159], v[198:201], v[80:83]
	v_mfma_f32_16x16x32_bf16 v[88:91], v[140:143], v[198:201], v[88:91]
	v_mfma_f32_16x16x32_bf16 v[56:59], v[140:143], v[206:209], v[56:59]
	v_mfma_f32_16x16x32_bf16 v[48:51], v[156:159], v[206:209], v[48:51]
	v_mfma_f32_16x16x32_bf16 v[16:19], v[156:159], v[228:231], v[16:19]
	v_mfma_f32_16x16x32_bf16 v[24:27], v[140:143], v[228:231], v[24:27]
	s_setprio 0
	s_setprio 1
	v_mfma_f32_16x16x32_bf16 v[100:103], v[160:163], v[176:179], v[100:103]
	v_mfma_f32_16x16x32_bf16 v[96:99], v[168:171], v[176:179], v[96:99]
	v_mfma_f32_16x16x32_bf16 v[64:67], v[168:171], v[194:197], v[64:67]
	v_mfma_f32_16x16x32_bf16 v[68:71], v[160:163], v[194:197], v[68:71]
	v_mfma_f32_16x16x32_bf16 v[36:39], v[160:163], v[202:205], v[36:39]
	v_mfma_f32_16x16x32_bf16 v[32:35], v[168:171], v[202:205], v[32:35]
	v_mfma_f32_16x16x32_bf16 v[0:3], v[168:171], v[224:227], v[0:3]
	v_mfma_f32_16x16x32_bf16 v[4:7], v[160:163], v[224:227], v[4:7]
	v_mfma_f32_16x16x32_bf16 v[100:103], v[164:167], v[180:183], v[100:103]
	v_mfma_f32_16x16x32_bf16 v[96:99], v[172:175], v[180:183], v[96:99]
	v_mfma_f32_16x16x32_bf16 v[64:67], v[172:175], v[198:201], v[64:67]
	v_mfma_f32_16x16x32_bf16 v[68:71], v[164:167], v[198:201], v[68:71]
	v_mfma_f32_16x16x32_bf16 v[36:39], v[164:167], v[206:209], v[36:39]
	v_mfma_f32_16x16x32_bf16 v[32:35], v[172:175], v[206:209], v[32:35]
	v_mfma_f32_16x16x32_bf16 v[0:3], v[172:175], v[228:231], v[0:3]
	v_mfma_f32_16x16x32_bf16 v[4:7], v[164:167], v[228:231], v[4:7]
	s_setprio 0
	s_barrier
	s_andn2_b64 vcc, exec, s[18:19]
	s_mov_b64 s[30:31], -1
	s_mov_b64 s[18:19], 0
	s_movk_i32 s36, 0x100
	s_cbranch_vccz .LBB0_599
	s_and_b64 vcc, exec, s[6:7]
	s_cbranch_vccz .LBB0_602
	s_barrier

.LBB0_667:
	s_add_i32 s29, s28, 0x100
	s_and_b64 s[36:37], s[30:31], exec
	s_cselect_b32 s29, 0, s29
	s_cselect_b32 s36, 0, 0
	s_add_u32 s38, s34, s29
	s_addc_u32 s39, s35, s36
	s_add_u32 s29, s16, s28
	s_addc_u32 s36, s17, 0
	s_add_u32 s29, s29, 0x100
	s_addc_u32 s36, s36, 0
	s_add_i32 s42, 0, 0x10000
	s_and_b64 s[30:31], s[30:31], exec
	s_cselect_b32 s41, s9, s36
	s_cselect_b32 s40, s58, s29
	s_add_i32 s29, 0, 0x14000
	s_add_u32 s46, s56, s28
	s_addc_u32 s47, s57, 0
	s_add_i32 s49, s42, s4
	s_add_i32 m0, s20, 0xc000
	s_add_i32 s43, s20, 0xe000
	s_add_i32 s59, s49, 0x2000
	v_add_u32_e32 v75, s42, v72
	s_add_u32 s44, s40, 0x10000
	ds_read_b128 v[76:79], v75
	ds_read_b128 v[80:83], v75 offset:1024
	ds_read_b128 v[84:87], v75 offset:2048
	ds_read_b128 v[88:91], v75 offset:3072
	v_add_u32_e32 v75, s29, v72
	s_addc_u32 s45, s41, 0
	s_add_i32 s60, s29, s4
	ds_read_b128 v[92:95], v75
	ds_read_b128 v[96:99], v75 offset:1024
	ds_read_b128 v[100:103], v75 offset:2048
	ds_read_b128 v[104:107], v75 offset:3072
	s_add_i32 s61, s60, 0x2000
	s_add_i32 s62, 0, 0x18000
	s_add_i32 s63, 0, 0x1c000
	s_add_u32 s36, s38, 0x10000
	s_addc_u32 s37, s39, 0
	s_add_i32 s48, s62, s4
	s_add_i32 s28, s48, 0x2000
	s_add_u32 s30, s40, 0x10080
	s_addc_u32 s31, s41, 0
	s_add_i32 s29, s63, s4
	s_add_i32 s42, s29, 0x2000
	v_lshl_add_u64 v[140:141], s[46:47], 0, v[70:71]
	v_lshl_add_u64 v[140:141], v[140:141], 0, s[68:69]
	ds_read_b128 v[108:111], v74
	ds_read_b128 v[112:115], v74 offset:1024
	ds_read_b128 v[116:119], v74 offset:2048
	ds_read_b128 v[120:123], v74 offset:3072
	ds_read_b128 v[124:127], v74 offset:4096
	ds_read_b128 v[128:131], v74 offset:5120
	ds_read_b128 v[132:135], v74 offset:6144
	ds_read_b128 v[136:139], v74 offset:7168
	global_load_lds_dwordx4 v[140:141], off
	v_lshl_add_u64 v[140:141], s[46:47], 0, v[66:67]
	v_lshl_add_u64 v[140:141], v[140:141], 0, s[68:69]
	s_mov_b32 m0, s43
	s_nop 0
	global_load_lds_dwordx4 v[140:141], off
	s_waitcnt vmcnt(8)
	s_waitcnt lgkmcnt(0)
	s_barrier
	s_setprio 1
	s_waitcnt lgkmcnt(0)
	v_mfma_f32_16x16x32_bf16 v[60:63], v[76:79], v[108:111], v[60:63]
	v_mfma_f32_16x16x32_bf16 v[56:59], v[84:87], v[108:111], v[56:59]
	v_mfma_f32_16x16x32_bf16 v[44:47], v[84:87], v[116:119], v[44:47]
	v_mfma_f32_16x16x32_bf16 v[52:55], v[76:79], v[116:119], v[52:55]
	v_mfma_f32_16x16x32_bf16 v[36:39], v[76:79], v[124:127], v[36:39]
	v_mfma_f32_16x16x32_bf16 v[28:31], v[84:87], v[124:127], v[28:31]
	v_mfma_f32_16x16x32_bf16 v[12:15], v[84:87], v[132:135], v[12:15]
	v_mfma_f32_16x16x32_bf16 v[20:23], v[76:79], v[132:135], v[20:23]
	v_mfma_f32_16x16x32_bf16 v[60:63], v[80:83], v[112:115], v[60:63]
	v_mfma_f32_16x16x32_bf16 v[56:59], v[88:91], v[112:115], v[56:59]
	v_mfma_f32_16x16x32_bf16 v[44:47], v[88:91], v[120:123], v[44:47]
	v_mfma_f32_16x16x32_bf16 v[52:55], v[80:83], v[120:123], v[52:55]
	v_mfma_f32_16x16x32_bf16 v[36:39], v[80:83], v[128:131], v[36:39]
	v_mfma_f32_16x16x32_bf16 v[28:31], v[88:91], v[128:131], v[28:31]
	v_mfma_f32_16x16x32_bf16 v[12:15], v[88:91], v[136:139], v[12:15]
	v_mfma_f32_16x16x32_bf16 v[20:23], v[80:83], v[136:139], v[20:23]
	s_setprio 0
	s_setprio 1
	v_mfma_f32_16x16x32_bf16 v[48:51], v[92:95], v[108:111], v[48:51]
	v_mfma_f32_16x16x32_bf16 v[40:43], v[100:103], v[108:111], v[40:43]
	v_mfma_f32_16x16x32_bf16 v[24:27], v[100:103], v[116:119], v[24:27]
	v_mfma_f32_16x16x32_bf16 v[32:35], v[92:95], v[116:119], v[32:35]
	v_mfma_f32_16x16x32_bf16 v[16:19], v[92:95], v[124:127], v[16:19]
	v_mfma_f32_16x16x32_bf16 v[8:11], v[100:103], v[124:127], v[8:11]
	v_mfma_f32_16x16x32_bf16 v[0:3], v[100:103], v[132:135], v[0:3]
	v_mfma_f32_16x16x32_bf16 v[4:7], v[92:95], v[132:135], v[4:7]
	v_mfma_f32_16x16x32_bf16 v[48:51], v[96:99], v[112:115], v[48:51]
	v_mfma_f32_16x16x32_bf16 v[40:43], v[104:107], v[112:115], v[40:43]
	v_mfma_f32_16x16x32_bf16 v[24:27], v[104:107], v[120:123], v[24:27]
	v_mfma_f32_16x16x32_bf16 v[32:35], v[96:99], v[120:123], v[32:35]
	v_mfma_f32_16x16x32_bf16 v[16:19], v[96:99], v[128:131], v[16:19]
	v_mfma_f32_16x16x32_bf16 v[8:11], v[104:107], v[128:131], v[8:11]
	v_mfma_f32_16x16x32_bf16 v[0:3], v[104:107], v[136:139], v[0:3]
	v_mfma_f32_16x16x32_bf16 v[4:7], v[96:99], v[136:139], v[4:7]
	s_setprio 0
	s_barrier
	s_mov_b32 m0, s49
	v_lshl_add_u64 v[140:141], s[40:41], 0, v[68:69]
	global_load_lds_dwordx4 v[140:141], off
	v_lshl_add_u64 v[142:143], s[40:41], 0, v[64:65]
	s_mov_b32 m0, s59
	v_lshl_add_u64 v[76:77], s[44:45], 0, v[68:69]
	global_load_lds_dwordx4 v[142:143], off
	s_mov_b32 m0, s60
	v_lshl_add_u64 v[144:145], s[38:39], 0, v[70:71]
	global_load_lds_dwordx4 v[76:77], off
	v_lshl_add_u64 v[76:77], s[44:45], 0, v[64:65]
	s_mov_b32 m0, s61
	v_lshl_add_u64 v[146:147], s[38:39], 0, v[66:67]
	global_load_lds_dwordx4 v[76:77], off
	s_mov_b32 m0, s20
	s_nop 0
	global_load_lds_dwordx4 v[144:145], off
	s_mov_b32 m0, s21
	s_nop 0
	global_load_lds_dwordx4 v[146:147], off
	s_waitcnt vmcnt(8)
	s_waitcnt lgkmcnt(0)
	s_barrier
	s_setprio 1
	s_setprio 0
	s_setprio 1
	s_setprio 0
	s_barrier
	v_add_u32_e32 v75, s62, v72
	ds_read_b128 v[76:79], v75
	ds_read_b128 v[80:83], v75 offset:1024
	ds_read_b128 v[84:87], v75 offset:2048
	ds_read_b128 v[88:91], v75 offset:3072
	v_add_u32_e32 v75, s63, v72
	ds_read_b128 v[92:95], v75
	ds_read_b128 v[96:99], v75 offset:1024
	ds_read_b128 v[100:103], v75 offset:2048
	ds_read_b128 v[104:107], v75 offset:3072
	s_mov_b32 m0, s26
	v_lshl_add_u64 v[148:149], s[36:37], 0, v[70:71]
	ds_read_b128 v[108:111], v74 offset:32768
	ds_read_b128 v[112:115], v74 offset:33792
	ds_read_b128 v[116:119], v74 offset:34816
	ds_read_b128 v[120:123], v74 offset:35840
	ds_read_b128 v[124:127], v74 offset:36864
	ds_read_b128 v[128:131], v74 offset:37888
	ds_read_b128 v[132:135], v74 offset:38912
	ds_read_b128 v[136:139], v74 offset:39936
	global_load_lds_dwordx4 v[148:149], off
	v_lshl_add_u64 v[148:149], s[36:37], 0, v[66:67]
	s_mov_b32 m0, s27
	s_nop 0
	global_load_lds_dwordx4 v[148:149], off
	s_waitcnt vmcnt(8)
	s_waitcnt lgkmcnt(0)
	s_barrier
	s_setprio 1
	s_waitcnt lgkmcnt(0)
	v_mfma_f32_16x16x32_bf16 v[60:63], v[76:79], v[108:111], v[60:63]
	v_mfma_f32_16x16x32_bf16 v[56:59], v[84:87], v[108:111], v[56:59]
	v_mfma_f32_16x16x32_bf16 v[44:47], v[84:87], v[116:119], v[44:47]
	v_mfma_f32_16x16x32_bf16 v[52:55], v[76:79], v[116:119], v[52:55]
	v_mfma_f32_16x16x32_bf16 v[36:39], v[76:79], v[124:127], v[36:39]
	v_mfma_f32_16x16x32_bf16 v[28:31], v[84:87], v[124:127], v[28:31]
	v_mfma_f32_16x16x32_bf16 v[12:15], v[84:87], v[132:135], v[12:15]
	v_mfma_f32_16x16x32_bf16 v[20:23], v[76:79], v[132:135], v[20:23]
	v_mfma_f32_16x16x32_bf16 v[60:63], v[80:83], v[112:115], v[60:63]
	v_mfma_f32_16x16x32_bf16 v[56:59], v[88:91], v[112:115], v[56:59]
	v_mfma_f32_16x16x32_bf16 v[44:47], v[88:91], v[120:123], v[44:47]
	v_mfma_f32_16x16x32_bf16 v[52:55], v[80:83], v[120:123], v[52:55]
	v_mfma_f32_16x16x32_bf16 v[36:39], v[80:83], v[128:131], v[36:39]
	v_mfma_f32_16x16x32_bf16 v[28:31], v[88:91], v[128:131], v[28:31]
	v_mfma_f32_16x16x32_bf16 v[12:15], v[88:91], v[136:139], v[12:15]
	v_mfma_f32_16x16x32_bf16 v[20:23], v[80:83], v[136:139], v[20:23]
	s_setprio 0
	s_setprio 1
	v_mfma_f32_16x16x32_bf16 v[48:51], v[92:95], v[108:111], v[48:51]
	v_mfma_f32_16x16x32_bf16 v[40:43], v[100:103], v[108:111], v[40:43]
	v_mfma_f32_16x16x32_bf16 v[24:27], v[100:103], v[116:119], v[24:27]
	v_mfma_f32_16x16x32_bf16 v[32:35], v[92:95], v[116:119], v[32:35]
	v_mfma_f32_16x16x32_bf16 v[16:19], v[92:95], v[124:127], v[16:19]
	v_mfma_f32_16x16x32_bf16 v[8:11], v[100:103], v[124:127], v[8:11]
	v_mfma_f32_16x16x32_bf16 v[0:3], v[100:103], v[132:135], v[0:3]
	v_mfma_f32_16x16x32_bf16 v[4:7], v[92:95], v[132:135], v[4:7]
	v_mfma_f32_16x16x32_bf16 v[48:51], v[96:99], v[112:115], v[48:51]
	v_mfma_f32_16x16x32_bf16 v[40:43], v[104:107], v[112:115], v[40:43]
	v_mfma_f32_16x16x32_bf16 v[24:27], v[104:107], v[120:123], v[24:27]
	v_mfma_f32_16x16x32_bf16 v[32:35], v[96:99], v[120:123], v[32:35]
	v_mfma_f32_16x16x32_bf16 v[16:19], v[96:99], v[128:131], v[16:19]
	v_mfma_f32_16x16x32_bf16 v[8:11], v[104:107], v[128:131], v[8:11]
	v_mfma_f32_16x16x32_bf16 v[0:3], v[104:107], v[136:139], v[0:3]
	v_mfma_f32_16x16x32_bf16 v[4:7], v[96:99], v[136:139], v[4:7]
	s_setprio 0
	s_barrier
	s_mov_b32 m0, s48
	v_lshl_add_u64 v[76:77], v[140:141], 0, s[68:69]
	global_load_lds_dwordx4 v[76:77], off
	v_lshl_add_u64 v[76:77], v[142:143], 0, s[68:69]
	s_mov_b32 m0, s28
	s_nop 0
	global_load_lds_dwordx4 v[76:77], off
	v_lshl_add_u64 v[76:77], s[30:31], 0, v[68:69]
	s_mov_b32 m0, s29
	s_nop 0
	global_load_lds_dwordx4 v[76:77], off
	v_lshl_add_u64 v[76:77], s[30:31], 0, v[64:65]
	s_mov_b32 m0, s42
	s_nop 0
	global_load_lds_dwordx4 v[76:77], off
	v_lshl_add_u64 v[76:77], v[144:145], 0, s[68:69]
	s_mov_b32 m0, s50
	s_nop 0
	global_load_lds_dwordx4 v[76:77], off
	v_lshl_add_u64 v[76:77], v[146:147], 0, s[68:69]
	s_mov_b32 m0, s51
	s_nop 0
	global_load_lds_dwordx4 v[76:77], off
	s_waitcnt vmcnt(8)
	s_waitcnt lgkmcnt(0)
	s_barrier
	s_setprio 1
	s_setprio 0
	s_setprio 1
	s_setprio 0
	s_barrier
	s_andn2_b64 vcc, exec, s[18:19]
	s_mov_b64 s[30:31], -1
	s_mov_b64 s[18:19], 0
	s_movk_i32 s28, 0x100
	s_cbranch_vccz .LBB0_667
	s_and_b64 vcc, exec, s[6:7]
	s_cbranch_vccz .LBB0_670
	s_barrier

.LBB0_682:
	s_add_u32 s18, s16, 0x100
	s_addc_u32 s19, s17, 0
	s_add_u32 s28, s45, s16
	s_addc_u32 s29, s46, s17
	s_cmp_eq_u32 s47, 4
	s_cselect_b32 s36, 0, s18
	s_cselect_b32 s37, 0, s19
	s_cselect_b32 s30, s44, s28
	s_cselect_b32 s31, s9, s29
	s_add_u32 s36, s64, s36
	s_addc_u32 s37, s65, s37
	s_add_i32 s28, 0, 0x10000
	s_add_i32 s29, 0, 0x14000
	v_add_u32_e32 v168, s28, v154
	v_add_u32_e32 v194, s29, v154
	ds_read_b128 v[156:159], v168
	ds_read_b128 v[160:163], v168 offset:1024
	ds_read_b128 v[164:167], v168 offset:2048
	ds_read_b128 v[168:171], v168 offset:3072
	ds_read_b128 v[172:175], v194
	ds_read_b128 v[176:179], v194 offset:1024
	ds_read_b128 v[180:183], v194 offset:2048
	ds_read_b128 v[194:197], v194 offset:3072
	v_lshl_add_u64 v[210:211], v[150:151], 0, s[16:17]
	s_add_i32 m0, s20, 0xc000
	ds_read_b128 v[198:201], v155
	ds_read_b128 v[202:205], v155 offset:1024
	ds_read_b128 v[206:209], v155 offset:2048
	ds_read_b128 v[224:227], v155 offset:3072
	ds_read_b128 v[228:231], v155 offset:4096
	ds_read_b128 v[232:235], v155 offset:5120
	ds_read_b128 v[236:239], v155 offset:6144
	ds_read_b128 v[240:243], v155 offset:7168
	global_load_lds_dwordx4 v[210:211], off
	v_lshl_add_u64 v[210:211], v[152:153], 0, s[16:17]
	s_add_i32 m0, s20, 0xe000
	s_nop 0
	global_load_lds_dwordx4 v[210:211], off
	s_waitcnt vmcnt(8)
	s_waitcnt lgkmcnt(0)
	s_barrier
	s_setprio 1
	s_waitcnt lgkmcnt(0)
	v_mfma_f32_16x16x32_bf16 v[124:127], v[156:159], v[198:201], v[124:127]
	v_mfma_f32_16x16x32_bf16 v[120:123], v[164:167], v[198:201], v[120:123]
	v_mfma_f32_16x16x32_bf16 v[108:111], v[164:167], v[206:209], v[108:111]
	v_mfma_f32_16x16x32_bf16 v[116:119], v[156:159], v[206:209], v[116:119]
	v_mfma_f32_16x16x32_bf16 v[100:103], v[156:159], v[228:231], v[100:103]
	v_mfma_f32_16x16x32_bf16 v[92:95], v[164:167], v[228:231], v[92:95]
	v_mfma_f32_16x16x32_bf16 v[76:79], v[164:167], v[236:239], v[76:79]
	v_mfma_f32_16x16x32_bf16 v[84:87], v[156:159], v[236:239], v[84:87]
	v_mfma_f32_16x16x32_bf16 v[124:127], v[160:163], v[202:205], v[124:127]
	v_mfma_f32_16x16x32_bf16 v[120:123], v[168:171], v[202:205], v[120:123]
	v_mfma_f32_16x16x32_bf16 v[108:111], v[168:171], v[224:227], v[108:111]
	v_mfma_f32_16x16x32_bf16 v[116:119], v[160:163], v[224:227], v[116:119]
	v_mfma_f32_16x16x32_bf16 v[100:103], v[160:163], v[232:235], v[100:103]
	v_mfma_f32_16x16x32_bf16 v[92:95], v[168:171], v[232:235], v[92:95]
	v_mfma_f32_16x16x32_bf16 v[76:79], v[168:171], v[240:243], v[76:79]
	v_mfma_f32_16x16x32_bf16 v[84:87], v[160:163], v[240:243], v[84:87]
	s_setprio 0
	s_setprio 1
	v_mfma_f32_16x16x32_bf16 v[112:115], v[172:175], v[198:201], v[112:115]
	v_mfma_f32_16x16x32_bf16 v[104:107], v[180:183], v[198:201], v[104:107]
	v_mfma_f32_16x16x32_bf16 v[88:91], v[180:183], v[206:209], v[88:91]
	v_mfma_f32_16x16x32_bf16 v[96:99], v[172:175], v[206:209], v[96:99]
	v_mfma_f32_16x16x32_bf16 v[80:83], v[172:175], v[228:231], v[80:83]
	v_mfma_f32_16x16x32_bf16 v[72:75], v[180:183], v[228:231], v[72:75]
	v_mfma_f32_16x16x32_bf16 v[64:67], v[180:183], v[236:239], v[64:67]
	v_mfma_f32_16x16x32_bf16 v[68:71], v[172:175], v[236:239], v[68:71]
	v_mfma_f32_16x16x32_bf16 v[112:115], v[176:179], v[202:205], v[112:115]
	v_mfma_f32_16x16x32_bf16 v[104:107], v[194:197], v[202:205], v[104:107]
	v_mfma_f32_16x16x32_bf16 v[88:91], v[194:197], v[224:227], v[88:91]
	v_mfma_f32_16x16x32_bf16 v[96:99], v[176:179], v[224:227], v[96:99]
	v_mfma_f32_16x16x32_bf16 v[80:83], v[176:179], v[232:235], v[80:83]
	v_mfma_f32_16x16x32_bf16 v[72:75], v[194:197], v[232:235], v[72:75]
	v_mfma_f32_16x16x32_bf16 v[64:67], v[194:197], v[240:243], v[64:67]
	v_mfma_f32_16x16x32_bf16 v[68:71], v[176:179], v[240:243], v[68:71]
	s_setprio 0
	s_barrier
	s_add_i32 s16, s28, s4
	v_lshl_add_u64 v[210:211], s[30:31], 0, v[184:185]
	s_mov_b32 m0, s16
	ds_read_b128 v[198:201], v155 offset:16384
	ds_read_b128 v[202:205], v155 offset:17408
	ds_read_b128 v[206:209], v155 offset:18432
	ds_read_b128 v[224:227], v155 offset:19456
	ds_read_b128 v[228:231], v155 offset:20480
	ds_read_b128 v[232:235], v155 offset:21504
	ds_read_b128 v[236:239], v155 offset:22528
	ds_read_b128 v[240:243], v155 offset:23552
	global_load_lds_dwordx4 v[210:211], off
	s_add_i32 m0, s16, 0x2000
	s_add_u32 s16, s30, 0x20000
	v_lshl_add_u64 v[244:245], s[30:31], 0, v[128:129]
	s_addc_u32 s17, s31, 0
	s_add_i32 s28, s29, s4
	global_load_lds_dwordx4 v[244:245], off
	v_lshl_add_u64 v[246:247], s[16:17], 0, v[184:185]
	s_mov_b32 m0, s28
	v_lshl_add_u64 v[218:219], s[36:37], 0, v[130:131]
	global_load_lds_dwordx4 v[246:247], off
	v_lshl_add_u64 v[246:247], s[16:17], 0, v[128:129]
	s_add_i32 m0, s28, 0x2000
	s_nop 0
	global_load_lds_dwordx4 v[246:247], off
	v_lshl_add_u64 v[246:247], s[36:37], 0, v[132:133]
	s_mov_b32 m0, s20
	s_nop 0
	global_load_lds_dwordx4 v[246:247], off
	s_mov_b32 m0, s21
	s_nop 0
	global_load_lds_dwordx4 v[218:219], off
	s_waitcnt vmcnt(8)
	s_waitcnt lgkmcnt(0)
	s_barrier
	s_setprio 1
	s_waitcnt lgkmcnt(0)
	v_mfma_f32_16x16x32_bf16 v[60:63], v[156:159], v[198:201], v[60:63]
	v_mfma_f32_16x16x32_bf16 v[56:59], v[164:167], v[198:201], v[56:59]
	v_mfma_f32_16x16x32_bf16 v[44:47], v[164:167], v[206:209], v[44:47]
	v_mfma_f32_16x16x32_bf16 v[52:55], v[156:159], v[206:209], v[52:55]
	v_mfma_f32_16x16x32_bf16 v[36:39], v[156:159], v[228:231], v[36:39]
	v_mfma_f32_16x16x32_bf16 v[28:31], v[164:167], v[228:231], v[28:31]
	v_mfma_f32_16x16x32_bf16 v[12:15], v[164:167], v[236:239], v[12:15]
	v_mfma_f32_16x16x32_bf16 v[20:23], v[156:159], v[236:239], v[20:23]
	v_mfma_f32_16x16x32_bf16 v[60:63], v[160:163], v[202:205], v[60:63]
	v_mfma_f32_16x16x32_bf16 v[56:59], v[168:171], v[202:205], v[56:59]
	v_mfma_f32_16x16x32_bf16 v[44:47], v[168:171], v[224:227], v[44:47]
	v_mfma_f32_16x16x32_bf16 v[52:55], v[160:163], v[224:227], v[52:55]
	v_mfma_f32_16x16x32_bf16 v[36:39], v[160:163], v[232:235], v[36:39]
	v_mfma_f32_16x16x32_bf16 v[28:31], v[168:171], v[232:235], v[28:31]
	v_mfma_f32_16x16x32_bf16 v[12:15], v[168:171], v[240:243], v[12:15]
	v_mfma_f32_16x16x32_bf16 v[20:23], v[160:163], v[240:243], v[20:23]
	s_setprio 0
	s_setprio 1
	v_mfma_f32_16x16x32_bf16 v[48:51], v[172:175], v[198:201], v[48:51]
	v_mfma_f32_16x16x32_bf16 v[40:43], v[180:183], v[198:201], v[40:43]
	v_mfma_f32_16x16x32_bf16 v[24:27], v[180:183], v[206:209], v[24:27]
	v_mfma_f32_16x16x32_bf16 v[32:35], v[172:175], v[206:209], v[32:35]
	v_mfma_f32_16x16x32_bf16 v[16:19], v[172:175], v[228:231], v[16:19]
	v_mfma_f32_16x16x32_bf16 v[8:11], v[180:183], v[228:231], v[8:11]
	v_mfma_f32_16x16x32_bf16 v[0:3], v[180:183], v[236:239], v[0:3]
	v_mfma_f32_16x16x32_bf16 v[4:7], v[172:175], v[236:239], v[4:7]
	v_mfma_f32_16x16x32_bf16 v[48:51], v[176:179], v[202:205], v[48:51]
	v_mfma_f32_16x16x32_bf16 v[40:43], v[194:197], v[202:205], v[40:43]
	v_mfma_f32_16x16x32_bf16 v[24:27], v[194:197], v[224:227], v[24:27]
	v_mfma_f32_16x16x32_bf16 v[32:35], v[176:179], v[224:227], v[32:35]
	v_mfma_f32_16x16x32_bf16 v[16:19], v[176:179], v[232:235], v[16:19]
	v_mfma_f32_16x16x32_bf16 v[8:11], v[194:197], v[232:235], v[8:11]
	v_mfma_f32_16x16x32_bf16 v[0:3], v[194:197], v[240:243], v[0:3]
	v_mfma_f32_16x16x32_bf16 v[4:7], v[176:179], v[240:243], v[4:7]
	s_setprio 0
	s_barrier
	s_add_i32 s28, 0, 0x18000
	s_add_i32 s29, 0, 0x1c000
	v_add_u32_e32 v168, s28, v154
	v_add_u32_e32 v194, s29, v154
	ds_read_b128 v[156:159], v168
	ds_read_b128 v[160:163], v168 offset:1024
	ds_read_b128 v[164:167], v168 offset:2048
	ds_read_b128 v[168:171], v168 offset:3072
	ds_read_b128 v[172:175], v194
	ds_read_b128 v[176:179], v194 offset:1024
	ds_read_b128 v[180:183], v194 offset:2048
	ds_read_b128 v[194:197], v194 offset:3072
	s_add_u32 s16, s36, 0x20000
	s_addc_u32 s17, s37, 0
	s_mov_b32 m0, s26
	v_lshl_add_u64 v[216:217], s[16:17], 0, v[132:133]
	ds_read_b128 v[198:201], v155 offset:32768
	ds_read_b128 v[202:205], v155 offset:33792
	ds_read_b128 v[206:209], v155 offset:34816
	ds_read_b128 v[224:227], v155 offset:35840
	ds_read_b128 v[228:231], v155 offset:36864
	ds_read_b128 v[232:235], v155 offset:37888
	ds_read_b128 v[236:239], v155 offset:38912
	ds_read_b128 v[240:243], v155 offset:39936
	global_load_lds_dwordx4 v[216:217], off
	v_lshl_add_u64 v[216:217], s[16:17], 0, v[130:131]
	s_mov_b32 m0, s27
	s_nop 0
	global_load_lds_dwordx4 v[216:217], off
	s_waitcnt vmcnt(8)
	s_waitcnt lgkmcnt(0)
	s_barrier
	s_setprio 1
	s_waitcnt lgkmcnt(0)
	v_mfma_f32_16x16x32_bf16 v[124:127], v[156:159], v[198:201], v[124:127]
	v_mfma_f32_16x16x32_bf16 v[120:123], v[164:167], v[198:201], v[120:123]
	v_mfma_f32_16x16x32_bf16 v[108:111], v[164:167], v[206:209], v[108:111]
	v_mfma_f32_16x16x32_bf16 v[116:119], v[156:159], v[206:209], v[116:119]
	v_mfma_f32_16x16x32_bf16 v[100:103], v[156:159], v[228:231], v[100:103]
	v_mfma_f32_16x16x32_bf16 v[92:95], v[164:167], v[228:231], v[92:95]
	v_mfma_f32_16x16x32_bf16 v[76:79], v[164:167], v[236:239], v[76:79]
	v_mfma_f32_16x16x32_bf16 v[84:87], v[156:159], v[236:239], v[84:87]
	v_mfma_f32_16x16x32_bf16 v[124:127], v[160:163], v[202:205], v[124:127]
	v_mfma_f32_16x16x32_bf16 v[120:123], v[168:171], v[202:205], v[120:123]
	v_mfma_f32_16x16x32_bf16 v[108:111], v[168:171], v[224:227], v[108:111]
	v_mfma_f32_16x16x32_bf16 v[116:119], v[160:163], v[224:227], v[116:119]
	v_mfma_f32_16x16x32_bf16 v[100:103], v[160:163], v[232:235], v[100:103]
	v_mfma_f32_16x16x32_bf16 v[92:95], v[168:171], v[232:235], v[92:95]
	v_mfma_f32_16x16x32_bf16 v[76:79], v[168:171], v[240:243], v[76:79]
	v_mfma_f32_16x16x32_bf16 v[84:87], v[160:163], v[240:243], v[84:87]
	s_setprio 0
	s_setprio 1
	v_mfma_f32_16x16x32_bf16 v[112:115], v[172:175], v[198:201], v[112:115]
	v_mfma_f32_16x16x32_bf16 v[104:107], v[180:183], v[198:201], v[104:107]
	v_mfma_f32_16x16x32_bf16 v[88:91], v[180:183], v[206:209], v[88:91]
	v_mfma_f32_16x16x32_bf16 v[96:99], v[172:175], v[206:209], v[96:99]
	v_mfma_f32_16x16x32_bf16 v[80:83], v[172:175], v[228:231], v[80:83]
	v_mfma_f32_16x16x32_bf16 v[72:75], v[180:183], v[228:231], v[72:75]
	v_mfma_f32_16x16x32_bf16 v[64:67], v[180:183], v[236:239], v[64:67]
	v_mfma_f32_16x16x32_bf16 v[68:71], v[172:175], v[236:239], v[68:71]
	v_mfma_f32_16x16x32_bf16 v[112:115], v[176:179], v[202:205], v[112:115]
	v_mfma_f32_16x16x32_bf16 v[104:107], v[194:197], v[202:205], v[104:107]
	v_mfma_f32_16x16x32_bf16 v[88:91], v[194:197], v[224:227], v[88:91]
	v_mfma_f32_16x16x32_bf16 v[96:99], v[176:179], v[224:227], v[96:99]
	v_mfma_f32_16x16x32_bf16 v[80:83], v[176:179], v[232:235], v[80:83]
	v_mfma_f32_16x16x32_bf16 v[72:75], v[194:197], v[232:235], v[72:75]
	v_mfma_f32_16x16x32_bf16 v[64:67], v[194:197], v[240:243], v[64:67]
	v_mfma_f32_16x16x32_bf16 v[68:71], v[176:179], v[240:243], v[68:71]
	s_setprio 0
	s_barrier
	s_add_i32 s16, s28, s4
	v_lshl_add_u64 v[210:211], v[210:211], 0, s[68:69]
	s_mov_b32 m0, s16
	ds_read_b128 v[198:201], v155 offset:49152
	ds_read_b128 v[202:205], v155 offset:50176
	ds_read_b128 v[206:209], v155 offset:51200
	ds_read_b128 v[224:227], v155 offset:52224
	ds_read_b128 v[228:231], v155 offset:53248
	ds_read_b128 v[232:235], v155 offset:54272
	ds_read_b128 v[236:239], v155 offset:55296
	ds_read_b128 v[240:243], v155 offset:56320
	global_load_lds_dwordx4 v[210:211], off
	s_add_i32 m0, s16, 0x2000
	s_add_u32 s16, s30, 0x20080
	v_lshl_add_u64 v[210:211], v[244:245], 0, s[68:69]
	s_addc_u32 s17, s31, 0
	s_add_i32 s28, s29, s4
	global_load_lds_dwordx4 v[210:211], off
	v_lshl_add_u64 v[210:211], s[16:17], 0, v[184:185]
	s_mov_b32 m0, s28
	s_nop 0
	global_load_lds_dwordx4 v[210:211], off
	v_lshl_add_u64 v[210:211], s[16:17], 0, v[128:129]
	s_add_i32 m0, s28, 0x2000
	s_nop 0
	global_load_lds_dwordx4 v[210:211], off
	v_lshl_add_u64 v[210:211], v[246:247], 0, s[68:69]
	s_mov_b32 m0, s38
	s_nop 0
	global_load_lds_dwordx4 v[210:211], off
	v_lshl_add_u64 v[210:211], v[218:219], 0, s[68:69]
	s_mov_b32 m0, s39
	s_nop 0
	global_load_lds_dwordx4 v[210:211], off
	s_waitcnt vmcnt(8)
	s_waitcnt lgkmcnt(0)
	s_barrier
	s_setprio 1
	s_waitcnt lgkmcnt(0)
	v_mfma_f32_16x16x32_bf16 v[60:63], v[156:159], v[198:201], v[60:63]
	v_mfma_f32_16x16x32_bf16 v[56:59], v[164:167], v[198:201], v[56:59]
	v_mfma_f32_16x16x32_bf16 v[44:47], v[164:167], v[206:209], v[44:47]
	v_mfma_f32_16x16x32_bf16 v[52:55], v[156:159], v[206:209], v[52:55]
	v_mfma_f32_16x16x32_bf16 v[36:39], v[156:159], v[228:231], v[36:39]
	v_mfma_f32_16x16x32_bf16 v[28:31], v[164:167], v[228:231], v[28:31]
	v_mfma_f32_16x16x32_bf16 v[12:15], v[164:167], v[236:239], v[12:15]
	v_mfma_f32_16x16x32_bf16 v[20:23], v[156:159], v[236:239], v[20:23]
	v_mfma_f32_16x16x32_bf16 v[60:63], v[160:163], v[202:205], v[60:63]
	v_mfma_f32_16x16x32_bf16 v[56:59], v[168:171], v[202:205], v[56:59]
	v_mfma_f32_16x16x32_bf16 v[44:47], v[168:171], v[224:227], v[44:47]
	v_mfma_f32_16x16x32_bf16 v[52:55], v[160:163], v[224:227], v[52:55]
	v_mfma_f32_16x16x32_bf16 v[36:39], v[160:163], v[232:235], v[36:39]
	v_mfma_f32_16x16x32_bf16 v[28:31], v[168:171], v[232:235], v[28:31]
	v_mfma_f32_16x16x32_bf16 v[12:15], v[168:171], v[240:243], v[12:15]
	v_mfma_f32_16x16x32_bf16 v[20:23], v[160:163], v[240:243], v[20:23]
	s_setprio 0
	s_setprio 1
	v_mfma_f32_16x16x32_bf16 v[48:51], v[172:175], v[198:201], v[48:51]
	v_mfma_f32_16x16x32_bf16 v[40:43], v[180:183], v[198:201], v[40:43]
	v_mfma_f32_16x16x32_bf16 v[24:27], v[180:183], v[206:209], v[24:27]
	v_mfma_f32_16x16x32_bf16 v[32:35], v[172:175], v[206:209], v[32:35]
	v_mfma_f32_16x16x32_bf16 v[16:19], v[172:175], v[228:231], v[16:19]
	v_mfma_f32_16x16x32_bf16 v[8:11], v[180:183], v[228:231], v[8:11]
	v_mfma_f32_16x16x32_bf16 v[0:3], v[180:183], v[236:239], v[0:3]
	v_mfma_f32_16x16x32_bf16 v[4:7], v[172:175], v[236:239], v[4:7]
	v_mfma_f32_16x16x32_bf16 v[48:51], v[176:179], v[202:205], v[48:51]
	v_mfma_f32_16x16x32_bf16 v[40:43], v[194:197], v[202:205], v[40:43]
	v_mfma_f32_16x16x32_bf16 v[24:27], v[194:197], v[224:227], v[24:27]
	v_mfma_f32_16x16x32_bf16 v[32:35], v[176:179], v[224:227], v[32:35]
	v_mfma_f32_16x16x32_bf16 v[16:19], v[176:179], v[232:235], v[16:19]
	v_mfma_f32_16x16x32_bf16 v[8:11], v[194:197], v[232:235], v[8:11]
	v_mfma_f32_16x16x32_bf16 v[0:3], v[194:197], v[240:243], v[0:3]
	v_mfma_f32_16x16x32_bf16 v[4:7], v[176:179], v[240:243], v[4:7]
	s_setprio 0
	s_barrier
	s_add_i32 s47, s47, 2
	s_cmp_gt_u32 s47, 5
	s_mov_b64 s[16:17], s[18:19]
	s_cbranch_scc0 .LBB0_682
	s_and_b64 vcc, exec, s[6:7]
	s_cbranch_vccz .LBB0_685
	s_barrier

.LBB0_805:
	s_add_u32 s28, s30, 0xfff80080
	s_addc_u32 s29, s31, -1
	s_add_i32 s38, 0, 0x10000
	s_cmp_eq_u32 s78, 28
	s_cselect_b32 s45, s9, s29
	s_cselect_b32 s44, s11, s28
	s_cselect_b32 s41, s60, s63
	s_cselect_b32 s40, s61, s62
	s_add_i32 s39, 0, 0x14000
	v_add_u32_e32 v154, s38, v143
	v_add_u32_e32 v170, s39, v143
	ds_read_b128 v[138:141], v154
	ds_read_b128 v[146:149], v154 offset:1024
	ds_read_b128 v[150:153], v154 offset:2048
	ds_read_b128 v[154:157], v154 offset:3072
	ds_read_b128 v[158:161], v170
	ds_read_b128 v[162:165], v170 offset:1024
	ds_read_b128 v[166:169], v170 offset:2048
	ds_read_b128 v[170:173], v170 offset:3072
	v_lshl_add_u64 v[182:183], s[30:31], 0, v[134:135]
	s_add_i32 m0, s21, 0xc000
	ds_read_b128 v[174:177], v145
	ds_read_b128 v[178:181], v145 offset:1024
	ds_read_b128 v[194:197], v145 offset:2048
	ds_read_b128 v[198:201], v145 offset:3072
	ds_read_b128 v[202:205], v145 offset:4096
	ds_read_b128 v[206:209], v145 offset:5120
	ds_read_b128 v[224:227], v145 offset:6144
	ds_read_b128 v[228:231], v145 offset:7168
	global_load_lds_dwordx4 v[182:183], off
	v_lshl_add_u64 v[182:183], s[30:31], 0, v[136:137]
	s_add_i32 m0, s21, 0xe000
	s_nop 0
	global_load_lds_dwordx4 v[182:183], off
	s_waitcnt vmcnt(8)
	s_waitcnt lgkmcnt(0)
	s_barrier
	s_setprio 1
	s_waitcnt lgkmcnt(0)
	v_mfma_f32_16x16x32_bf16 v[124:127], v[138:141], v[174:177], v[124:127]
	v_mfma_f32_16x16x32_bf16 v[120:123], v[150:153], v[174:177], v[120:123]
	v_mfma_f32_16x16x32_bf16 v[104:107], v[150:153], v[194:197], v[104:107]
	v_mfma_f32_16x16x32_bf16 v[116:119], v[138:141], v[194:197], v[116:119]
	v_mfma_f32_16x16x32_bf16 v[100:103], v[138:141], v[202:205], v[100:103]
	v_mfma_f32_16x16x32_bf16 v[88:91], v[150:153], v[202:205], v[88:91]
	v_mfma_f32_16x16x32_bf16 v[72:75], v[150:153], v[224:227], v[72:75]
	v_mfma_f32_16x16x32_bf16 v[84:87], v[138:141], v[224:227], v[84:87]
	v_mfma_f32_16x16x32_bf16 v[124:127], v[146:149], v[178:181], v[124:127]
	v_mfma_f32_16x16x32_bf16 v[120:123], v[154:157], v[178:181], v[120:123]
	v_mfma_f32_16x16x32_bf16 v[104:107], v[154:157], v[198:201], v[104:107]
	v_mfma_f32_16x16x32_bf16 v[116:119], v[146:149], v[198:201], v[116:119]
	v_mfma_f32_16x16x32_bf16 v[100:103], v[146:149], v[206:209], v[100:103]
	v_mfma_f32_16x16x32_bf16 v[88:91], v[154:157], v[206:209], v[88:91]
	v_mfma_f32_16x16x32_bf16 v[72:75], v[154:157], v[228:231], v[72:75]
	v_mfma_f32_16x16x32_bf16 v[84:87], v[146:149], v[228:231], v[84:87]
	s_setprio 0
	s_setprio 1
	v_mfma_f32_16x16x32_bf16 v[112:115], v[158:161], v[174:177], v[112:115]
	v_mfma_f32_16x16x32_bf16 v[108:111], v[166:169], v[174:177], v[108:111]
	v_mfma_f32_16x16x32_bf16 v[92:95], v[166:169], v[194:197], v[92:95]
	v_mfma_f32_16x16x32_bf16 v[96:99], v[158:161], v[194:197], v[96:99]
	v_mfma_f32_16x16x32_bf16 v[80:83], v[158:161], v[202:205], v[80:83]
	v_mfma_f32_16x16x32_bf16 v[76:79], v[166:169], v[202:205], v[76:79]
	v_mfma_f32_16x16x32_bf16 v[64:67], v[166:169], v[224:227], v[64:67]
	v_mfma_f32_16x16x32_bf16 v[68:71], v[158:161], v[224:227], v[68:71]
	v_mfma_f32_16x16x32_bf16 v[112:115], v[162:165], v[178:181], v[112:115]
	v_mfma_f32_16x16x32_bf16 v[108:111], v[170:173], v[178:181], v[108:111]
	v_mfma_f32_16x16x32_bf16 v[92:95], v[170:173], v[198:201], v[92:95]
	v_mfma_f32_16x16x32_bf16 v[96:99], v[162:165], v[198:201], v[96:99]
	v_mfma_f32_16x16x32_bf16 v[80:83], v[162:165], v[206:209], v[80:83]
	v_mfma_f32_16x16x32_bf16 v[76:79], v[170:173], v[206:209], v[76:79]
	v_mfma_f32_16x16x32_bf16 v[64:67], v[170:173], v[228:231], v[64:67]
	v_mfma_f32_16x16x32_bf16 v[68:71], v[162:165], v[228:231], v[68:71]
	s_setprio 0
	s_barrier
	s_add_i32 s28, s38, s20
	v_lshl_add_u64 v[182:183], s[40:41], 0, v[184:185]
	s_mov_b32 m0, s28
	ds_read_b128 v[174:177], v145 offset:16384
	ds_read_b128 v[178:181], v145 offset:17408
	ds_read_b128 v[194:197], v145 offset:18432
	ds_read_b128 v[198:201], v145 offset:19456
	ds_read_b128 v[202:205], v145 offset:20480
	ds_read_b128 v[206:209], v145 offset:21504
	ds_read_b128 v[224:227], v145 offset:22528
	ds_read_b128 v[228:231], v145 offset:23552
	global_load_lds_dwordx4 v[182:183], off
	s_add_i32 m0, s28, 0x2000
	s_add_u32 s28, s40, 0x80000
	v_lshl_add_u64 v[210:211], s[40:41], 0, v[128:129]
	s_addc_u32 s29, s41, 0
	s_add_i32 s38, s39, s20
	global_load_lds_dwordx4 v[210:211], off
	v_lshl_add_u64 v[216:217], s[28:29], 0, v[184:185]
	s_mov_b32 m0, s38
	v_lshl_add_u64 v[218:219], s[44:45], 0, v[130:131]
	global_load_lds_dwordx4 v[216:217], off
	v_lshl_add_u64 v[216:217], s[28:29], 0, v[128:129]
	s_add_i32 m0, s38, 0x2000
	s_nop 0
	global_load_lds_dwordx4 v[216:217], off
	v_lshl_add_u64 v[216:217], s[44:45], 0, v[132:133]
	s_mov_b32 m0, s21
	s_nop 0
	global_load_lds_dwordx4 v[216:217], off
	s_mov_b32 m0, s46
	s_nop 0
	global_load_lds_dwordx4 v[218:219], off
	s_waitcnt vmcnt(8)
	s_waitcnt lgkmcnt(0)
	s_barrier
	s_setprio 1
	s_waitcnt lgkmcnt(0)
	v_mfma_f32_16x16x32_bf16 v[60:63], v[138:141], v[174:177], v[60:63]
	v_mfma_f32_16x16x32_bf16 v[56:59], v[150:153], v[174:177], v[56:59]
	v_mfma_f32_16x16x32_bf16 v[40:43], v[150:153], v[194:197], v[40:43]
	v_mfma_f32_16x16x32_bf16 v[52:55], v[138:141], v[194:197], v[52:55]
	v_mfma_f32_16x16x32_bf16 v[36:39], v[138:141], v[202:205], v[36:39]
	v_mfma_f32_16x16x32_bf16 v[24:27], v[150:153], v[202:205], v[24:27]
	v_mfma_f32_16x16x32_bf16 v[8:11], v[150:153], v[224:227], v[8:11]
	v_mfma_f32_16x16x32_bf16 v[20:23], v[138:141], v[224:227], v[20:23]
	v_mfma_f32_16x16x32_bf16 v[60:63], v[146:149], v[178:181], v[60:63]
	v_mfma_f32_16x16x32_bf16 v[56:59], v[154:157], v[178:181], v[56:59]
	v_mfma_f32_16x16x32_bf16 v[40:43], v[154:157], v[198:201], v[40:43]
	v_mfma_f32_16x16x32_bf16 v[52:55], v[146:149], v[198:201], v[52:55]
	v_mfma_f32_16x16x32_bf16 v[36:39], v[146:149], v[206:209], v[36:39]
	v_mfma_f32_16x16x32_bf16 v[24:27], v[154:157], v[206:209], v[24:27]
	v_mfma_f32_16x16x32_bf16 v[8:11], v[154:157], v[228:231], v[8:11]
	v_mfma_f32_16x16x32_bf16 v[20:23], v[146:149], v[228:231], v[20:23]
	s_setprio 0
	s_setprio 1
	v_mfma_f32_16x16x32_bf16 v[48:51], v[158:161], v[174:177], v[48:51]
	v_mfma_f32_16x16x32_bf16 v[44:47], v[166:169], v[174:177], v[44:47]
	v_mfma_f32_16x16x32_bf16 v[28:31], v[166:169], v[194:197], v[28:31]
	v_mfma_f32_16x16x32_bf16 v[32:35], v[158:161], v[194:197], v[32:35]
	v_mfma_f32_16x16x32_bf16 v[16:19], v[158:161], v[202:205], v[16:19]
	v_mfma_f32_16x16x32_bf16 v[12:15], v[166:169], v[202:205], v[12:15]
	v_mfma_f32_16x16x32_bf16 v[0:3], v[166:169], v[224:227], v[0:3]
	v_mfma_f32_16x16x32_bf16 v[4:7], v[158:161], v[224:227], v[4:7]
	v_mfma_f32_16x16x32_bf16 v[48:51], v[162:165], v[178:181], v[48:51]
	v_mfma_f32_16x16x32_bf16 v[44:47], v[170:173], v[178:181], v[44:47]
	v_mfma_f32_16x16x32_bf16 v[28:31], v[170:173], v[198:201], v[28:31]
	v_mfma_f32_16x16x32_bf16 v[32:35], v[162:165], v[198:201], v[32:35]
	v_mfma_f32_16x16x32_bf16 v[16:19], v[162:165], v[206:209], v[16:19]
	v_mfma_f32_16x16x32_bf16 v[12:15], v[170:173], v[206:209], v[12:15]
	v_mfma_f32_16x16x32_bf16 v[0:3], v[170:173], v[228:231], v[0:3]
	v_mfma_f32_16x16x32_bf16 v[4:7], v[162:165], v[228:231], v[4:7]
	s_setprio 0
	s_barrier
	s_add_i32 s38, 0, 0x18000
	s_add_i32 s39, 0, 0x1c000
	v_add_u32_e32 v154, s38, v143
	v_add_u32_e32 v170, s39, v143
	ds_read_b128 v[138:141], v154
	ds_read_b128 v[146:149], v154 offset:1024
	ds_read_b128 v[150:153], v154 offset:2048
	ds_read_b128 v[154:157], v154 offset:3072
	ds_read_b128 v[158:161], v170
	ds_read_b128 v[162:165], v170 offset:1024
	ds_read_b128 v[166:169], v170 offset:2048
	ds_read_b128 v[170:173], v170 offset:3072
	s_add_u32 s28, s44, 0x80000
	s_addc_u32 s29, s45, 0
	s_mov_b32 m0, s47
	v_lshl_add_u64 v[232:233], s[28:29], 0, v[132:133]
	ds_read_b128 v[174:177], v145 offset:32768
	ds_read_b128 v[178:181], v145 offset:33792
	ds_read_b128 v[194:197], v145 offset:34816
	ds_read_b128 v[198:201], v145 offset:35840
	ds_read_b128 v[202:205], v145 offset:36864
	ds_read_b128 v[206:209], v145 offset:37888
	ds_read_b128 v[224:227], v145 offset:38912
	ds_read_b128 v[228:231], v145 offset:39936
	global_load_lds_dwordx4 v[232:233], off
	v_lshl_add_u64 v[232:233], s[28:29], 0, v[130:131]
	s_mov_b32 m0, s50
	s_nop 0
	global_load_lds_dwordx4 v[232:233], off
	s_waitcnt vmcnt(8)
	s_waitcnt lgkmcnt(0)
	s_barrier
	s_setprio 1
	s_waitcnt lgkmcnt(0)
	v_mfma_f32_16x16x32_bf16 v[124:127], v[138:141], v[174:177], v[124:127]
	v_mfma_f32_16x16x32_bf16 v[120:123], v[150:153], v[174:177], v[120:123]
	v_mfma_f32_16x16x32_bf16 v[104:107], v[150:153], v[194:197], v[104:107]
	v_mfma_f32_16x16x32_bf16 v[116:119], v[138:141], v[194:197], v[116:119]
	v_mfma_f32_16x16x32_bf16 v[100:103], v[138:141], v[202:205], v[100:103]
	v_mfma_f32_16x16x32_bf16 v[88:91], v[150:153], v[202:205], v[88:91]
	v_mfma_f32_16x16x32_bf16 v[72:75], v[150:153], v[224:227], v[72:75]
	v_mfma_f32_16x16x32_bf16 v[84:87], v[138:141], v[224:227], v[84:87]
	v_mfma_f32_16x16x32_bf16 v[124:127], v[146:149], v[178:181], v[124:127]
	v_mfma_f32_16x16x32_bf16 v[120:123], v[154:157], v[178:181], v[120:123]
	v_mfma_f32_16x16x32_bf16 v[104:107], v[154:157], v[198:201], v[104:107]
	v_mfma_f32_16x16x32_bf16 v[116:119], v[146:149], v[198:201], v[116:119]
	v_mfma_f32_16x16x32_bf16 v[100:103], v[146:149], v[206:209], v[100:103]
	v_mfma_f32_16x16x32_bf16 v[88:91], v[154:157], v[206:209], v[88:91]
	v_mfma_f32_16x16x32_bf16 v[72:75], v[154:157], v[228:231], v[72:75]
	v_mfma_f32_16x16x32_bf16 v[84:87], v[146:149], v[228:231], v[84:87]
	s_setprio 0
	s_setprio 1
	v_mfma_f32_16x16x32_bf16 v[112:115], v[158:161], v[174:177], v[112:115]
	v_mfma_f32_16x16x32_bf16 v[108:111], v[166:169], v[174:177], v[108:111]
	v_mfma_f32_16x16x32_bf16 v[92:95], v[166:169], v[194:197], v[92:95]
	v_mfma_f32_16x16x32_bf16 v[96:99], v[158:161], v[194:197], v[96:99]
	v_mfma_f32_16x16x32_bf16 v[80:83], v[158:161], v[202:205], v[80:83]
	v_mfma_f32_16x16x32_bf16 v[76:79], v[166:169], v[202:205], v[76:79]
	v_mfma_f32_16x16x32_bf16 v[64:67], v[166:169], v[224:227], v[64:67]
	v_mfma_f32_16x16x32_bf16 v[68:71], v[158:161], v[224:227], v[68:71]
	v_mfma_f32_16x16x32_bf16 v[112:115], v[162:165], v[178:181], v[112:115]
	v_mfma_f32_16x16x32_bf16 v[108:111], v[170:173], v[178:181], v[108:111]
	v_mfma_f32_16x16x32_bf16 v[92:95], v[170:173], v[198:201], v[92:95]
	v_mfma_f32_16x16x32_bf16 v[96:99], v[162:165], v[198:201], v[96:99]
	v_mfma_f32_16x16x32_bf16 v[80:83], v[162:165], v[206:209], v[80:83]
	v_mfma_f32_16x16x32_bf16 v[76:79], v[170:173], v[206:209], v[76:79]
	v_mfma_f32_16x16x32_bf16 v[64:67], v[170:173], v[228:231], v[64:67]
	v_mfma_f32_16x16x32_bf16 v[68:71], v[162:165], v[228:231], v[68:71]
	s_setprio 0
	s_barrier
	s_add_i32 s28, s38, s20
	v_lshl_add_u64 v[182:183], v[182:183], 0, s[68:69]
	s_mov_b32 m0, s28
	ds_read_b128 v[174:177], v145 offset:49152
	ds_read_b128 v[178:181], v145 offset:50176
	ds_read_b128 v[194:197], v145 offset:51200
	ds_read_b128 v[198:201], v145 offset:52224
	ds_read_b128 v[202:205], v145 offset:53248
	ds_read_b128 v[206:209], v145 offset:54272
	ds_read_b128 v[224:227], v145 offset:55296
	ds_read_b128 v[228:231], v145 offset:56320
	global_load_lds_dwordx4 v[182:183], off
	s_add_i32 m0, s28, 0x2000
	s_add_u32 s28, s40, 0x80080
	v_lshl_add_u64 v[182:183], v[210:211], 0, s[68:69]
	s_addc_u32 s29, s41, 0
	s_add_i32 s38, s39, s20
	global_load_lds_dwordx4 v[182:183], off
	v_lshl_add_u64 v[182:183], s[28:29], 0, v[184:185]
	s_mov_b32 m0, s38
	s_nop 0
	global_load_lds_dwordx4 v[182:183], off
	v_lshl_add_u64 v[182:183], s[28:29], 0, v[128:129]
	s_add_i32 m0, s38, 0x2000
	s_nop 0
	global_load_lds_dwordx4 v[182:183], off
	v_lshl_add_u64 v[182:183], v[216:217], 0, s[68:69]
	s_mov_b32 m0, s51
	s_nop 0
	global_load_lds_dwordx4 v[182:183], off
	v_lshl_add_u64 v[182:183], v[218:219], 0, s[68:69]
	s_mov_b32 m0, s52
	s_nop 0
	global_load_lds_dwordx4 v[182:183], off
	s_waitcnt vmcnt(8)
	s_waitcnt lgkmcnt(0)
	s_barrier
	s_setprio 1
	s_waitcnt lgkmcnt(0)
	v_mfma_f32_16x16x32_bf16 v[60:63], v[138:141], v[174:177], v[60:63]
	v_mfma_f32_16x16x32_bf16 v[56:59], v[150:153], v[174:177], v[56:59]
	v_mfma_f32_16x16x32_bf16 v[40:43], v[150:153], v[194:197], v[40:43]
	v_mfma_f32_16x16x32_bf16 v[52:55], v[138:141], v[194:197], v[52:55]
	v_mfma_f32_16x16x32_bf16 v[36:39], v[138:141], v[202:205], v[36:39]
	v_mfma_f32_16x16x32_bf16 v[24:27], v[150:153], v[202:205], v[24:27]
	v_mfma_f32_16x16x32_bf16 v[8:11], v[150:153], v[224:227], v[8:11]
	v_mfma_f32_16x16x32_bf16 v[20:23], v[138:141], v[224:227], v[20:23]
	v_mfma_f32_16x16x32_bf16 v[60:63], v[146:149], v[178:181], v[60:63]
	v_mfma_f32_16x16x32_bf16 v[56:59], v[154:157], v[178:181], v[56:59]
	v_mfma_f32_16x16x32_bf16 v[40:43], v[154:157], v[198:201], v[40:43]
	v_mfma_f32_16x16x32_bf16 v[52:55], v[146:149], v[198:201], v[52:55]
	v_mfma_f32_16x16x32_bf16 v[36:39], v[146:149], v[206:209], v[36:39]
	v_mfma_f32_16x16x32_bf16 v[24:27], v[154:157], v[206:209], v[24:27]
	v_mfma_f32_16x16x32_bf16 v[8:11], v[154:157], v[228:231], v[8:11]
	v_mfma_f32_16x16x32_bf16 v[20:23], v[146:149], v[228:231], v[20:23]
	s_setprio 0
	s_setprio 1
	v_mfma_f32_16x16x32_bf16 v[48:51], v[158:161], v[174:177], v[48:51]
	v_mfma_f32_16x16x32_bf16 v[44:47], v[166:169], v[174:177], v[44:47]
	v_mfma_f32_16x16x32_bf16 v[28:31], v[166:169], v[194:197], v[28:31]
	v_mfma_f32_16x16x32_bf16 v[32:35], v[158:161], v[194:197], v[32:35]
	v_mfma_f32_16x16x32_bf16 v[16:19], v[158:161], v[202:205], v[16:19]
	v_mfma_f32_16x16x32_bf16 v[12:15], v[166:169], v[202:205], v[12:15]
	v_mfma_f32_16x16x32_bf16 v[0:3], v[166:169], v[224:227], v[0:3]
	v_mfma_f32_16x16x32_bf16 v[4:7], v[158:161], v[224:227], v[4:7]
	v_mfma_f32_16x16x32_bf16 v[48:51], v[162:165], v[178:181], v[48:51]
	v_mfma_f32_16x16x32_bf16 v[44:47], v[170:173], v[178:181], v[44:47]
	v_mfma_f32_16x16x32_bf16 v[28:31], v[170:173], v[198:201], v[28:31]
	v_mfma_f32_16x16x32_bf16 v[32:35], v[162:165], v[198:201], v[32:35]
	v_mfma_f32_16x16x32_bf16 v[16:19], v[162:165], v[206:209], v[16:19]
	v_mfma_f32_16x16x32_bf16 v[12:15], v[170:173], v[206:209], v[12:15]
	v_mfma_f32_16x16x32_bf16 v[0:3], v[170:173], v[228:231], v[0:3]
	v_mfma_f32_16x16x32_bf16 v[4:7], v[162:165], v[228:231], v[4:7]
	s_setprio 0
	s_barrier
	s_add_i32 s78, s78, 2
	s_add_u32 s30, s30, 0x100
	s_addc_u32 s31, s31, 0
	s_add_u32 s62, s62, 0x100
	s_addc_u32 s63, s63, 0
	s_cmp_gt_u32 s78, 29
	s_cbranch_scc0 .LBB0_805
	s_and_b64 vcc, exec, s[6:7]
	s_cbranch_vccz .LBB0_808
	s_barrier

.LBB0_822:
	s_add_u32 s38, s46, s50
	s_addc_u32 s39, s47, 0
	s_add_u32 s42, s38, 0x100
	s_addc_u32 s43, s39, 0
	s_and_b64 s[28:29], s[78:79], exec
	s_cselect_b32 s53, s11, s43
	s_cselect_b32 s52, s13, s42
	s_add_u32 s28, s6, s50
	s_addc_u32 s29, s7, 0
	s_add_u32 s42, s28, 0x100
	s_addc_u32 s43, s29, 0
	s_add_i32 s76, 0, 0x10000
	s_and_b64 s[28:29], s[78:79], exec
	s_cselect_b32 s61, s36, s43
	s_cselect_b32 s60, s37, s42
	s_add_i32 s29, 0, 0x14000
	s_add_u32 vcc_lo, s38, 0x80080
	s_addc_u32 vcc_hi, s39, 0
	s_add_i32 s85, s76, s20
	s_add_i32 m0, s21, 0xc000
	s_add_i32 s90, s21, 0xe000
	s_add_i32 s49, s85, 0x2000
	v_add_u32_e32 v153, s76, v150
	s_add_u32 s62, s60, 0x80000
	ds_read_b128 v[154:157], v153
	ds_read_b128 v[158:161], v153 offset:1024
	ds_read_b128 v[162:165], v153 offset:2048
	ds_read_b128 v[166:169], v153 offset:3072
	v_add_u32_e32 v153, s29, v150
	s_addc_u32 s63, s61, 0
	s_add_i32 s43, s29, s20
	ds_read_b128 v[170:173], v153
	ds_read_b128 v[174:177], v153 offset:1024
	ds_read_b128 v[178:181], v153 offset:2048
	ds_read_b128 v[194:197], v153 offset:3072
	s_add_i32 s42, s43, 0x2000
	s_add_i32 s39, 0, 0x18000
	s_add_i32 s28, 0, 0x1c000
	s_add_u32 s50, s52, 0x80000
	s_addc_u32 s51, s53, 0
	s_add_i32 s38, s39, s20
	s_add_i32 s48, s38, 0x2000
	s_add_u32 s78, s60, 0x80080
	s_addc_u32 s79, s61, 0
	s_add_i32 s76, s28, s20
	s_add_i32 s29, s76, 0x2000
	v_lshl_add_u64 v[182:183], vcc, 0, v[132:133]
	ds_read_b128 v[198:201], v152
	ds_read_b128 v[202:205], v152 offset:1024
	ds_read_b128 v[206:209], v152 offset:2048
	ds_read_b128 v[224:227], v152 offset:3072
	ds_read_b128 v[228:231], v152 offset:4096
	ds_read_b128 v[232:235], v152 offset:5120
	ds_read_b128 v[236:239], v152 offset:6144
	ds_read_b128 v[240:243], v152 offset:7168
	global_load_lds_dwordx4 v[182:183], off
	v_lshl_add_u64 v[182:183], vcc, 0, v[130:131]
	s_mov_b32 m0, s90
	s_nop 0
	global_load_lds_dwordx4 v[182:183], off
	s_waitcnt vmcnt(8)
	s_waitcnt lgkmcnt(0)
	s_barrier
	s_setprio 1
	s_waitcnt lgkmcnt(0)
	v_mfma_f32_16x16x32_bf16 v[124:127], v[154:157], v[198:201], v[124:127]
	v_mfma_f32_16x16x32_bf16 v[120:123], v[162:165], v[198:201], v[120:123]
	v_mfma_f32_16x16x32_bf16 v[112:115], v[162:165], v[206:209], v[112:115]
	v_mfma_f32_16x16x32_bf16 v[116:119], v[154:157], v[206:209], v[116:119]
	v_mfma_f32_16x16x32_bf16 v[108:111], v[154:157], v[228:231], v[108:111]
	v_mfma_f32_16x16x32_bf16 v[104:107], v[162:165], v[228:231], v[104:107]
	v_mfma_f32_16x16x32_bf16 v[88:91], v[162:165], v[236:239], v[88:91]
	v_mfma_f32_16x16x32_bf16 v[96:99], v[154:157], v[236:239], v[96:99]
	v_mfma_f32_16x16x32_bf16 v[124:127], v[158:161], v[202:205], v[124:127]
	v_mfma_f32_16x16x32_bf16 v[120:123], v[166:169], v[202:205], v[120:123]
	v_mfma_f32_16x16x32_bf16 v[112:115], v[166:169], v[224:227], v[112:115]
	v_mfma_f32_16x16x32_bf16 v[116:119], v[158:161], v[224:227], v[116:119]
	v_mfma_f32_16x16x32_bf16 v[108:111], v[158:161], v[232:235], v[108:111]
	v_mfma_f32_16x16x32_bf16 v[104:107], v[166:169], v[232:235], v[104:107]
	v_mfma_f32_16x16x32_bf16 v[88:91], v[166:169], v[240:243], v[88:91]
	v_mfma_f32_16x16x32_bf16 v[96:99], v[158:161], v[240:243], v[96:99]
	s_setprio 0
	s_setprio 1
	v_mfma_f32_16x16x32_bf16 v[100:103], v[170:173], v[198:201], v[100:103]
	v_mfma_f32_16x16x32_bf16 v[92:95], v[178:181], v[198:201], v[92:95]
	v_mfma_f32_16x16x32_bf16 v[80:83], v[178:181], v[206:209], v[80:83]
	v_mfma_f32_16x16x32_bf16 v[84:87], v[170:173], v[206:209], v[84:87]
	v_mfma_f32_16x16x32_bf16 v[76:79], v[170:173], v[228:231], v[76:79]
	v_mfma_f32_16x16x32_bf16 v[72:75], v[178:181], v[228:231], v[72:75]
	v_mfma_f32_16x16x32_bf16 v[64:67], v[178:181], v[236:239], v[64:67]
	v_mfma_f32_16x16x32_bf16 v[68:71], v[170:173], v[236:239], v[68:71]
	v_mfma_f32_16x16x32_bf16 v[100:103], v[174:177], v[202:205], v[100:103]
	v_mfma_f32_16x16x32_bf16 v[92:95], v[194:197], v[202:205], v[92:95]
	v_mfma_f32_16x16x32_bf16 v[80:83], v[194:197], v[224:227], v[80:83]
	v_mfma_f32_16x16x32_bf16 v[84:87], v[174:177], v[224:227], v[84:87]
	v_mfma_f32_16x16x32_bf16 v[76:79], v[174:177], v[232:235], v[76:79]
	v_mfma_f32_16x16x32_bf16 v[72:75], v[194:197], v[232:235], v[72:75]
	v_mfma_f32_16x16x32_bf16 v[64:67], v[194:197], v[240:243], v[64:67]
	v_mfma_f32_16x16x32_bf16 v[68:71], v[174:177], v[240:243], v[68:71]
	s_setprio 0
	s_barrier
	s_mov_b32 m0, s85
	v_lshl_add_u64 v[182:183], s[60:61], 0, v[184:185]
	ds_read_b128 v[198:201], v152 offset:16384
	ds_read_b128 v[202:205], v152 offset:17408
	ds_read_b128 v[206:209], v152 offset:18432
	ds_read_b128 v[224:227], v152 offset:19456
	ds_read_b128 v[228:231], v152 offset:20480
	ds_read_b128 v[232:235], v152 offset:21504
	ds_read_b128 v[236:239], v152 offset:22528
	ds_read_b128 v[240:243], v152 offset:23552
	global_load_lds_dwordx4 v[182:183], off
	v_lshl_add_u64 v[210:211], s[60:61], 0, v[128:129]
	s_mov_b32 m0, s49
	v_lshl_add_u64 v[216:217], s[62:63], 0, v[184:185]
	global_load_lds_dwordx4 v[210:211], off
	s_mov_b32 m0, s43
	v_lshl_add_u64 v[218:219], s[52:53], 0, v[130:131]
	global_load_lds_dwordx4 v[216:217], off
	v_lshl_add_u64 v[216:217], s[62:63], 0, v[128:129]
	s_mov_b32 m0, s42
	s_nop 0
	global_load_lds_dwordx4 v[216:217], off
	v_lshl_add_u64 v[216:217], s[52:53], 0, v[132:133]
	s_mov_b32 m0, s21
	s_nop 0
	global_load_lds_dwordx4 v[216:217], off
	s_mov_b32 m0, s88
	s_nop 0
	global_load_lds_dwordx4 v[218:219], off
	s_waitcnt vmcnt(8)
	s_waitcnt lgkmcnt(0)
	s_barrier
	s_setprio 1
	s_waitcnt lgkmcnt(0)
	v_mfma_f32_16x16x32_bf16 v[60:63], v[154:157], v[198:201], v[60:63]
	v_mfma_f32_16x16x32_bf16 v[56:59], v[162:165], v[198:201], v[56:59]
	v_mfma_f32_16x16x32_bf16 v[48:51], v[162:165], v[206:209], v[48:51]
	v_mfma_f32_16x16x32_bf16 v[52:55], v[154:157], v[206:209], v[52:55]
	v_mfma_f32_16x16x32_bf16 v[44:47], v[154:157], v[228:231], v[44:47]
	v_mfma_f32_16x16x32_bf16 v[40:43], v[162:165], v[228:231], v[40:43]
	v_mfma_f32_16x16x32_bf16 v[24:27], v[162:165], v[236:239], v[24:27]
	v_mfma_f32_16x16x32_bf16 v[32:35], v[154:157], v[236:239], v[32:35]
	v_mfma_f32_16x16x32_bf16 v[60:63], v[158:161], v[202:205], v[60:63]
	v_mfma_f32_16x16x32_bf16 v[56:59], v[166:169], v[202:205], v[56:59]
	v_mfma_f32_16x16x32_bf16 v[48:51], v[166:169], v[224:227], v[48:51]
	v_mfma_f32_16x16x32_bf16 v[52:55], v[158:161], v[224:227], v[52:55]
	v_mfma_f32_16x16x32_bf16 v[44:47], v[158:161], v[232:235], v[44:47]
	v_mfma_f32_16x16x32_bf16 v[40:43], v[166:169], v[232:235], v[40:43]
	v_mfma_f32_16x16x32_bf16 v[24:27], v[166:169], v[240:243], v[24:27]
	v_mfma_f32_16x16x32_bf16 v[32:35], v[158:161], v[240:243], v[32:35]
	s_setprio 0
	s_setprio 1
	v_mfma_f32_16x16x32_bf16 v[36:39], v[170:173], v[198:201], v[36:39]
	v_mfma_f32_16x16x32_bf16 v[28:31], v[178:181], v[198:201], v[28:31]
	v_mfma_f32_16x16x32_bf16 v[16:19], v[178:181], v[206:209], v[16:19]
	v_mfma_f32_16x16x32_bf16 v[20:23], v[170:173], v[206:209], v[20:23]
	v_mfma_f32_16x16x32_bf16 v[12:15], v[170:173], v[228:231], v[12:15]
	v_mfma_f32_16x16x32_bf16 v[8:11], v[178:181], v[228:231], v[8:11]
	v_mfma_f32_16x16x32_bf16 v[0:3], v[178:181], v[236:239], v[0:3]
	v_mfma_f32_16x16x32_bf16 v[4:7], v[170:173], v[236:239], v[4:7]
	v_mfma_f32_16x16x32_bf16 v[36:39], v[174:177], v[202:205], v[36:39]
	v_mfma_f32_16x16x32_bf16 v[28:31], v[194:197], v[202:205], v[28:31]
	v_mfma_f32_16x16x32_bf16 v[16:19], v[194:197], v[224:227], v[16:19]
	v_mfma_f32_16x16x32_bf16 v[20:23], v[174:177], v[224:227], v[20:23]
	v_mfma_f32_16x16x32_bf16 v[12:15], v[174:177], v[232:235], v[12:15]
	v_mfma_f32_16x16x32_bf16 v[8:11], v[194:197], v[232:235], v[8:11]
	v_mfma_f32_16x16x32_bf16 v[0:3], v[194:197], v[240:243], v[0:3]
	v_mfma_f32_16x16x32_bf16 v[4:7], v[174:177], v[240:243], v[4:7]
	s_setprio 0
	s_barrier
	v_add_u32_e32 v153, s39, v150
	ds_read_b128 v[154:157], v153
	ds_read_b128 v[158:161], v153 offset:1024
	ds_read_b128 v[162:165], v153 offset:2048
	ds_read_b128 v[166:169], v153 offset:3072
	v_add_u32_e32 v153, s28, v150
	ds_read_b128 v[170:173], v153
	ds_read_b128 v[174:177], v153 offset:1024
	ds_read_b128 v[178:181], v153 offset:2048
	ds_read_b128 v[194:197], v153 offset:3072
	s_mov_b32 m0, s89
	v_lshl_add_u64 v[244:245], s[50:51], 0, v[132:133]
	ds_read_b128 v[198:201], v152 offset:32768
	ds_read_b128 v[202:205], v152 offset:33792
	ds_read_b128 v[206:209], v152 offset:34816
	ds_read_b128 v[224:227], v152 offset:35840
	ds_read_b128 v[228:231], v152 offset:36864
	ds_read_b128 v[232:235], v152 offset:37888
	ds_read_b128 v[236:239], v152 offset:38912
	ds_read_b128 v[240:243], v152 offset:39936
	global_load_lds_dwordx4 v[244:245], off
	v_lshl_add_u64 v[244:245], s[50:51], 0, v[130:131]
	s_mov_b32 m0, s92
	s_nop 0
	global_load_lds_dwordx4 v[244:245], off
	s_waitcnt vmcnt(8)
	s_waitcnt lgkmcnt(0)
	s_barrier
	s_setprio 1
	s_waitcnt lgkmcnt(0)
	v_mfma_f32_16x16x32_bf16 v[124:127], v[154:157], v[198:201], v[124:127]
	v_mfma_f32_16x16x32_bf16 v[120:123], v[162:165], v[198:201], v[120:123]
	v_mfma_f32_16x16x32_bf16 v[112:115], v[162:165], v[206:209], v[112:115]
	v_mfma_f32_16x16x32_bf16 v[116:119], v[154:157], v[206:209], v[116:119]
	v_mfma_f32_16x16x32_bf16 v[108:111], v[154:157], v[228:231], v[108:111]
	v_mfma_f32_16x16x32_bf16 v[104:107], v[162:165], v[228:231], v[104:107]
	v_mfma_f32_16x16x32_bf16 v[88:91], v[162:165], v[236:239], v[88:91]
	v_mfma_f32_16x16x32_bf16 v[96:99], v[154:157], v[236:239], v[96:99]
	v_mfma_f32_16x16x32_bf16 v[124:127], v[158:161], v[202:205], v[124:127]
	v_mfma_f32_16x16x32_bf16 v[120:123], v[166:169], v[202:205], v[120:123]
	v_mfma_f32_16x16x32_bf16 v[112:115], v[166:169], v[224:227], v[112:115]
	v_mfma_f32_16x16x32_bf16 v[116:119], v[158:161], v[224:227], v[116:119]
	v_mfma_f32_16x16x32_bf16 v[108:111], v[158:161], v[232:235], v[108:111]
	v_mfma_f32_16x16x32_bf16 v[104:107], v[166:169], v[232:235], v[104:107]
	v_mfma_f32_16x16x32_bf16 v[88:91], v[166:169], v[240:243], v[88:91]
	v_mfma_f32_16x16x32_bf16 v[96:99], v[158:161], v[240:243], v[96:99]
	s_setprio 0
	s_setprio 1
	v_mfma_f32_16x16x32_bf16 v[100:103], v[170:173], v[198:201], v[100:103]
	v_mfma_f32_16x16x32_bf16 v[92:95], v[178:181], v[198:201], v[92:95]
	v_mfma_f32_16x16x32_bf16 v[80:83], v[178:181], v[206:209], v[80:83]
	v_mfma_f32_16x16x32_bf16 v[84:87], v[170:173], v[206:209], v[84:87]
	v_mfma_f32_16x16x32_bf16 v[76:79], v[170:173], v[228:231], v[76:79]
	v_mfma_f32_16x16x32_bf16 v[72:75], v[178:181], v[228:231], v[72:75]
	v_mfma_f32_16x16x32_bf16 v[64:67], v[178:181], v[236:239], v[64:67]
	v_mfma_f32_16x16x32_bf16 v[68:71], v[170:173], v[236:239], v[68:71]
	v_mfma_f32_16x16x32_bf16 v[100:103], v[174:177], v[202:205], v[100:103]
	v_mfma_f32_16x16x32_bf16 v[92:95], v[194:197], v[202:205], v[92:95]
	v_mfma_f32_16x16x32_bf16 v[80:83], v[194:197], v[224:227], v[80:83]
	v_mfma_f32_16x16x32_bf16 v[84:87], v[174:177], v[224:227], v[84:87]
	v_mfma_f32_16x16x32_bf16 v[76:79], v[174:177], v[232:235], v[76:79]
	v_mfma_f32_16x16x32_bf16 v[72:75], v[194:197], v[232:235], v[72:75]
	v_mfma_f32_16x16x32_bf16 v[64:67], v[194:197], v[240:243], v[64:67]
	v_mfma_f32_16x16x32_bf16 v[68:71], v[174:177], v[240:243], v[68:71]
	s_setprio 0
	s_barrier
	s_mov_b32 m0, s38
	v_lshl_add_u64 v[182:183], v[182:183], 0, s[68:69]
	ds_read_b128 v[198:201], v152 offset:49152
	ds_read_b128 v[202:205], v152 offset:50176
	ds_read_b128 v[206:209], v152 offset:51200
	ds_read_b128 v[224:227], v152 offset:52224
	ds_read_b128 v[228:231], v152 offset:53248
	ds_read_b128 v[232:235], v152 offset:54272
	ds_read_b128 v[236:239], v152 offset:55296
	ds_read_b128 v[240:243], v152 offset:56320
	global_load_lds_dwordx4 v[182:183], off
	v_lshl_add_u64 v[182:183], v[210:211], 0, s[68:69]
	s_mov_b32 m0, s48
	s_nop 0
	global_load_lds_dwordx4 v[182:183], off
	v_lshl_add_u64 v[182:183], s[78:79], 0, v[184:185]
	s_mov_b32 m0, s76
	s_nop 0
	global_load_lds_dwordx4 v[182:183], off
	v_lshl_add_u64 v[182:183], s[78:79], 0, v[128:129]
	s_mov_b32 m0, s29
	s_nop 0
	global_load_lds_dwordx4 v[182:183], off
	v_lshl_add_u64 v[182:183], v[216:217], 0, s[68:69]
	s_mov_b32 m0, s93
	s_nop 0
	global_load_lds_dwordx4 v[182:183], off
	v_lshl_add_u64 v[182:183], v[218:219], 0, s[68:69]
	s_mov_b32 m0, s94
	s_nop 0
	global_load_lds_dwordx4 v[182:183], off
	s_waitcnt vmcnt(8)
	s_waitcnt lgkmcnt(0)
	s_barrier
	s_setprio 1
	s_waitcnt lgkmcnt(0)
	v_mfma_f32_16x16x32_bf16 v[60:63], v[154:157], v[198:201], v[60:63]
	v_mfma_f32_16x16x32_bf16 v[56:59], v[162:165], v[198:201], v[56:59]
	v_mfma_f32_16x16x32_bf16 v[48:51], v[162:165], v[206:209], v[48:51]
	v_mfma_f32_16x16x32_bf16 v[52:55], v[154:157], v[206:209], v[52:55]
	v_mfma_f32_16x16x32_bf16 v[44:47], v[154:157], v[228:231], v[44:47]
	v_mfma_f32_16x16x32_bf16 v[40:43], v[162:165], v[228:231], v[40:43]
	v_mfma_f32_16x16x32_bf16 v[24:27], v[162:165], v[236:239], v[24:27]
	v_mfma_f32_16x16x32_bf16 v[32:35], v[154:157], v[236:239], v[32:35]
	v_mfma_f32_16x16x32_bf16 v[60:63], v[158:161], v[202:205], v[60:63]
	v_mfma_f32_16x16x32_bf16 v[56:59], v[166:169], v[202:205], v[56:59]
	v_mfma_f32_16x16x32_bf16 v[48:51], v[166:169], v[224:227], v[48:51]
	v_mfma_f32_16x16x32_bf16 v[52:55], v[158:161], v[224:227], v[52:55]
	v_mfma_f32_16x16x32_bf16 v[44:47], v[158:161], v[232:235], v[44:47]
	v_mfma_f32_16x16x32_bf16 v[40:43], v[166:169], v[232:235], v[40:43]
	v_mfma_f32_16x16x32_bf16 v[24:27], v[166:169], v[240:243], v[24:27]
	v_mfma_f32_16x16x32_bf16 v[32:35], v[158:161], v[240:243], v[32:35]
	s_setprio 0
	s_setprio 1
	v_mfma_f32_16x16x32_bf16 v[36:39], v[170:173], v[198:201], v[36:39]
	v_mfma_f32_16x16x32_bf16 v[28:31], v[178:181], v[198:201], v[28:31]
	v_mfma_f32_16x16x32_bf16 v[16:19], v[178:181], v[206:209], v[16:19]
	v_mfma_f32_16x16x32_bf16 v[20:23], v[170:173], v[206:209], v[20:23]
	v_mfma_f32_16x16x32_bf16 v[12:15], v[170:173], v[228:231], v[12:15]
	v_mfma_f32_16x16x32_bf16 v[8:11], v[178:181], v[228:231], v[8:11]
	v_mfma_f32_16x16x32_bf16 v[0:3], v[178:181], v[236:239], v[0:3]
	v_mfma_f32_16x16x32_bf16 v[4:7], v[170:173], v[236:239], v[4:7]
	v_mfma_f32_16x16x32_bf16 v[36:39], v[174:177], v[202:205], v[36:39]
	v_mfma_f32_16x16x32_bf16 v[28:31], v[194:197], v[202:205], v[28:31]
	v_mfma_f32_16x16x32_bf16 v[16:19], v[194:197], v[224:227], v[16:19]
	v_mfma_f32_16x16x32_bf16 v[20:23], v[174:177], v[224:227], v[20:23]
	v_mfma_f32_16x16x32_bf16 v[12:15], v[174:177], v[232:235], v[12:15]
	v_mfma_f32_16x16x32_bf16 v[8:11], v[194:197], v[232:235], v[8:11]
	v_mfma_f32_16x16x32_bf16 v[0:3], v[194:197], v[240:243], v[0:3]
	v_mfma_f32_16x16x32_bf16 v[4:7], v[174:177], v[240:243], v[4:7]
	s_setprio 0
	s_barrier
	s_movk_i32 s50, 0x100
	s_andn2_b64 vcc, exec, s[58:59]
	s_mov_b64 s[78:79], -1
	s_mov_b64 s[58:59], 0
	s_cbranch_vccz .LBB0_822
	s_and_b64 vcc, exec, s[8:9]
	s_cbranch_vccz .LBB0_825
	s_barrier

.LBB0_842:
	s_add_u32 s28, s30, 0xfffc0080
	s_addc_u32 s29, s31, -1
	s_add_i32 s42, 0, 0x10000
	s_cmp_eq_u32 s60, 12
	s_cselect_b32 s45, s9, s29
	s_cselect_b32 s44, s11, s28
	s_cselect_b32 s41, s36, s59
	s_cselect_b32 s40, s37, s58
	s_add_i32 s43, 0, 0x14000
	v_add_u32_e32 v154, s42, v147
	v_add_u32_e32 v170, s43, v147
	ds_read_b128 v[138:141], v154
	ds_read_b128 v[142:145], v154 offset:1024
	ds_read_b128 v[150:153], v154 offset:2048
	ds_read_b128 v[154:157], v154 offset:3072
	ds_read_b128 v[158:161], v170
	ds_read_b128 v[162:165], v170 offset:1024
	ds_read_b128 v[166:169], v170 offset:2048
	ds_read_b128 v[170:173], v170 offset:3072
	v_lshl_add_u64 v[182:183], s[30:31], 0, v[134:135]
	s_add_i32 m0, s21, 0xc000
	ds_read_b128 v[174:177], v149
	ds_read_b128 v[178:181], v149 offset:1024
	ds_read_b128 v[194:197], v149 offset:2048
	ds_read_b128 v[198:201], v149 offset:3072
	ds_read_b128 v[202:205], v149 offset:4096
	ds_read_b128 v[206:209], v149 offset:5120
	ds_read_b128 v[224:227], v149 offset:6144
	ds_read_b128 v[228:231], v149 offset:7168
	global_load_lds_dwordx4 v[182:183], off
	v_lshl_add_u64 v[182:183], s[30:31], 0, v[136:137]
	s_add_i32 m0, s21, 0xe000
	s_nop 0
	global_load_lds_dwordx4 v[182:183], off
	s_waitcnt vmcnt(8)
	s_waitcnt lgkmcnt(0)
	s_barrier
	s_setprio 1
	s_waitcnt lgkmcnt(0)
	v_mfma_f32_16x16x32_bf16 v[124:127], v[138:141], v[174:177], v[124:127]
	v_mfma_f32_16x16x32_bf16 v[120:123], v[150:153], v[174:177], v[120:123]
	v_mfma_f32_16x16x32_bf16 v[104:107], v[150:153], v[194:197], v[104:107]
	v_mfma_f32_16x16x32_bf16 v[108:111], v[138:141], v[194:197], v[108:111]
	v_mfma_f32_16x16x32_bf16 v[92:95], v[138:141], v[202:205], v[92:95]
	v_mfma_f32_16x16x32_bf16 v[88:91], v[150:153], v[202:205], v[88:91]
	v_mfma_f32_16x16x32_bf16 v[72:75], v[150:153], v[224:227], v[72:75]
	v_mfma_f32_16x16x32_bf16 v[76:79], v[138:141], v[224:227], v[76:79]
	v_mfma_f32_16x16x32_bf16 v[124:127], v[142:145], v[178:181], v[124:127]
	v_mfma_f32_16x16x32_bf16 v[120:123], v[154:157], v[178:181], v[120:123]
	v_mfma_f32_16x16x32_bf16 v[104:107], v[154:157], v[198:201], v[104:107]
	v_mfma_f32_16x16x32_bf16 v[108:111], v[142:145], v[198:201], v[108:111]
	v_mfma_f32_16x16x32_bf16 v[92:95], v[142:145], v[206:209], v[92:95]
	v_mfma_f32_16x16x32_bf16 v[88:91], v[154:157], v[206:209], v[88:91]
	v_mfma_f32_16x16x32_bf16 v[72:75], v[154:157], v[228:231], v[72:75]
	v_mfma_f32_16x16x32_bf16 v[76:79], v[142:145], v[228:231], v[76:79]
	s_setprio 0
	s_setprio 1
	v_mfma_f32_16x16x32_bf16 v[116:119], v[158:161], v[174:177], v[116:119]
	v_mfma_f32_16x16x32_bf16 v[112:115], v[166:169], v[174:177], v[112:115]
	v_mfma_f32_16x16x32_bf16 v[96:99], v[166:169], v[194:197], v[96:99]
	v_mfma_f32_16x16x32_bf16 v[100:103], v[158:161], v[194:197], v[100:103]
	v_mfma_f32_16x16x32_bf16 v[84:87], v[158:161], v[202:205], v[84:87]
	v_mfma_f32_16x16x32_bf16 v[80:83], v[166:169], v[202:205], v[80:83]
	v_mfma_f32_16x16x32_bf16 v[64:67], v[166:169], v[224:227], v[64:67]
	v_mfma_f32_16x16x32_bf16 v[68:71], v[158:161], v[224:227], v[68:71]
	v_mfma_f32_16x16x32_bf16 v[116:119], v[162:165], v[178:181], v[116:119]
	v_mfma_f32_16x16x32_bf16 v[112:115], v[170:173], v[178:181], v[112:115]
	v_mfma_f32_16x16x32_bf16 v[96:99], v[170:173], v[198:201], v[96:99]
	v_mfma_f32_16x16x32_bf16 v[100:103], v[162:165], v[198:201], v[100:103]
	v_mfma_f32_16x16x32_bf16 v[84:87], v[162:165], v[206:209], v[84:87]
	v_mfma_f32_16x16x32_bf16 v[80:83], v[170:173], v[206:209], v[80:83]
	v_mfma_f32_16x16x32_bf16 v[64:67], v[170:173], v[228:231], v[64:67]
	v_mfma_f32_16x16x32_bf16 v[68:71], v[162:165], v[228:231], v[68:71]
	s_setprio 0
	s_barrier
	s_add_i32 s28, s42, s20
	v_lshl_add_u64 v[182:183], s[40:41], 0, v[184:185]
	s_mov_b32 m0, s28
	ds_read_b128 v[174:177], v149 offset:16384
	ds_read_b128 v[178:181], v149 offset:17408
	ds_read_b128 v[194:197], v149 offset:18432
	ds_read_b128 v[198:201], v149 offset:19456
	ds_read_b128 v[202:205], v149 offset:20480
	ds_read_b128 v[206:209], v149 offset:21504
	ds_read_b128 v[224:227], v149 offset:22528
	ds_read_b128 v[228:231], v149 offset:23552
	global_load_lds_dwordx4 v[182:183], off
	s_add_i32 m0, s28, 0x2000
	s_add_u32 s28, s40, 0x40000
	v_lshl_add_u64 v[210:211], s[40:41], 0, v[128:129]
	s_addc_u32 s29, s41, 0
	s_add_i32 s42, s43, s20
	global_load_lds_dwordx4 v[210:211], off
	v_lshl_add_u64 v[216:217], s[28:29], 0, v[184:185]
	s_mov_b32 m0, s42
	v_lshl_add_u64 v[218:219], s[44:45], 0, v[130:131]
	global_load_lds_dwordx4 v[216:217], off
	v_lshl_add_u64 v[216:217], s[28:29], 0, v[128:129]
	s_add_i32 m0, s42, 0x2000
	s_nop 0
	global_load_lds_dwordx4 v[216:217], off
	v_lshl_add_u64 v[216:217], s[44:45], 0, v[132:133]
	s_mov_b32 m0, s21
	s_nop 0
	global_load_lds_dwordx4 v[216:217], off
	s_mov_b32 m0, s26
	s_nop 0
	global_load_lds_dwordx4 v[218:219], off
	s_waitcnt vmcnt(8)
	s_waitcnt lgkmcnt(0)
	s_barrier
	s_setprio 1
	s_waitcnt lgkmcnt(0)
	v_mfma_f32_16x16x32_bf16 v[60:63], v[138:141], v[174:177], v[60:63]
	v_mfma_f32_16x16x32_bf16 v[56:59], v[150:153], v[174:177], v[56:59]
	v_mfma_f32_16x16x32_bf16 v[40:43], v[150:153], v[194:197], v[40:43]
	v_mfma_f32_16x16x32_bf16 v[44:47], v[138:141], v[194:197], v[44:47]
	v_mfma_f32_16x16x32_bf16 v[28:31], v[138:141], v[202:205], v[28:31]
	v_mfma_f32_16x16x32_bf16 v[24:27], v[150:153], v[202:205], v[24:27]
	v_mfma_f32_16x16x32_bf16 v[8:11], v[150:153], v[224:227], v[8:11]
	v_mfma_f32_16x16x32_bf16 v[12:15], v[138:141], v[224:227], v[12:15]
	v_mfma_f32_16x16x32_bf16 v[60:63], v[142:145], v[178:181], v[60:63]
	v_mfma_f32_16x16x32_bf16 v[56:59], v[154:157], v[178:181], v[56:59]
	v_mfma_f32_16x16x32_bf16 v[40:43], v[154:157], v[198:201], v[40:43]
	v_mfma_f32_16x16x32_bf16 v[44:47], v[142:145], v[198:201], v[44:47]
	v_mfma_f32_16x16x32_bf16 v[28:31], v[142:145], v[206:209], v[28:31]
	v_mfma_f32_16x16x32_bf16 v[24:27], v[154:157], v[206:209], v[24:27]
	v_mfma_f32_16x16x32_bf16 v[8:11], v[154:157], v[228:231], v[8:11]
	v_mfma_f32_16x16x32_bf16 v[12:15], v[142:145], v[228:231], v[12:15]
	s_setprio 0
	s_setprio 1
	v_mfma_f32_16x16x32_bf16 v[52:55], v[158:161], v[174:177], v[52:55]
	v_mfma_f32_16x16x32_bf16 v[48:51], v[166:169], v[174:177], v[48:51]
	v_mfma_f32_16x16x32_bf16 v[32:35], v[166:169], v[194:197], v[32:35]
	v_mfma_f32_16x16x32_bf16 v[36:39], v[158:161], v[194:197], v[36:39]
	v_mfma_f32_16x16x32_bf16 v[20:23], v[158:161], v[202:205], v[20:23]
	v_mfma_f32_16x16x32_bf16 v[16:19], v[166:169], v[202:205], v[16:19]
	v_mfma_f32_16x16x32_bf16 v[0:3], v[166:169], v[224:227], v[0:3]
	v_mfma_f32_16x16x32_bf16 v[4:7], v[158:161], v[224:227], v[4:7]
	v_mfma_f32_16x16x32_bf16 v[52:55], v[162:165], v[178:181], v[52:55]
	v_mfma_f32_16x16x32_bf16 v[48:51], v[170:173], v[178:181], v[48:51]
	v_mfma_f32_16x16x32_bf16 v[32:35], v[170:173], v[198:201], v[32:35]
	v_mfma_f32_16x16x32_bf16 v[36:39], v[162:165], v[198:201], v[36:39]
	v_mfma_f32_16x16x32_bf16 v[20:23], v[162:165], v[206:209], v[20:23]
	v_mfma_f32_16x16x32_bf16 v[16:19], v[170:173], v[206:209], v[16:19]
	v_mfma_f32_16x16x32_bf16 v[0:3], v[170:173], v[228:231], v[0:3]
	v_mfma_f32_16x16x32_bf16 v[4:7], v[162:165], v[228:231], v[4:7]
	s_setprio 0
	s_barrier
	s_add_i32 s42, 0, 0x18000
	s_add_i32 s43, 0, 0x1c000
	v_add_u32_e32 v154, s42, v147
	v_add_u32_e32 v170, s43, v147
	ds_read_b128 v[138:141], v154
	ds_read_b128 v[142:145], v154 offset:1024
	ds_read_b128 v[150:153], v154 offset:2048
	ds_read_b128 v[154:157], v154 offset:3072
	ds_read_b128 v[158:161], v170
	ds_read_b128 v[162:165], v170 offset:1024
	ds_read_b128 v[166:169], v170 offset:2048
	ds_read_b128 v[170:173], v170 offset:3072
	s_add_u32 s28, s44, 0x40000
	s_addc_u32 s29, s45, 0
	s_mov_b32 m0, s27
	v_lshl_add_u64 v[232:233], s[28:29], 0, v[132:133]
	ds_read_b128 v[174:177], v149 offset:32768
	ds_read_b128 v[178:181], v149 offset:33792
	ds_read_b128 v[194:197], v149 offset:34816
	ds_read_b128 v[198:201], v149 offset:35840
	ds_read_b128 v[202:205], v149 offset:36864
	ds_read_b128 v[206:209], v149 offset:37888
	ds_read_b128 v[224:227], v149 offset:38912
	ds_read_b128 v[228:231], v149 offset:39936
	global_load_lds_dwordx4 v[232:233], off
	v_lshl_add_u64 v[232:233], s[28:29], 0, v[130:131]
	s_mov_b32 m0, s46
	s_nop 0
	global_load_lds_dwordx4 v[232:233], off
	s_waitcnt vmcnt(8)
	s_waitcnt lgkmcnt(0)
	s_barrier
	s_setprio 1
	s_waitcnt lgkmcnt(0)
	v_mfma_f32_16x16x32_bf16 v[124:127], v[138:141], v[174:177], v[124:127]
	v_mfma_f32_16x16x32_bf16 v[120:123], v[150:153], v[174:177], v[120:123]
	v_mfma_f32_16x16x32_bf16 v[104:107], v[150:153], v[194:197], v[104:107]
	v_mfma_f32_16x16x32_bf16 v[108:111], v[138:141], v[194:197], v[108:111]
	v_mfma_f32_16x16x32_bf16 v[92:95], v[138:141], v[202:205], v[92:95]
	v_mfma_f32_16x16x32_bf16 v[88:91], v[150:153], v[202:205], v[88:91]
	v_mfma_f32_16x16x32_bf16 v[72:75], v[150:153], v[224:227], v[72:75]
	v_mfma_f32_16x16x32_bf16 v[76:79], v[138:141], v[224:227], v[76:79]
	v_mfma_f32_16x16x32_bf16 v[124:127], v[142:145], v[178:181], v[124:127]
	v_mfma_f32_16x16x32_bf16 v[120:123], v[154:157], v[178:181], v[120:123]
	v_mfma_f32_16x16x32_bf16 v[104:107], v[154:157], v[198:201], v[104:107]
	v_mfma_f32_16x16x32_bf16 v[108:111], v[142:145], v[198:201], v[108:111]
	v_mfma_f32_16x16x32_bf16 v[92:95], v[142:145], v[206:209], v[92:95]
	v_mfma_f32_16x16x32_bf16 v[88:91], v[154:157], v[206:209], v[88:91]
	v_mfma_f32_16x16x32_bf16 v[72:75], v[154:157], v[228:231], v[72:75]
	v_mfma_f32_16x16x32_bf16 v[76:79], v[142:145], v[228:231], v[76:79]
	s_setprio 0
	s_setprio 1
	v_mfma_f32_16x16x32_bf16 v[116:119], v[158:161], v[174:177], v[116:119]
	v_mfma_f32_16x16x32_bf16 v[112:115], v[166:169], v[174:177], v[112:115]
	v_mfma_f32_16x16x32_bf16 v[96:99], v[166:169], v[194:197], v[96:99]
	v_mfma_f32_16x16x32_bf16 v[100:103], v[158:161], v[194:197], v[100:103]
	v_mfma_f32_16x16x32_bf16 v[84:87], v[158:161], v[202:205], v[84:87]
	v_mfma_f32_16x16x32_bf16 v[80:83], v[166:169], v[202:205], v[80:83]
	v_mfma_f32_16x16x32_bf16 v[64:67], v[166:169], v[224:227], v[64:67]
	v_mfma_f32_16x16x32_bf16 v[68:71], v[158:161], v[224:227], v[68:71]
	v_mfma_f32_16x16x32_bf16 v[116:119], v[162:165], v[178:181], v[116:119]
	v_mfma_f32_16x16x32_bf16 v[112:115], v[170:173], v[178:181], v[112:115]
	v_mfma_f32_16x16x32_bf16 v[96:99], v[170:173], v[198:201], v[96:99]
	v_mfma_f32_16x16x32_bf16 v[100:103], v[162:165], v[198:201], v[100:103]
	v_mfma_f32_16x16x32_bf16 v[84:87], v[162:165], v[206:209], v[84:87]
	v_mfma_f32_16x16x32_bf16 v[80:83], v[170:173], v[206:209], v[80:83]
	v_mfma_f32_16x16x32_bf16 v[64:67], v[170:173], v[228:231], v[64:67]
	v_mfma_f32_16x16x32_bf16 v[68:71], v[162:165], v[228:231], v[68:71]
	s_setprio 0
	s_barrier
	s_add_i32 s28, s42, s20
	v_lshl_add_u64 v[182:183], v[182:183], 0, s[68:69]
	s_mov_b32 m0, s28
	ds_read_b128 v[174:177], v149 offset:49152
	ds_read_b128 v[178:181], v149 offset:50176
	ds_read_b128 v[194:197], v149 offset:51200
	ds_read_b128 v[198:201], v149 offset:52224
	ds_read_b128 v[202:205], v149 offset:53248
	ds_read_b128 v[206:209], v149 offset:54272
	ds_read_b128 v[224:227], v149 offset:55296
	ds_read_b128 v[228:231], v149 offset:56320
	global_load_lds_dwordx4 v[182:183], off
	s_add_i32 m0, s28, 0x2000
	s_add_u32 s28, s40, 0x40080
	v_lshl_add_u64 v[182:183], v[210:211], 0, s[68:69]
	s_addc_u32 s29, s41, 0
	s_add_i32 s40, s43, s20
	global_load_lds_dwordx4 v[182:183], off
	v_lshl_add_u64 v[182:183], s[28:29], 0, v[184:185]
	s_mov_b32 m0, s40
	s_nop 0
	global_load_lds_dwordx4 v[182:183], off
	v_lshl_add_u64 v[182:183], s[28:29], 0, v[128:129]
	s_add_i32 m0, s40, 0x2000
	s_nop 0
	global_load_lds_dwordx4 v[182:183], off
	v_lshl_add_u64 v[182:183], v[216:217], 0, s[68:69]
	s_mov_b32 m0, s47
	s_nop 0
	global_load_lds_dwordx4 v[182:183], off
	v_lshl_add_u64 v[182:183], v[218:219], 0, s[68:69]
	s_mov_b32 m0, s50
	s_nop 0
	global_load_lds_dwordx4 v[182:183], off
	s_waitcnt vmcnt(8)
	s_waitcnt lgkmcnt(0)
	s_barrier
	s_setprio 1
	s_waitcnt lgkmcnt(0)
	v_mfma_f32_16x16x32_bf16 v[60:63], v[138:141], v[174:177], v[60:63]
	v_mfma_f32_16x16x32_bf16 v[56:59], v[150:153], v[174:177], v[56:59]
	v_mfma_f32_16x16x32_bf16 v[40:43], v[150:153], v[194:197], v[40:43]
	v_mfma_f32_16x16x32_bf16 v[44:47], v[138:141], v[194:197], v[44:47]
	v_mfma_f32_16x16x32_bf16 v[28:31], v[138:141], v[202:205], v[28:31]
	v_mfma_f32_16x16x32_bf16 v[24:27], v[150:153], v[202:205], v[24:27]
	v_mfma_f32_16x16x32_bf16 v[8:11], v[150:153], v[224:227], v[8:11]
	v_mfma_f32_16x16x32_bf16 v[12:15], v[138:141], v[224:227], v[12:15]
	v_mfma_f32_16x16x32_bf16 v[60:63], v[142:145], v[178:181], v[60:63]
	v_mfma_f32_16x16x32_bf16 v[56:59], v[154:157], v[178:181], v[56:59]
	v_mfma_f32_16x16x32_bf16 v[40:43], v[154:157], v[198:201], v[40:43]
	v_mfma_f32_16x16x32_bf16 v[44:47], v[142:145], v[198:201], v[44:47]
	v_mfma_f32_16x16x32_bf16 v[28:31], v[142:145], v[206:209], v[28:31]
	v_mfma_f32_16x16x32_bf16 v[24:27], v[154:157], v[206:209], v[24:27]
	v_mfma_f32_16x16x32_bf16 v[8:11], v[154:157], v[228:231], v[8:11]
	v_mfma_f32_16x16x32_bf16 v[12:15], v[142:145], v[228:231], v[12:15]
	s_setprio 0
	s_setprio 1
	v_mfma_f32_16x16x32_bf16 v[52:55], v[158:161], v[174:177], v[52:55]
	v_mfma_f32_16x16x32_bf16 v[48:51], v[166:169], v[174:177], v[48:51]
	v_mfma_f32_16x16x32_bf16 v[32:35], v[166:169], v[194:197], v[32:35]
	v_mfma_f32_16x16x32_bf16 v[36:39], v[158:161], v[194:197], v[36:39]
	v_mfma_f32_16x16x32_bf16 v[20:23], v[158:161], v[202:205], v[20:23]
	v_mfma_f32_16x16x32_bf16 v[16:19], v[166:169], v[202:205], v[16:19]
	v_mfma_f32_16x16x32_bf16 v[0:3], v[166:169], v[224:227], v[0:3]
	v_mfma_f32_16x16x32_bf16 v[4:7], v[158:161], v[224:227], v[4:7]
	v_mfma_f32_16x16x32_bf16 v[52:55], v[162:165], v[178:181], v[52:55]
	v_mfma_f32_16x16x32_bf16 v[48:51], v[170:173], v[178:181], v[48:51]
	v_mfma_f32_16x16x32_bf16 v[32:35], v[170:173], v[198:201], v[32:35]
	v_mfma_f32_16x16x32_bf16 v[36:39], v[162:165], v[198:201], v[36:39]
	v_mfma_f32_16x16x32_bf16 v[20:23], v[162:165], v[206:209], v[20:23]
	v_mfma_f32_16x16x32_bf16 v[16:19], v[170:173], v[206:209], v[16:19]
	v_mfma_f32_16x16x32_bf16 v[0:3], v[170:173], v[228:231], v[0:3]
	v_mfma_f32_16x16x32_bf16 v[4:7], v[162:165], v[228:231], v[4:7]
	s_setprio 0
	s_barrier
	s_add_i32 s60, s60, 2
	s_add_u32 s30, s30, 0x100
	s_addc_u32 s31, s31, 0
	s_add_u32 s58, s58, 0x100
	s_addc_u32 s59, s59, 0
	s_cmp_gt_u32 s60, 13
	s_cbranch_scc0 .LBB0_842
	s_and_b64 vcc, exec, s[6:7]
	s_cbranch_vccz .LBB0_845
	s_barrier

.LBB0_859:
	s_add_u32 s42, s40, s50
	s_addc_u32 s43, s41, 0
	s_add_u32 s48, s42, 0x100
	s_addc_u32 s49, s43, 0
	s_and_b64 s[28:29], s[46:47], exec
	s_cselect_b32 s53, s11, s49
	s_cselect_b32 s52, s13, s48
	s_add_u32 s28, s6, s50
	s_addc_u32 s29, s7, 0
	s_add_u32 s48, s28, 0x100
	s_addc_u32 s49, s29, 0
	s_add_i32 s76, 0, 0x10000
	s_and_b64 s[28:29], s[46:47], exec
	s_cselect_b32 s59, s93, s49
	s_cselect_b32 s58, s94, s48
	s_add_i32 s29, 0, 0x14000
	s_add_u32 s62, s42, 0x40080
	s_addc_u32 s63, s43, 0
	s_add_i32 s85, s76, s20
	s_add_i32 m0, s21, 0xc000
	s_add_i32 s90, s21, 0xe000
	s_add_i32 s42, s85, 0x2000
	v_add_u32_e32 v153, s76, v150
	s_add_u32 s60, s58, 0x40000
	ds_read_b128 v[154:157], v153
	ds_read_b128 v[158:161], v153 offset:1024
	ds_read_b128 v[162:165], v153 offset:2048
	ds_read_b128 v[166:169], v153 offset:3072
	v_add_u32_e32 v153, s29, v150
	s_addc_u32 s61, s59, 0
	s_add_i32 s49, s29, s20
	ds_read_b128 v[170:173], v153
	ds_read_b128 v[174:177], v153 offset:1024
	ds_read_b128 v[178:181], v153 offset:2048
	ds_read_b128 v[194:197], v153 offset:3072
	s_add_i32 s43, s49, 0x2000
	s_add_i32 s48, 0, 0x18000
	s_add_i32 s28, 0, 0x1c000
	s_add_u32 s50, s52, 0x40000
	s_addc_u32 s51, s53, 0
	s_add_i32 vcc_lo, s48, s20
	s_add_i32 s95, vcc_lo, 0x2000
	s_add_u32 s46, s58, 0x40080
	s_addc_u32 s47, s59, 0
	s_add_i32 s76, s28, s20
	s_add_i32 s29, s76, 0x2000
	v_lshl_add_u64 v[182:183], s[62:63], 0, v[132:133]
	ds_read_b128 v[198:201], v152
	ds_read_b128 v[202:205], v152 offset:1024
	ds_read_b128 v[206:209], v152 offset:2048
	ds_read_b128 v[224:227], v152 offset:3072
	ds_read_b128 v[228:231], v152 offset:4096
	ds_read_b128 v[232:235], v152 offset:5120
	ds_read_b128 v[236:239], v152 offset:6144
	ds_read_b128 v[240:243], v152 offset:7168
	global_load_lds_dwordx4 v[182:183], off
	v_lshl_add_u64 v[182:183], s[62:63], 0, v[130:131]
	s_mov_b32 m0, s90
	s_nop 0
	global_load_lds_dwordx4 v[182:183], off
	s_waitcnt vmcnt(8)
	s_waitcnt lgkmcnt(0)
	s_barrier
	s_setprio 1
	s_waitcnt lgkmcnt(0)
	v_mfma_f32_16x16x32_bf16 v[124:127], v[154:157], v[198:201], v[124:127]
	v_mfma_f32_16x16x32_bf16 v[120:123], v[162:165], v[198:201], v[120:123]
	v_mfma_f32_16x16x32_bf16 v[112:115], v[162:165], v[206:209], v[112:115]
	v_mfma_f32_16x16x32_bf16 v[116:119], v[154:157], v[206:209], v[116:119]
	v_mfma_f32_16x16x32_bf16 v[108:111], v[154:157], v[228:231], v[108:111]
	v_mfma_f32_16x16x32_bf16 v[104:107], v[162:165], v[228:231], v[104:107]
	v_mfma_f32_16x16x32_bf16 v[88:91], v[162:165], v[236:239], v[88:91]
	v_mfma_f32_16x16x32_bf16 v[96:99], v[154:157], v[236:239], v[96:99]
	v_mfma_f32_16x16x32_bf16 v[124:127], v[158:161], v[202:205], v[124:127]
	v_mfma_f32_16x16x32_bf16 v[120:123], v[166:169], v[202:205], v[120:123]
	v_mfma_f32_16x16x32_bf16 v[112:115], v[166:169], v[224:227], v[112:115]
	v_mfma_f32_16x16x32_bf16 v[116:119], v[158:161], v[224:227], v[116:119]
	v_mfma_f32_16x16x32_bf16 v[108:111], v[158:161], v[232:235], v[108:111]
	v_mfma_f32_16x16x32_bf16 v[104:107], v[166:169], v[232:235], v[104:107]
	v_mfma_f32_16x16x32_bf16 v[88:91], v[166:169], v[240:243], v[88:91]
	v_mfma_f32_16x16x32_bf16 v[96:99], v[158:161], v[240:243], v[96:99]
	s_setprio 0
	s_setprio 1
	v_mfma_f32_16x16x32_bf16 v[100:103], v[170:173], v[198:201], v[100:103]
	v_mfma_f32_16x16x32_bf16 v[92:95], v[178:181], v[198:201], v[92:95]
	v_mfma_f32_16x16x32_bf16 v[80:83], v[178:181], v[206:209], v[80:83]
	v_mfma_f32_16x16x32_bf16 v[84:87], v[170:173], v[206:209], v[84:87]
	v_mfma_f32_16x16x32_bf16 v[76:79], v[170:173], v[228:231], v[76:79]
	v_mfma_f32_16x16x32_bf16 v[72:75], v[178:181], v[228:231], v[72:75]
	v_mfma_f32_16x16x32_bf16 v[64:67], v[178:181], v[236:239], v[64:67]
	v_mfma_f32_16x16x32_bf16 v[68:71], v[170:173], v[236:239], v[68:71]
	v_mfma_f32_16x16x32_bf16 v[100:103], v[174:177], v[202:205], v[100:103]
	v_mfma_f32_16x16x32_bf16 v[92:95], v[194:197], v[202:205], v[92:95]
	v_mfma_f32_16x16x32_bf16 v[80:83], v[194:197], v[224:227], v[80:83]
	v_mfma_f32_16x16x32_bf16 v[84:87], v[174:177], v[224:227], v[84:87]
	v_mfma_f32_16x16x32_bf16 v[76:79], v[174:177], v[232:235], v[76:79]
	v_mfma_f32_16x16x32_bf16 v[72:75], v[194:197], v[232:235], v[72:75]
	v_mfma_f32_16x16x32_bf16 v[64:67], v[194:197], v[240:243], v[64:67]
	v_mfma_f32_16x16x32_bf16 v[68:71], v[174:177], v[240:243], v[68:71]
	s_setprio 0
	s_barrier
	s_mov_b32 m0, s85
	v_lshl_add_u64 v[182:183], s[58:59], 0, v[184:185]
	ds_read_b128 v[198:201], v152 offset:16384
	ds_read_b128 v[202:205], v152 offset:17408
	ds_read_b128 v[206:209], v152 offset:18432
	ds_read_b128 v[224:227], v152 offset:19456
	ds_read_b128 v[228:231], v152 offset:20480
	ds_read_b128 v[232:235], v152 offset:21504
	ds_read_b128 v[236:239], v152 offset:22528
	ds_read_b128 v[240:243], v152 offset:23552
	global_load_lds_dwordx4 v[182:183], off
	v_lshl_add_u64 v[210:211], s[58:59], 0, v[128:129]
	s_mov_b32 m0, s42
	v_lshl_add_u64 v[216:217], s[60:61], 0, v[184:185]
	global_load_lds_dwordx4 v[210:211], off
	s_mov_b32 m0, s49
	v_lshl_add_u64 v[218:219], s[52:53], 0, v[130:131]
	global_load_lds_dwordx4 v[216:217], off
	v_lshl_add_u64 v[216:217], s[60:61], 0, v[128:129]
	s_mov_b32 m0, s43
	s_nop 0
	global_load_lds_dwordx4 v[216:217], off
	v_lshl_add_u64 v[216:217], s[52:53], 0, v[132:133]
	s_mov_b32 m0, s21
	s_nop 0
	global_load_lds_dwordx4 v[216:217], off
	s_mov_b32 m0, s26
	s_nop 0
	global_load_lds_dwordx4 v[218:219], off
	s_waitcnt vmcnt(8)
	s_waitcnt lgkmcnt(0)
	s_barrier
	s_setprio 1
	s_waitcnt lgkmcnt(0)
	v_mfma_f32_16x16x32_bf16 v[60:63], v[154:157], v[198:201], v[60:63]
	v_mfma_f32_16x16x32_bf16 v[56:59], v[162:165], v[198:201], v[56:59]
	v_mfma_f32_16x16x32_bf16 v[48:51], v[162:165], v[206:209], v[48:51]
	v_mfma_f32_16x16x32_bf16 v[52:55], v[154:157], v[206:209], v[52:55]
	v_mfma_f32_16x16x32_bf16 v[44:47], v[154:157], v[228:231], v[44:47]
	v_mfma_f32_16x16x32_bf16 v[40:43], v[162:165], v[228:231], v[40:43]
	v_mfma_f32_16x16x32_bf16 v[24:27], v[162:165], v[236:239], v[24:27]
	v_mfma_f32_16x16x32_bf16 v[32:35], v[154:157], v[236:239], v[32:35]
	v_mfma_f32_16x16x32_bf16 v[60:63], v[158:161], v[202:205], v[60:63]
	v_mfma_f32_16x16x32_bf16 v[56:59], v[166:169], v[202:205], v[56:59]
	v_mfma_f32_16x16x32_bf16 v[48:51], v[166:169], v[224:227], v[48:51]
	v_mfma_f32_16x16x32_bf16 v[52:55], v[158:161], v[224:227], v[52:55]
	v_mfma_f32_16x16x32_bf16 v[44:47], v[158:161], v[232:235], v[44:47]
	v_mfma_f32_16x16x32_bf16 v[40:43], v[166:169], v[232:235], v[40:43]
	v_mfma_f32_16x16x32_bf16 v[24:27], v[166:169], v[240:243], v[24:27]
	v_mfma_f32_16x16x32_bf16 v[32:35], v[158:161], v[240:243], v[32:35]
	s_setprio 0
	s_setprio 1
	v_mfma_f32_16x16x32_bf16 v[36:39], v[170:173], v[198:201], v[36:39]
	v_mfma_f32_16x16x32_bf16 v[28:31], v[178:181], v[198:201], v[28:31]
	v_mfma_f32_16x16x32_bf16 v[16:19], v[178:181], v[206:209], v[16:19]
	v_mfma_f32_16x16x32_bf16 v[20:23], v[170:173], v[206:209], v[20:23]
	v_mfma_f32_16x16x32_bf16 v[12:15], v[170:173], v[228:231], v[12:15]
	v_mfma_f32_16x16x32_bf16 v[8:11], v[178:181], v[228:231], v[8:11]
	v_mfma_f32_16x16x32_bf16 v[0:3], v[178:181], v[236:239], v[0:3]
	v_mfma_f32_16x16x32_bf16 v[4:7], v[170:173], v[236:239], v[4:7]
	v_mfma_f32_16x16x32_bf16 v[36:39], v[174:177], v[202:205], v[36:39]
	v_mfma_f32_16x16x32_bf16 v[28:31], v[194:197], v[202:205], v[28:31]
	v_mfma_f32_16x16x32_bf16 v[16:19], v[194:197], v[224:227], v[16:19]
	v_mfma_f32_16x16x32_bf16 v[20:23], v[174:177], v[224:227], v[20:23]
	v_mfma_f32_16x16x32_bf16 v[12:15], v[174:177], v[232:235], v[12:15]
	v_mfma_f32_16x16x32_bf16 v[8:11], v[194:197], v[232:235], v[8:11]
	v_mfma_f32_16x16x32_bf16 v[0:3], v[194:197], v[240:243], v[0:3]
	v_mfma_f32_16x16x32_bf16 v[4:7], v[174:177], v[240:243], v[4:7]
	s_setprio 0
	s_barrier
	v_add_u32_e32 v153, s48, v150
	ds_read_b128 v[154:157], v153
	ds_read_b128 v[158:161], v153 offset:1024
	ds_read_b128 v[162:165], v153 offset:2048
	ds_read_b128 v[166:169], v153 offset:3072
	v_add_u32_e32 v153, s28, v150
	ds_read_b128 v[170:173], v153
	ds_read_b128 v[174:177], v153 offset:1024
	ds_read_b128 v[178:181], v153 offset:2048
	ds_read_b128 v[194:197], v153 offset:3072
	s_mov_b32 m0, s27
	v_lshl_add_u64 v[244:245], s[50:51], 0, v[132:133]
	ds_read_b128 v[198:201], v152 offset:32768
	ds_read_b128 v[202:205], v152 offset:33792
	ds_read_b128 v[206:209], v152 offset:34816
	ds_read_b128 v[224:227], v152 offset:35840
	ds_read_b128 v[228:231], v152 offset:36864
	ds_read_b128 v[232:235], v152 offset:37888
	ds_read_b128 v[236:239], v152 offset:38912
	ds_read_b128 v[240:243], v152 offset:39936
	global_load_lds_dwordx4 v[244:245], off
	v_lshl_add_u64 v[244:245], s[50:51], 0, v[130:131]
	s_mov_b32 m0, s79
	s_nop 0
	global_load_lds_dwordx4 v[244:245], off
	s_waitcnt vmcnt(8)
	s_waitcnt lgkmcnt(0)
	s_barrier
	s_setprio 1
	s_waitcnt lgkmcnt(0)
	v_mfma_f32_16x16x32_bf16 v[124:127], v[154:157], v[198:201], v[124:127]
	v_mfma_f32_16x16x32_bf16 v[120:123], v[162:165], v[198:201], v[120:123]
	v_mfma_f32_16x16x32_bf16 v[112:115], v[162:165], v[206:209], v[112:115]
	v_mfma_f32_16x16x32_bf16 v[116:119], v[154:157], v[206:209], v[116:119]
	v_mfma_f32_16x16x32_bf16 v[108:111], v[154:157], v[228:231], v[108:111]
	v_mfma_f32_16x16x32_bf16 v[104:107], v[162:165], v[228:231], v[104:107]
	v_mfma_f32_16x16x32_bf16 v[88:91], v[162:165], v[236:239], v[88:91]
	v_mfma_f32_16x16x32_bf16 v[96:99], v[154:157], v[236:239], v[96:99]
	v_mfma_f32_16x16x32_bf16 v[124:127], v[158:161], v[202:205], v[124:127]
	v_mfma_f32_16x16x32_bf16 v[120:123], v[166:169], v[202:205], v[120:123]
	v_mfma_f32_16x16x32_bf16 v[112:115], v[166:169], v[224:227], v[112:115]
	v_mfma_f32_16x16x32_bf16 v[116:119], v[158:161], v[224:227], v[116:119]
	v_mfma_f32_16x16x32_bf16 v[108:111], v[158:161], v[232:235], v[108:111]
	v_mfma_f32_16x16x32_bf16 v[104:107], v[166:169], v[232:235], v[104:107]
	v_mfma_f32_16x16x32_bf16 v[88:91], v[166:169], v[240:243], v[88:91]
	v_mfma_f32_16x16x32_bf16 v[96:99], v[158:161], v[240:243], v[96:99]
	s_setprio 0
	s_setprio 1
	v_mfma_f32_16x16x32_bf16 v[100:103], v[170:173], v[198:201], v[100:103]
	v_mfma_f32_16x16x32_bf16 v[92:95], v[178:181], v[198:201], v[92:95]
	v_mfma_f32_16x16x32_bf16 v[80:83], v[178:181], v[206:209], v[80:83]
	v_mfma_f32_16x16x32_bf16 v[84:87], v[170:173], v[206:209], v[84:87]
	v_mfma_f32_16x16x32_bf16 v[76:79], v[170:173], v[228:231], v[76:79]
	v_mfma_f32_16x16x32_bf16 v[72:75], v[178:181], v[228:231], v[72:75]
	v_mfma_f32_16x16x32_bf16 v[64:67], v[178:181], v[236:239], v[64:67]
	v_mfma_f32_16x16x32_bf16 v[68:71], v[170:173], v[236:239], v[68:71]
	v_mfma_f32_16x16x32_bf16 v[100:103], v[174:177], v[202:205], v[100:103]
	v_mfma_f32_16x16x32_bf16 v[92:95], v[194:197], v[202:205], v[92:95]
	v_mfma_f32_16x16x32_bf16 v[80:83], v[194:197], v[224:227], v[80:83]
	v_mfma_f32_16x16x32_bf16 v[84:87], v[174:177], v[224:227], v[84:87]
	v_mfma_f32_16x16x32_bf16 v[76:79], v[174:177], v[232:235], v[76:79]
	v_mfma_f32_16x16x32_bf16 v[72:75], v[194:197], v[232:235], v[72:75]
	v_mfma_f32_16x16x32_bf16 v[64:67], v[194:197], v[240:243], v[64:67]
	v_mfma_f32_16x16x32_bf16 v[68:71], v[174:177], v[240:243], v[68:71]
	s_setprio 0
	s_barrier
	s_mov_b32 m0, vcc_lo
	v_lshl_add_u64 v[182:183], v[182:183], 0, s[68:69]
	ds_read_b128 v[198:201], v152 offset:49152
	ds_read_b128 v[202:205], v152 offset:50176
	ds_read_b128 v[206:209], v152 offset:51200
	ds_read_b128 v[224:227], v152 offset:52224
	ds_read_b128 v[228:231], v152 offset:53248
	ds_read_b128 v[232:235], v152 offset:54272
	ds_read_b128 v[236:239], v152 offset:55296
	ds_read_b128 v[240:243], v152 offset:56320
	global_load_lds_dwordx4 v[182:183], off
	v_lshl_add_u64 v[182:183], v[210:211], 0, s[68:69]
	s_mov_b32 m0, s95
	s_nop 0
	global_load_lds_dwordx4 v[182:183], off
	v_lshl_add_u64 v[182:183], s[46:47], 0, v[184:185]
	s_mov_b32 m0, s76
	s_nop 0
	global_load_lds_dwordx4 v[182:183], off
	v_lshl_add_u64 v[182:183], s[46:47], 0, v[128:129]
	s_mov_b32 m0, s29
	s_nop 0
	global_load_lds_dwordx4 v[182:183], off
	v_lshl_add_u64 v[182:183], v[216:217], 0, s[68:69]
	s_mov_b32 m0, s88
	s_nop 0
	global_load_lds_dwordx4 v[182:183], off
	v_lshl_add_u64 v[182:183], v[218:219], 0, s[68:69]
	s_mov_b32 m0, s89
	s_nop 0
	global_load_lds_dwordx4 v[182:183], off
	s_waitcnt vmcnt(8)
	s_waitcnt lgkmcnt(0)
	s_barrier
	s_setprio 1
	s_waitcnt lgkmcnt(0)
	v_mfma_f32_16x16x32_bf16 v[60:63], v[154:157], v[198:201], v[60:63]
	v_mfma_f32_16x16x32_bf16 v[56:59], v[162:165], v[198:201], v[56:59]
	v_mfma_f32_16x16x32_bf16 v[48:51], v[162:165], v[206:209], v[48:51]
	v_mfma_f32_16x16x32_bf16 v[52:55], v[154:157], v[206:209], v[52:55]
	v_mfma_f32_16x16x32_bf16 v[44:47], v[154:157], v[228:231], v[44:47]
	v_mfma_f32_16x16x32_bf16 v[40:43], v[162:165], v[228:231], v[40:43]
	v_mfma_f32_16x16x32_bf16 v[24:27], v[162:165], v[236:239], v[24:27]
	v_mfma_f32_16x16x32_bf16 v[32:35], v[154:157], v[236:239], v[32:35]
	v_mfma_f32_16x16x32_bf16 v[60:63], v[158:161], v[202:205], v[60:63]
	v_mfma_f32_16x16x32_bf16 v[56:59], v[166:169], v[202:205], v[56:59]
	v_mfma_f32_16x16x32_bf16 v[48:51], v[166:169], v[224:227], v[48:51]
	v_mfma_f32_16x16x32_bf16 v[52:55], v[158:161], v[224:227], v[52:55]
	v_mfma_f32_16x16x32_bf16 v[44:47], v[158:161], v[232:235], v[44:47]
	v_mfma_f32_16x16x32_bf16 v[40:43], v[166:169], v[232:235], v[40:43]
	v_mfma_f32_16x16x32_bf16 v[24:27], v[166:169], v[240:243], v[24:27]
	v_mfma_f32_16x16x32_bf16 v[32:35], v[158:161], v[240:243], v[32:35]
	s_setprio 0
	s_setprio 1
	v_mfma_f32_16x16x32_bf16 v[36:39], v[170:173], v[198:201], v[36:39]
	v_mfma_f32_16x16x32_bf16 v[28:31], v[178:181], v[198:201], v[28:31]
	v_mfma_f32_16x16x32_bf16 v[16:19], v[178:181], v[206:209], v[16:19]
	v_mfma_f32_16x16x32_bf16 v[20:23], v[170:173], v[206:209], v[20:23]
	v_mfma_f32_16x16x32_bf16 v[12:15], v[170:173], v[228:231], v[12:15]
	v_mfma_f32_16x16x32_bf16 v[8:11], v[178:181], v[228:231], v[8:11]
	v_mfma_f32_16x16x32_bf16 v[0:3], v[178:181], v[236:239], v[0:3]
	v_mfma_f32_16x16x32_bf16 v[4:7], v[170:173], v[236:239], v[4:7]
	v_mfma_f32_16x16x32_bf16 v[36:39], v[174:177], v[202:205], v[36:39]
	v_mfma_f32_16x16x32_bf16 v[28:31], v[194:197], v[202:205], v[28:31]
	v_mfma_f32_16x16x32_bf16 v[16:19], v[194:197], v[224:227], v[16:19]
	v_mfma_f32_16x16x32_bf16 v[20:23], v[174:177], v[224:227], v[20:23]
	v_mfma_f32_16x16x32_bf16 v[12:15], v[174:177], v[232:235], v[12:15]
	v_mfma_f32_16x16x32_bf16 v[8:11], v[194:197], v[232:235], v[8:11]
	v_mfma_f32_16x16x32_bf16 v[0:3], v[194:197], v[240:243], v[0:3]
	v_mfma_f32_16x16x32_bf16 v[4:7], v[174:177], v[240:243], v[4:7]
	s_setprio 0
	s_barrier
	s_movk_i32 s50, 0x100
	s_andn2_b64 vcc, exec, s[44:45]
	s_mov_b64 s[46:47], -1
	s_mov_b64 s[44:45], 0
	s_cbranch_vccz .LBB0_859
	s_and_b64 vcc, exec, s[8:9]
	s_cbranch_vccz .LBB0_862
	s_barrier

.LBB0_991:
	s_add_u32 s28, s40, 0xfff80080
	s_addc_u32 s29, s41, -1
	s_add_i32 s48, 0, 0x10000
	s_cmp_eq_u32 s79, 28
	s_cselect_b32 s45, s11, s29
	s_cselect_b32 s44, s13, s28
	s_cselect_b32 s43, s60, s63
	s_cselect_b32 s42, s61, s62
	s_add_i32 s49, 0, 0x14000
	s_waitcnt vmcnt(0)
	v_add_u32_e32 v60, s48, v169
	v_add_u32_e32 v166, s49, v169
	ds_read_b128 v[40:43], v60
	ds_read_b128 v[44:47], v60 offset:1024
	ds_read_b128 v[56:59], v60 offset:2048
	ds_read_b128 v[60:63], v60 offset:3072
	ds_read_b128 v[144:147], v166
	ds_read_b128 v[148:151], v166 offset:1024
	ds_read_b128 v[162:165], v166 offset:2048
	ds_read_b128 v[172:175], v166 offset:3072
	v_lshl_add_u64 v[166:167], s[40:41], 0, v[158:159]
	s_add_i32 m0, s26, 0xc000
	ds_read_b128 v[176:179], v171
	ds_read_b128 v[180:183], v171 offset:1024
	ds_read_b128 v[194:197], v171 offset:2048
	ds_read_b128 v[198:201], v171 offset:3072
	ds_read_b128 v[202:205], v171 offset:4096
	ds_read_b128 v[206:209], v171 offset:5120
	ds_read_b128 v[224:227], v171 offset:6144
	ds_read_b128 v[228:231], v171 offset:7168
	global_load_lds_dwordx4 v[166:167], off
	v_lshl_add_u64 v[166:167], s[40:41], 0, v[160:161]
	s_add_i32 m0, s26, 0xe000
	s_nop 0
	global_load_lds_dwordx4 v[166:167], off
	s_waitcnt vmcnt(8)
	s_waitcnt lgkmcnt(0)
	s_barrier
	s_setprio 1
	s_waitcnt lgkmcnt(0)
	v_mfma_f32_16x16x32_bf16 v[140:143], v[40:43], v[176:179], v[140:143]
	v_mfma_f32_16x16x32_bf16 v[136:139], v[56:59], v[176:179], v[136:139]
	v_mfma_f32_16x16x32_bf16 v[120:123], v[56:59], v[194:197], v[120:123]
	v_mfma_f32_16x16x32_bf16 v[124:127], v[40:43], v[194:197], v[124:127]
	v_mfma_f32_16x16x32_bf16 v[108:111], v[40:43], v[202:205], v[108:111]
	v_mfma_f32_16x16x32_bf16 v[104:107], v[56:59], v[202:205], v[104:107]
	v_mfma_f32_16x16x32_bf16 v[88:91], v[56:59], v[224:227], v[88:91]
	v_mfma_f32_16x16x32_bf16 v[92:95], v[40:43], v[224:227], v[92:95]
	v_mfma_f32_16x16x32_bf16 v[140:143], v[44:47], v[180:183], v[140:143]
	v_mfma_f32_16x16x32_bf16 v[136:139], v[60:63], v[180:183], v[136:139]
	v_mfma_f32_16x16x32_bf16 v[120:123], v[60:63], v[198:201], v[120:123]
	v_mfma_f32_16x16x32_bf16 v[124:127], v[44:47], v[198:201], v[124:127]
	v_mfma_f32_16x16x32_bf16 v[108:111], v[44:47], v[206:209], v[108:111]
	v_mfma_f32_16x16x32_bf16 v[104:107], v[60:63], v[206:209], v[104:107]
	v_mfma_f32_16x16x32_bf16 v[88:91], v[60:63], v[228:231], v[88:91]
	v_mfma_f32_16x16x32_bf16 v[92:95], v[44:47], v[228:231], v[92:95]
	s_setprio 0
	s_setprio 1
	v_mfma_f32_16x16x32_bf16 v[132:135], v[144:147], v[176:179], v[132:135]
	v_mfma_f32_16x16x32_bf16 v[128:131], v[162:165], v[176:179], v[128:131]
	v_mfma_f32_16x16x32_bf16 v[112:115], v[162:165], v[194:197], v[112:115]
	v_mfma_f32_16x16x32_bf16 v[116:119], v[144:147], v[194:197], v[116:119]
	v_mfma_f32_16x16x32_bf16 v[100:103], v[144:147], v[202:205], v[100:103]
	v_mfma_f32_16x16x32_bf16 v[96:99], v[162:165], v[202:205], v[96:99]
	v_mfma_f32_16x16x32_bf16 v[80:83], v[162:165], v[224:227], v[80:83]
	v_mfma_f32_16x16x32_bf16 v[84:87], v[144:147], v[224:227], v[84:87]
	v_mfma_f32_16x16x32_bf16 v[132:135], v[148:151], v[180:183], v[132:135]
	v_mfma_f32_16x16x32_bf16 v[128:131], v[172:175], v[180:183], v[128:131]
	v_mfma_f32_16x16x32_bf16 v[112:115], v[172:175], v[198:201], v[112:115]
	v_mfma_f32_16x16x32_bf16 v[116:119], v[148:151], v[198:201], v[116:119]
	v_mfma_f32_16x16x32_bf16 v[100:103], v[148:151], v[206:209], v[100:103]
	v_mfma_f32_16x16x32_bf16 v[96:99], v[172:175], v[206:209], v[96:99]
	v_mfma_f32_16x16x32_bf16 v[80:83], v[172:175], v[228:231], v[80:83]
	v_mfma_f32_16x16x32_bf16 v[84:87], v[148:151], v[228:231], v[84:87]
	s_setprio 0
	s_barrier
	s_add_i32 s28, s48, s46
	v_lshl_add_u64 v[166:167], s[42:43], 0, v[184:185]
	s_mov_b32 m0, s28
	ds_read_b128 v[176:179], v171 offset:16384
	ds_read_b128 v[180:183], v171 offset:17408
	ds_read_b128 v[194:197], v171 offset:18432
	ds_read_b128 v[198:201], v171 offset:19456
	ds_read_b128 v[202:205], v171 offset:20480
	ds_read_b128 v[206:209], v171 offset:21504
	ds_read_b128 v[224:227], v171 offset:22528
	ds_read_b128 v[228:231], v171 offset:23552
	global_load_lds_dwordx4 v[166:167], off
	s_add_i32 m0, s28, 0x2000
	s_add_u32 s28, s42, 0x80000
	v_lshl_add_u64 v[210:211], s[42:43], 0, v[152:153]
	s_addc_u32 s29, s43, 0
	s_add_i32 s48, s49, s46
	global_load_lds_dwordx4 v[210:211], off
	v_lshl_add_u64 v[216:217], s[28:29], 0, v[184:185]
	s_mov_b32 m0, s48
	v_lshl_add_u64 v[218:219], s[44:45], 0, v[154:155]
	global_load_lds_dwordx4 v[216:217], off
	v_lshl_add_u64 v[216:217], s[28:29], 0, v[152:153]
	s_add_i32 m0, s48, 0x2000
	s_nop 0
	global_load_lds_dwordx4 v[216:217], off
	v_lshl_add_u64 v[216:217], s[44:45], 0, v[156:157]
	s_mov_b32 m0, s26
	s_nop 0
	global_load_lds_dwordx4 v[216:217], off
	s_mov_b32 m0, s27
	s_nop 0
	global_load_lds_dwordx4 v[218:219], off
	s_waitcnt vmcnt(8)
	s_waitcnt lgkmcnt(0)
	s_barrier
	s_setprio 1
	s_waitcnt lgkmcnt(0)
	v_mfma_f32_16x16x32_bf16 v[76:79], v[40:43], v[176:179], v[76:79]
	v_mfma_f32_16x16x32_bf16 v[72:75], v[56:59], v[176:179], v[72:75]
	v_mfma_f32_16x16x32_bf16 v[48:51], v[56:59], v[194:197], v[48:51]
	v_mfma_f32_16x16x32_bf16 v[52:55], v[40:43], v[194:197], v[52:55]
	v_mfma_f32_16x16x32_bf16 v[28:31], v[40:43], v[202:205], v[28:31]
	v_mfma_f32_16x16x32_bf16 v[24:27], v[56:59], v[202:205], v[24:27]
	v_mfma_f32_16x16x32_bf16 v[8:11], v[56:59], v[224:227], v[8:11]
	v_mfma_f32_16x16x32_bf16 v[12:15], v[40:43], v[224:227], v[12:15]
	v_mfma_f32_16x16x32_bf16 v[76:79], v[44:47], v[180:183], v[76:79]
	v_mfma_f32_16x16x32_bf16 v[72:75], v[60:63], v[180:183], v[72:75]
	v_mfma_f32_16x16x32_bf16 v[48:51], v[60:63], v[198:201], v[48:51]
	v_mfma_f32_16x16x32_bf16 v[52:55], v[44:47], v[198:201], v[52:55]
	v_mfma_f32_16x16x32_bf16 v[28:31], v[44:47], v[206:209], v[28:31]
	v_mfma_f32_16x16x32_bf16 v[24:27], v[60:63], v[206:209], v[24:27]
	v_mfma_f32_16x16x32_bf16 v[8:11], v[60:63], v[228:231], v[8:11]
	v_mfma_f32_16x16x32_bf16 v[12:15], v[44:47], v[228:231], v[12:15]
	s_setprio 0
	s_setprio 1
	v_mfma_f32_16x16x32_bf16 v[36:39], v[144:147], v[194:197], v[36:39]
	v_mfma_f32_16x16x32_bf16 v[32:35], v[162:165], v[194:197], v[32:35]
	v_mfma_f32_16x16x32_bf16 v[16:19], v[162:165], v[202:205], v[16:19]
	v_mfma_f32_16x16x32_bf16 v[20:23], v[144:147], v[202:205], v[20:23]
	v_mfma_f32_16x16x32_bf16 v[4:7], v[144:147], v[224:227], v[4:7]
	v_mfma_f32_16x16x32_bf16 v[0:3], v[162:165], v[224:227], v[0:3]
	v_mfma_f32_16x16x32_bf16 v[44:47], v[162:165], v[176:179], v[64:67]
	v_mfma_f32_16x16x32_bf16 v[40:43], v[144:147], v[176:179], v[68:71]
	v_mfma_f32_16x16x32_bf16 v[36:39], v[148:151], v[198:201], v[36:39]
	v_mfma_f32_16x16x32_bf16 v[32:35], v[172:175], v[198:201], v[32:35]
	v_mfma_f32_16x16x32_bf16 v[16:19], v[172:175], v[206:209], v[16:19]
	v_mfma_f32_16x16x32_bf16 v[20:23], v[148:151], v[206:209], v[20:23]
	v_mfma_f32_16x16x32_bf16 v[4:7], v[148:151], v[228:231], v[4:7]
	v_mfma_f32_16x16x32_bf16 v[0:3], v[172:175], v[228:231], v[0:3]
	v_mfma_f32_16x16x32_bf16 v[44:47], v[172:175], v[180:183], v[44:47]
	v_mfma_f32_16x16x32_bf16 v[40:43], v[148:151], v[180:183], v[40:43]
	s_setprio 0
	s_barrier
	s_add_i32 s48, 0, 0x18000
	s_add_i32 s49, 0, 0x1c000
	v_add_u32_e32 v68, s48, v169
	v_add_u32_e32 v172, s49, v169
	ds_read_b128 v[56:59], v68
	ds_read_b128 v[60:63], v68 offset:1024
	ds_read_b128 v[64:67], v68 offset:2048
	ds_read_b128 v[68:71], v68 offset:3072
	ds_read_b128 v[144:147], v172
	ds_read_b128 v[148:151], v172 offset:1024
	ds_read_b128 v[162:165], v172 offset:2048
	ds_read_b128 v[172:175], v172 offset:3072
	s_add_u32 s28, s44, 0x80000
	s_addc_u32 s29, s45, 0
	s_mov_b32 m0, s47
	v_lshl_add_u64 v[232:233], s[28:29], 0, v[156:157]
	ds_read_b128 v[176:179], v171 offset:32768
	ds_read_b128 v[180:183], v171 offset:33792
	ds_read_b128 v[194:197], v171 offset:34816
	ds_read_b128 v[198:201], v171 offset:35840
	ds_read_b128 v[202:205], v171 offset:36864
	ds_read_b128 v[206:209], v171 offset:37888
	ds_read_b128 v[224:227], v171 offset:38912
	ds_read_b128 v[228:231], v171 offset:39936
	global_load_lds_dwordx4 v[232:233], off
	v_lshl_add_u64 v[232:233], s[28:29], 0, v[154:155]
	s_mov_b32 m0, s50
	s_nop 0
	global_load_lds_dwordx4 v[232:233], off
	s_waitcnt vmcnt(8)
	s_waitcnt lgkmcnt(0)
	s_barrier
	s_setprio 1
	s_waitcnt lgkmcnt(0)
	v_mfma_f32_16x16x32_bf16 v[140:143], v[56:59], v[176:179], v[140:143]
	v_mfma_f32_16x16x32_bf16 v[136:139], v[64:67], v[176:179], v[136:139]
	v_mfma_f32_16x16x32_bf16 v[120:123], v[64:67], v[194:197], v[120:123]
	v_mfma_f32_16x16x32_bf16 v[124:127], v[56:59], v[194:197], v[124:127]
	v_mfma_f32_16x16x32_bf16 v[108:111], v[56:59], v[202:205], v[108:111]
	v_mfma_f32_16x16x32_bf16 v[104:107], v[64:67], v[202:205], v[104:107]
	v_mfma_f32_16x16x32_bf16 v[88:91], v[64:67], v[224:227], v[88:91]
	v_mfma_f32_16x16x32_bf16 v[92:95], v[56:59], v[224:227], v[92:95]
	v_mfma_f32_16x16x32_bf16 v[140:143], v[60:63], v[180:183], v[140:143]
	v_mfma_f32_16x16x32_bf16 v[136:139], v[68:71], v[180:183], v[136:139]
	v_mfma_f32_16x16x32_bf16 v[120:123], v[68:71], v[198:201], v[120:123]
	v_mfma_f32_16x16x32_bf16 v[124:127], v[60:63], v[198:201], v[124:127]
	v_mfma_f32_16x16x32_bf16 v[108:111], v[60:63], v[206:209], v[108:111]
	v_mfma_f32_16x16x32_bf16 v[104:107], v[68:71], v[206:209], v[104:107]
	v_mfma_f32_16x16x32_bf16 v[88:91], v[68:71], v[228:231], v[88:91]
	v_mfma_f32_16x16x32_bf16 v[92:95], v[60:63], v[228:231], v[92:95]
	s_setprio 0
	s_setprio 1
	v_mfma_f32_16x16x32_bf16 v[132:135], v[144:147], v[176:179], v[132:135]
	v_mfma_f32_16x16x32_bf16 v[128:131], v[162:165], v[176:179], v[128:131]
	v_mfma_f32_16x16x32_bf16 v[112:115], v[162:165], v[194:197], v[112:115]
	v_mfma_f32_16x16x32_bf16 v[116:119], v[144:147], v[194:197], v[116:119]
	v_mfma_f32_16x16x32_bf16 v[100:103], v[144:147], v[202:205], v[100:103]
	v_mfma_f32_16x16x32_bf16 v[96:99], v[162:165], v[202:205], v[96:99]
	v_mfma_f32_16x16x32_bf16 v[80:83], v[162:165], v[224:227], v[80:83]
	v_mfma_f32_16x16x32_bf16 v[84:87], v[144:147], v[224:227], v[84:87]
	v_mfma_f32_16x16x32_bf16 v[132:135], v[148:151], v[180:183], v[132:135]
	v_mfma_f32_16x16x32_bf16 v[128:131], v[172:175], v[180:183], v[128:131]
	v_mfma_f32_16x16x32_bf16 v[112:115], v[172:175], v[198:201], v[112:115]
	v_mfma_f32_16x16x32_bf16 v[116:119], v[148:151], v[198:201], v[116:119]
	v_mfma_f32_16x16x32_bf16 v[100:103], v[148:151], v[206:209], v[100:103]
	v_mfma_f32_16x16x32_bf16 v[96:99], v[172:175], v[206:209], v[96:99]
	v_mfma_f32_16x16x32_bf16 v[80:83], v[172:175], v[228:231], v[80:83]
	v_mfma_f32_16x16x32_bf16 v[84:87], v[148:151], v[228:231], v[84:87]
	s_setprio 0
	s_barrier
	s_add_i32 s28, s48, s46
	v_lshl_add_u64 v[166:167], v[166:167], 0, s[68:69]
	s_mov_b32 m0, s28
	ds_read_b128 v[176:179], v171 offset:49152
	ds_read_b128 v[180:183], v171 offset:50176
	ds_read_b128 v[194:197], v171 offset:51200
	ds_read_b128 v[198:201], v171 offset:52224
	ds_read_b128 v[202:205], v171 offset:53248
	ds_read_b128 v[206:209], v171 offset:54272
	ds_read_b128 v[224:227], v171 offset:55296
	ds_read_b128 v[228:231], v171 offset:56320
	global_load_lds_dwordx4 v[166:167], off
	s_add_i32 m0, s28, 0x2000
	s_add_u32 s28, s42, 0x80080
	v_lshl_add_u64 v[166:167], v[210:211], 0, s[68:69]
	s_addc_u32 s29, s43, 0
	s_add_i32 s42, s49, s46
	global_load_lds_dwordx4 v[166:167], off
	v_lshl_add_u64 v[166:167], s[28:29], 0, v[184:185]
	s_mov_b32 m0, s42
	s_nop 0
	global_load_lds_dwordx4 v[166:167], off
	v_lshl_add_u64 v[166:167], s[28:29], 0, v[152:153]
	s_add_i32 m0, s42, 0x2000
	s_nop 0
	global_load_lds_dwordx4 v[166:167], off
	v_lshl_add_u64 v[166:167], v[216:217], 0, s[68:69]
	s_mov_b32 m0, s53
	s_nop 0
	global_load_lds_dwordx4 v[166:167], off
	v_lshl_add_u64 v[166:167], v[218:219], 0, s[68:69]
	s_mov_b32 m0, s58
	s_nop 0
	global_load_lds_dwordx4 v[166:167], off
	s_waitcnt vmcnt(8)
	s_waitcnt lgkmcnt(0)
	s_barrier
	s_setprio 1
	s_waitcnt lgkmcnt(0)
	v_mfma_f32_16x16x32_bf16 v[76:79], v[56:59], v[176:179], v[76:79]
	v_mfma_f32_16x16x32_bf16 v[72:75], v[64:67], v[176:179], v[72:75]
	v_mfma_f32_16x16x32_bf16 v[48:51], v[64:67], v[194:197], v[48:51]
	v_mfma_f32_16x16x32_bf16 v[52:55], v[56:59], v[194:197], v[52:55]
	v_mfma_f32_16x16x32_bf16 v[28:31], v[56:59], v[202:205], v[28:31]
	v_mfma_f32_16x16x32_bf16 v[24:27], v[64:67], v[202:205], v[24:27]
	v_mfma_f32_16x16x32_bf16 v[8:11], v[64:67], v[224:227], v[8:11]
	v_mfma_f32_16x16x32_bf16 v[12:15], v[56:59], v[224:227], v[12:15]
	v_mfma_f32_16x16x32_bf16 v[76:79], v[60:63], v[180:183], v[76:79]
	v_mfma_f32_16x16x32_bf16 v[72:75], v[68:71], v[180:183], v[72:75]
	v_mfma_f32_16x16x32_bf16 v[48:51], v[68:71], v[198:201], v[48:51]
	v_mfma_f32_16x16x32_bf16 v[52:55], v[60:63], v[198:201], v[52:55]
	v_mfma_f32_16x16x32_bf16 v[28:31], v[60:63], v[206:209], v[28:31]
	v_mfma_f32_16x16x32_bf16 v[24:27], v[68:71], v[206:209], v[24:27]
	v_mfma_f32_16x16x32_bf16 v[8:11], v[68:71], v[228:231], v[8:11]
	v_mfma_f32_16x16x32_bf16 v[12:15], v[60:63], v[228:231], v[12:15]
	s_setprio 0
	s_setprio 1
	v_mfma_f32_16x16x32_bf16 v[40:43], v[144:147], v[176:179], v[40:43]
	v_mfma_f32_16x16x32_bf16 v[68:71], v[148:151], v[180:183], v[40:43]
	v_mfma_f32_16x16x32_bf16 v[40:43], v[162:165], v[176:179], v[44:47]
	v_mfma_f32_16x16x32_bf16 v[36:39], v[144:147], v[194:197], v[36:39]
	v_mfma_f32_16x16x32_bf16 v[32:35], v[162:165], v[194:197], v[32:35]
	v_mfma_f32_16x16x32_bf16 v[20:23], v[144:147], v[202:205], v[20:23]
	v_mfma_f32_16x16x32_bf16 v[16:19], v[162:165], v[202:205], v[16:19]
	v_mfma_f32_16x16x32_bf16 v[4:7], v[144:147], v[224:227], v[4:7]
	v_mfma_f32_16x16x32_bf16 v[0:3], v[162:165], v[224:227], v[0:3]
	v_mfma_f32_16x16x32_bf16 v[64:67], v[172:175], v[180:183], v[40:43]
	v_mfma_f32_16x16x32_bf16 v[32:35], v[172:175], v[198:201], v[32:35]
	v_mfma_f32_16x16x32_bf16 v[36:39], v[148:151], v[198:201], v[36:39]
	v_mfma_f32_16x16x32_bf16 v[20:23], v[148:151], v[206:209], v[20:23]
	v_mfma_f32_16x16x32_bf16 v[16:19], v[172:175], v[206:209], v[16:19]
	v_mfma_f32_16x16x32_bf16 v[0:3], v[172:175], v[228:231], v[0:3]
	v_mfma_f32_16x16x32_bf16 v[4:7], v[148:151], v[228:231], v[4:7]
	s_setprio 0
	s_barrier
	s_add_i32 s79, s79, 2
	s_add_u32 s40, s40, 0x100
	s_addc_u32 s41, s41, 0
	s_add_u32 s62, s62, 0x100
	s_addc_u32 s63, s63, 0
	s_cmp_gt_u32 s79, 29
	s_cbranch_scc0 .LBB0_991
	s_and_b64 vcc, exec, s[8:9]
	s_cbranch_vccz .LBB0_994
	s_barrier

.LBB0_1136:
	s_add_u32 s48, s42, s50
	s_addc_u32 s49, s43, 0
	s_add_u32 s51, s48, 0x100
	s_addc_u32 s52, s49, 0
	s_and_b64 s[28:29], s[46:47], exec
	s_cselect_b32 s53, s11, s52
	s_cselect_b32 s52, s13, s51
	s_add_u32 s28, s38, s50
	s_addc_u32 s29, s39, 0
	s_add_u32 s50, s28, 0x100
	s_addc_u32 s51, s29, 0
	s_add_i32 s76, 0, 0x10000
	s_and_b64 s[28:29], s[46:47], exec
	s_cselect_b32 s59, s93, s51
	s_cselect_b32 s58, s94, s50
	s_add_i32 s47, 0, 0x14000
	s_add_u32 s62, s48, 0x80080
	s_addc_u32 s63, s49, 0
	s_add_i32 s49, s76, s20
	s_add_i32 m0, s21, 0xc000
	s_add_i32 s91, s21, 0xe000
	s_add_i32 s29, s49, 0x2000
	s_add_u32 s60, s58, 0x80000
	v_add_u32_e32 v132, s76, v168
	v_add_u32_e32 v166, s47, v168
	s_addc_u32 s61, s59, 0
	s_add_i32 vcc_hi, s47, s20
	ds_read_b128 v[112:115], v132
	ds_read_b128 v[116:119], v132 offset:1024
	ds_read_b128 v[124:127], v132 offset:2048
	ds_read_b128 v[132:135], v132 offset:3072
	ds_read_b128 v[172:175], v166
	ds_read_b128 v[176:179], v166 offset:1024
	ds_read_b128 v[180:183], v166 offset:2048
	ds_read_b128 v[194:197], v166 offset:3072
	s_add_i32 s85, vcc_hi, 0x2000
	s_add_i32 s48, 0, 0x18000
	s_add_i32 s28, 0, 0x1c000
	s_add_u32 s50, s52, 0x80000
	s_addc_u32 s51, s53, 0
	s_add_i32 vcc_lo, s48, s20
	s_add_i32 s95, vcc_lo, 0x2000
	s_add_u32 s46, s58, 0x80080
	s_addc_u32 s47, s59, 0
	s_add_i32 s76, s28, s20
	s_add_i32 s90, s76, 0x2000
	v_lshl_add_u64 v[166:167], s[62:63], 0, v[148:149]
	ds_read_b128 v[198:201], v170
	ds_read_b128 v[202:205], v170 offset:1024
	ds_read_b128 v[206:209], v170 offset:2048
	ds_read_b128 v[224:227], v170 offset:3072
	ds_read_b128 v[228:231], v170 offset:4096
	ds_read_b128 v[232:235], v170 offset:5120
	ds_read_b128 v[236:239], v170 offset:6144
	ds_read_b128 v[240:243], v170 offset:7168
	global_load_lds_dwordx4 v[166:167], off
	v_lshl_add_u64 v[166:167], s[62:63], 0, v[146:147]
	s_mov_b32 m0, s91
	s_nop 0
	global_load_lds_dwordx4 v[166:167], off
	s_waitcnt vmcnt(8)
	s_waitcnt lgkmcnt(0)
	s_barrier
	s_setprio 1
	s_waitcnt lgkmcnt(0)
	v_mfma_f32_16x16x32_bf16 v[140:143], v[112:115], v[198:201], v[140:143]
	v_mfma_f32_16x16x32_bf16 v[136:139], v[124:127], v[198:201], v[136:139]
	v_mfma_f32_16x16x32_bf16 v[104:107], v[124:127], v[206:209], v[104:107]
	v_mfma_f32_16x16x32_bf16 v[108:111], v[112:115], v[206:209], v[108:111]
	v_mfma_f32_16x16x32_bf16 v[92:95], v[112:115], v[228:231], v[92:95]
	v_mfma_f32_16x16x32_bf16 v[88:91], v[124:127], v[228:231], v[88:91]
	v_mfma_f32_16x16x32_bf16 v[72:75], v[124:127], v[236:239], v[72:75]
	v_mfma_f32_16x16x32_bf16 v[76:79], v[112:115], v[236:239], v[76:79]
	v_mfma_f32_16x16x32_bf16 v[140:143], v[116:119], v[202:205], v[140:143]
	v_mfma_f32_16x16x32_bf16 v[136:139], v[132:135], v[202:205], v[136:139]
	v_mfma_f32_16x16x32_bf16 v[104:107], v[132:135], v[224:227], v[104:107]
	v_mfma_f32_16x16x32_bf16 v[108:111], v[116:119], v[224:227], v[108:111]
	v_mfma_f32_16x16x32_bf16 v[92:95], v[116:119], v[232:235], v[92:95]
	v_mfma_f32_16x16x32_bf16 v[88:91], v[132:135], v[232:235], v[88:91]
	v_mfma_f32_16x16x32_bf16 v[72:75], v[132:135], v[240:243], v[72:75]
	v_mfma_f32_16x16x32_bf16 v[76:79], v[116:119], v[240:243], v[76:79]
	s_setprio 0
	s_setprio 1
	v_mfma_f32_16x16x32_bf16 v[128:131], v[172:175], v[198:201], v[128:131]
	v_mfma_f32_16x16x32_bf16 v[120:123], v[180:183], v[198:201], v[120:123]
	v_mfma_f32_16x16x32_bf16 v[96:99], v[180:183], v[206:209], v[96:99]
	v_mfma_f32_16x16x32_bf16 v[100:103], v[172:175], v[206:209], v[100:103]
	v_mfma_f32_16x16x32_bf16 v[84:87], v[172:175], v[228:231], v[84:87]
	v_mfma_f32_16x16x32_bf16 v[80:83], v[180:183], v[228:231], v[80:83]
	v_mfma_f32_16x16x32_bf16 v[64:67], v[180:183], v[236:239], v[64:67]
	v_mfma_f32_16x16x32_bf16 v[68:71], v[172:175], v[236:239], v[68:71]
	v_mfma_f32_16x16x32_bf16 v[128:131], v[176:179], v[202:205], v[128:131]
	v_mfma_f32_16x16x32_bf16 v[120:123], v[194:197], v[202:205], v[120:123]
	v_mfma_f32_16x16x32_bf16 v[96:99], v[194:197], v[224:227], v[96:99]
	v_mfma_f32_16x16x32_bf16 v[100:103], v[176:179], v[224:227], v[100:103]
	v_mfma_f32_16x16x32_bf16 v[84:87], v[176:179], v[232:235], v[84:87]
	v_mfma_f32_16x16x32_bf16 v[80:83], v[194:197], v[232:235], v[80:83]
	v_mfma_f32_16x16x32_bf16 v[64:67], v[194:197], v[240:243], v[64:67]
	v_mfma_f32_16x16x32_bf16 v[68:71], v[176:179], v[240:243], v[68:71]
	s_setprio 0
	s_barrier
	s_mov_b32 m0, s49
	v_lshl_add_u64 v[166:167], s[58:59], 0, v[184:185]
	ds_read_b128 v[198:201], v170 offset:16384
	ds_read_b128 v[202:205], v170 offset:17408
	ds_read_b128 v[206:209], v170 offset:18432
	ds_read_b128 v[224:227], v170 offset:19456
	ds_read_b128 v[228:231], v170 offset:20480
	ds_read_b128 v[232:235], v170 offset:21504
	ds_read_b128 v[236:239], v170 offset:22528
	ds_read_b128 v[240:243], v170 offset:23552
	global_load_lds_dwordx4 v[166:167], off
	v_lshl_add_u64 v[210:211], s[58:59], 0, v[144:145]
	s_mov_b32 m0, s29
	v_lshl_add_u64 v[216:217], s[60:61], 0, v[184:185]
	global_load_lds_dwordx4 v[210:211], off
	s_mov_b32 m0, vcc_hi
	v_lshl_add_u64 v[218:219], s[52:53], 0, v[146:147]
	global_load_lds_dwordx4 v[216:217], off
	v_lshl_add_u64 v[216:217], s[60:61], 0, v[144:145]
	s_mov_b32 m0, s85
	s_nop 0
	global_load_lds_dwordx4 v[216:217], off
	v_lshl_add_u64 v[216:217], s[52:53], 0, v[148:149]
	s_mov_b32 m0, s21
	s_nop 0
	global_load_lds_dwordx4 v[216:217], off
	s_mov_b32 m0, s26
	s_nop 0
	global_load_lds_dwordx4 v[218:219], off
	s_waitcnt vmcnt(8)
	s_waitcnt lgkmcnt(0)
	s_barrier
	s_setprio 1
	s_waitcnt lgkmcnt(0)
	v_mfma_f32_16x16x32_bf16 v[60:63], v[112:115], v[198:201], v[60:63]
	v_mfma_f32_16x16x32_bf16 v[56:59], v[124:127], v[198:201], v[56:59]
	v_mfma_f32_16x16x32_bf16 v[40:43], v[124:127], v[206:209], v[40:43]
	v_mfma_f32_16x16x32_bf16 v[44:47], v[112:115], v[206:209], v[44:47]
	v_mfma_f32_16x16x32_bf16 v[36:39], v[112:115], v[228:231], v[36:39]
	v_mfma_f32_16x16x32_bf16 v[28:31], v[124:127], v[228:231], v[28:31]
	v_mfma_f32_16x16x32_bf16 v[12:15], v[124:127], v[236:239], v[12:15]
	v_mfma_f32_16x16x32_bf16 v[20:23], v[112:115], v[236:239], v[20:23]
	v_mfma_f32_16x16x32_bf16 v[60:63], v[116:119], v[202:205], v[60:63]
	v_mfma_f32_16x16x32_bf16 v[56:59], v[132:135], v[202:205], v[56:59]
	v_mfma_f32_16x16x32_bf16 v[40:43], v[132:135], v[224:227], v[40:43]
	v_mfma_f32_16x16x32_bf16 v[44:47], v[116:119], v[224:227], v[44:47]
	v_mfma_f32_16x16x32_bf16 v[36:39], v[116:119], v[232:235], v[36:39]
	v_mfma_f32_16x16x32_bf16 v[28:31], v[132:135], v[232:235], v[28:31]
	v_mfma_f32_16x16x32_bf16 v[12:15], v[132:135], v[240:243], v[12:15]
	v_mfma_f32_16x16x32_bf16 v[20:23], v[116:119], v[240:243], v[20:23]
	s_setprio 0
	s_setprio 1
	v_mfma_f32_16x16x32_bf16 v[52:55], v[172:175], v[198:201], v[52:55]
	v_mfma_f32_16x16x32_bf16 v[48:51], v[180:183], v[198:201], v[48:51]
	v_mfma_f32_16x16x32_bf16 v[24:27], v[180:183], v[206:209], v[24:27]
	v_mfma_f32_16x16x32_bf16 v[32:35], v[172:175], v[206:209], v[32:35]
	v_mfma_f32_16x16x32_bf16 v[16:19], v[172:175], v[228:231], v[16:19]
	v_mfma_f32_16x16x32_bf16 v[8:11], v[180:183], v[228:231], v[8:11]
	v_mfma_f32_16x16x32_bf16 v[0:3], v[180:183], v[236:239], v[0:3]
	v_mfma_f32_16x16x32_bf16 v[4:7], v[172:175], v[236:239], v[4:7]
	v_mfma_f32_16x16x32_bf16 v[52:55], v[176:179], v[202:205], v[52:55]
	v_mfma_f32_16x16x32_bf16 v[48:51], v[194:197], v[202:205], v[48:51]
	v_mfma_f32_16x16x32_bf16 v[24:27], v[194:197], v[224:227], v[24:27]
	v_mfma_f32_16x16x32_bf16 v[32:35], v[176:179], v[224:227], v[32:35]
	v_mfma_f32_16x16x32_bf16 v[16:19], v[176:179], v[232:235], v[16:19]
	v_mfma_f32_16x16x32_bf16 v[8:11], v[194:197], v[232:235], v[8:11]
	v_mfma_f32_16x16x32_bf16 v[0:3], v[194:197], v[240:243], v[0:3]
	v_mfma_f32_16x16x32_bf16 v[4:7], v[176:179], v[240:243], v[4:7]
	s_setprio 0
	s_barrier
	v_add_u32_e32 v132, s48, v168
	v_add_u32_e32 v171, s28, v168
	ds_read_b128 v[112:115], v132
	ds_read_b128 v[116:119], v132 offset:1024
	ds_read_b128 v[124:127], v132 offset:2048
	ds_read_b128 v[132:135], v132 offset:3072
	ds_read_b128 v[172:175], v171
	ds_read_b128 v[176:179], v171 offset:1024
	ds_read_b128 v[180:183], v171 offset:2048
	ds_read_b128 v[194:197], v171 offset:3072
	s_mov_b32 m0, s27
	v_lshl_add_u64 v[244:245], s[50:51], 0, v[148:149]
	ds_read_b128 v[198:201], v170 offset:32768
	ds_read_b128 v[202:205], v170 offset:33792
	ds_read_b128 v[206:209], v170 offset:34816
	ds_read_b128 v[224:227], v170 offset:35840
	ds_read_b128 v[228:231], v170 offset:36864
	ds_read_b128 v[232:235], v170 offset:37888
	ds_read_b128 v[236:239], v170 offset:38912
	ds_read_b128 v[240:243], v170 offset:39936
	global_load_lds_dwordx4 v[244:245], off
	v_lshl_add_u64 v[244:245], s[50:51], 0, v[146:147]
	s_mov_b32 m0, s79
	s_nop 0
	global_load_lds_dwordx4 v[244:245], off
	s_waitcnt vmcnt(8)
	s_waitcnt lgkmcnt(0)
	s_barrier
	s_setprio 1
	s_waitcnt lgkmcnt(0)
	v_mfma_f32_16x16x32_bf16 v[140:143], v[112:115], v[198:201], v[140:143]
	v_mfma_f32_16x16x32_bf16 v[136:139], v[124:127], v[198:201], v[136:139]
	v_mfma_f32_16x16x32_bf16 v[104:107], v[124:127], v[206:209], v[104:107]
	v_mfma_f32_16x16x32_bf16 v[108:111], v[112:115], v[206:209], v[108:111]
	v_mfma_f32_16x16x32_bf16 v[92:95], v[112:115], v[228:231], v[92:95]
	v_mfma_f32_16x16x32_bf16 v[88:91], v[124:127], v[228:231], v[88:91]
	v_mfma_f32_16x16x32_bf16 v[72:75], v[124:127], v[236:239], v[72:75]
	v_mfma_f32_16x16x32_bf16 v[76:79], v[112:115], v[236:239], v[76:79]
	v_mfma_f32_16x16x32_bf16 v[140:143], v[116:119], v[202:205], v[140:143]
	v_mfma_f32_16x16x32_bf16 v[136:139], v[132:135], v[202:205], v[136:139]
	v_mfma_f32_16x16x32_bf16 v[104:107], v[132:135], v[224:227], v[104:107]
	v_mfma_f32_16x16x32_bf16 v[108:111], v[116:119], v[224:227], v[108:111]
	v_mfma_f32_16x16x32_bf16 v[92:95], v[116:119], v[232:235], v[92:95]
	v_mfma_f32_16x16x32_bf16 v[88:91], v[132:135], v[232:235], v[88:91]
	v_mfma_f32_16x16x32_bf16 v[72:75], v[132:135], v[240:243], v[72:75]
	v_mfma_f32_16x16x32_bf16 v[76:79], v[116:119], v[240:243], v[76:79]
	s_setprio 0
	s_setprio 1
	v_mfma_f32_16x16x32_bf16 v[128:131], v[172:175], v[198:201], v[128:131]
	v_mfma_f32_16x16x32_bf16 v[120:123], v[180:183], v[198:201], v[120:123]
	v_mfma_f32_16x16x32_bf16 v[96:99], v[180:183], v[206:209], v[96:99]
	v_mfma_f32_16x16x32_bf16 v[100:103], v[172:175], v[206:209], v[100:103]
	v_mfma_f32_16x16x32_bf16 v[84:87], v[172:175], v[228:231], v[84:87]
	v_mfma_f32_16x16x32_bf16 v[80:83], v[180:183], v[228:231], v[80:83]
	v_mfma_f32_16x16x32_bf16 v[64:67], v[180:183], v[236:239], v[64:67]
	v_mfma_f32_16x16x32_bf16 v[68:71], v[172:175], v[236:239], v[68:71]
	v_mfma_f32_16x16x32_bf16 v[128:131], v[176:179], v[202:205], v[128:131]
	v_mfma_f32_16x16x32_bf16 v[120:123], v[194:197], v[202:205], v[120:123]
	v_mfma_f32_16x16x32_bf16 v[96:99], v[194:197], v[224:227], v[96:99]
	v_mfma_f32_16x16x32_bf16 v[100:103], v[176:179], v[224:227], v[100:103]
	v_mfma_f32_16x16x32_bf16 v[84:87], v[176:179], v[232:235], v[84:87]
	v_mfma_f32_16x16x32_bf16 v[80:83], v[194:197], v[232:235], v[80:83]
	v_mfma_f32_16x16x32_bf16 v[64:67], v[194:197], v[240:243], v[64:67]
	v_mfma_f32_16x16x32_bf16 v[68:71], v[176:179], v[240:243], v[68:71]
	s_setprio 0
	s_barrier
	s_mov_b32 m0, vcc_lo
	v_lshl_add_u64 v[166:167], v[166:167], 0, s[68:69]
	ds_read_b128 v[198:201], v170 offset:49152
	ds_read_b128 v[202:205], v170 offset:50176
	ds_read_b128 v[206:209], v170 offset:51200
	ds_read_b128 v[224:227], v170 offset:52224
	ds_read_b128 v[228:231], v170 offset:53248
	ds_read_b128 v[232:235], v170 offset:54272
	ds_read_b128 v[236:239], v170 offset:55296
	ds_read_b128 v[240:243], v170 offset:56320
	global_load_lds_dwordx4 v[166:167], off
	v_lshl_add_u64 v[166:167], v[210:211], 0, s[68:69]
	s_mov_b32 m0, s95
	s_nop 0
	global_load_lds_dwordx4 v[166:167], off
	v_lshl_add_u64 v[166:167], s[46:47], 0, v[184:185]
	s_mov_b32 m0, s76
	s_nop 0
	global_load_lds_dwordx4 v[166:167], off
	v_lshl_add_u64 v[166:167], s[46:47], 0, v[144:145]
	s_mov_b32 m0, s90
	s_nop 0
	global_load_lds_dwordx4 v[166:167], off
	v_lshl_add_u64 v[166:167], v[216:217], 0, s[68:69]
	s_mov_b32 m0, s88
	s_nop 0
	global_load_lds_dwordx4 v[166:167], off
	v_lshl_add_u64 v[166:167], v[218:219], 0, s[68:69]
	s_mov_b32 m0, s89
	s_nop 0
	global_load_lds_dwordx4 v[166:167], off
	s_waitcnt vmcnt(8)
	s_waitcnt lgkmcnt(0)
	s_barrier
	s_setprio 1
	s_waitcnt lgkmcnt(0)
	v_mfma_f32_16x16x32_bf16 v[60:63], v[112:115], v[198:201], v[60:63]
	v_mfma_f32_16x16x32_bf16 v[56:59], v[124:127], v[198:201], v[56:59]
	v_mfma_f32_16x16x32_bf16 v[40:43], v[124:127], v[206:209], v[40:43]
	v_mfma_f32_16x16x32_bf16 v[44:47], v[112:115], v[206:209], v[44:47]
	v_mfma_f32_16x16x32_bf16 v[36:39], v[112:115], v[228:231], v[36:39]
	v_mfma_f32_16x16x32_bf16 v[28:31], v[124:127], v[228:231], v[28:31]
	v_mfma_f32_16x16x32_bf16 v[12:15], v[124:127], v[236:239], v[12:15]
	v_mfma_f32_16x16x32_bf16 v[20:23], v[112:115], v[236:239], v[20:23]
	v_mfma_f32_16x16x32_bf16 v[60:63], v[116:119], v[202:205], v[60:63]
	v_mfma_f32_16x16x32_bf16 v[56:59], v[132:135], v[202:205], v[56:59]
	v_mfma_f32_16x16x32_bf16 v[40:43], v[132:135], v[224:227], v[40:43]
	v_mfma_f32_16x16x32_bf16 v[44:47], v[116:119], v[224:227], v[44:47]
	v_mfma_f32_16x16x32_bf16 v[36:39], v[116:119], v[232:235], v[36:39]
	v_mfma_f32_16x16x32_bf16 v[28:31], v[132:135], v[232:235], v[28:31]
	v_mfma_f32_16x16x32_bf16 v[12:15], v[132:135], v[240:243], v[12:15]
	v_mfma_f32_16x16x32_bf16 v[20:23], v[116:119], v[240:243], v[20:23]
	s_setprio 0
	s_setprio 1
	v_mfma_f32_16x16x32_bf16 v[52:55], v[172:175], v[198:201], v[52:55]
	v_mfma_f32_16x16x32_bf16 v[48:51], v[180:183], v[198:201], v[48:51]
	v_mfma_f32_16x16x32_bf16 v[24:27], v[180:183], v[206:209], v[24:27]
	v_mfma_f32_16x16x32_bf16 v[32:35], v[172:175], v[206:209], v[32:35]
	v_mfma_f32_16x16x32_bf16 v[16:19], v[172:175], v[228:231], v[16:19]
	v_mfma_f32_16x16x32_bf16 v[8:11], v[180:183], v[228:231], v[8:11]
	v_mfma_f32_16x16x32_bf16 v[0:3], v[180:183], v[236:239], v[0:3]
	v_mfma_f32_16x16x32_bf16 v[4:7], v[172:175], v[236:239], v[4:7]
	v_mfma_f32_16x16x32_bf16 v[52:55], v[176:179], v[202:205], v[52:55]
	v_mfma_f32_16x16x32_bf16 v[48:51], v[194:197], v[202:205], v[48:51]
	v_mfma_f32_16x16x32_bf16 v[24:27], v[194:197], v[224:227], v[24:27]
	v_mfma_f32_16x16x32_bf16 v[32:35], v[176:179], v[224:227], v[32:35]
	v_mfma_f32_16x16x32_bf16 v[16:19], v[176:179], v[232:235], v[16:19]
	v_mfma_f32_16x16x32_bf16 v[8:11], v[194:197], v[232:235], v[8:11]
	v_mfma_f32_16x16x32_bf16 v[0:3], v[194:197], v[240:243], v[0:3]
	v_mfma_f32_16x16x32_bf16 v[4:7], v[176:179], v[240:243], v[4:7]
	s_setprio 0
	s_barrier
	s_movk_i32 s50, 0x100
	s_andn2_b64 vcc, exec, s[44:45]
	s_mov_b64 s[46:47], -1
	s_mov_b64 s[44:45], 0
	s_cbranch_vccz .LBB0_1136
	s_and_b64 vcc, exec, s[8:9]
	s_cbranch_vccz .LBB0_1139
	s_barrier

.LBB0_1419:
	s_add_u32 s28, s24, 0xfff80080
	s_addc_u32 s29, s25, -1
	s_add_i32 s48, 0, 0x10000
	s_cmp_eq_u32 s17, 28
	s_cselect_b32 s31, s9, s29
	s_cselect_b32 s30, s11, s28
	s_cselect_b64 vcc, -1, 0
	s_add_i32 s28, 0, 0x14000
	v_add_u32_e32 v164, s48, v147
	v_add_u32_e32 v180, s28, v147
	ds_read_b128 v[152:155], v164
	ds_read_b128 v[156:159], v164 offset:1024
	ds_read_b128 v[160:163], v164 offset:2048
	ds_read_b128 v[164:167], v164 offset:3072
	ds_read_b128 v[168:171], v180
	ds_read_b128 v[172:175], v180 offset:1024
	ds_read_b128 v[176:179], v180 offset:2048
	ds_read_b128 v[180:183], v180 offset:3072
	v_cndmask_b32_e32 v211, v145, v150, vcc
	v_cndmask_b32_e32 v210, v144, v151, vcc
	v_lshl_add_u64 v[216:217], s[24:25], 0, v[136:137]
	s_add_i32 m0, s19, 0xc000
	ds_read_b128 v[194:197], v149
	ds_read_b128 v[198:201], v149 offset:1024
	ds_read_b128 v[202:205], v149 offset:2048
	ds_read_b128 v[206:209], v149 offset:3072
	ds_read_b128 v[224:227], v149 offset:4096
	ds_read_b128 v[228:231], v149 offset:5120
	ds_read_b128 v[232:235], v149 offset:6144
	ds_read_b128 v[236:239], v149 offset:7168
	global_load_lds_dwordx4 v[216:217], off
	v_lshl_add_u64 v[216:217], s[24:25], 0, v[138:139]
	s_add_i32 m0, s19, 0xe000
	s_nop 0
	global_load_lds_dwordx4 v[216:217], off
	s_waitcnt vmcnt(8)
	s_waitcnt lgkmcnt(0)
	s_barrier
	s_setprio 1
	s_waitcnt lgkmcnt(0)
	v_mfma_f32_16x16x32_bf16 v[124:127], v[152:155], v[194:197], v[124:127]
	v_mfma_f32_16x16x32_bf16 v[116:119], v[160:163], v[194:197], v[116:119]
	v_mfma_f32_16x16x32_bf16 v[100:103], v[160:163], v[202:205], v[100:103]
	v_mfma_f32_16x16x32_bf16 v[108:111], v[152:155], v[202:205], v[108:111]
	v_mfma_f32_16x16x32_bf16 v[92:95], v[152:155], v[224:227], v[92:95]
	v_mfma_f32_16x16x32_bf16 v[84:87], v[160:163], v[224:227], v[84:87]
	v_mfma_f32_16x16x32_bf16 v[68:71], v[160:163], v[232:235], v[68:71]
	v_mfma_f32_16x16x32_bf16 v[76:79], v[152:155], v[232:235], v[76:79]
	v_mfma_f32_16x16x32_bf16 v[124:127], v[156:159], v[198:201], v[124:127]
	v_mfma_f32_16x16x32_bf16 v[116:119], v[164:167], v[198:201], v[116:119]
	v_mfma_f32_16x16x32_bf16 v[100:103], v[164:167], v[206:209], v[100:103]
	v_mfma_f32_16x16x32_bf16 v[108:111], v[156:159], v[206:209], v[108:111]
	v_mfma_f32_16x16x32_bf16 v[92:95], v[156:159], v[228:231], v[92:95]
	v_mfma_f32_16x16x32_bf16 v[84:87], v[164:167], v[228:231], v[84:87]
	v_mfma_f32_16x16x32_bf16 v[68:71], v[164:167], v[236:239], v[68:71]
	v_mfma_f32_16x16x32_bf16 v[76:79], v[156:159], v[236:239], v[76:79]
	s_setprio 0
	s_setprio 1
	v_mfma_f32_16x16x32_bf16 v[120:123], v[168:171], v[194:197], v[120:123]
	v_mfma_f32_16x16x32_bf16 v[112:115], v[176:179], v[194:197], v[112:115]
	v_mfma_f32_16x16x32_bf16 v[96:99], v[176:179], v[202:205], v[96:99]
	v_mfma_f32_16x16x32_bf16 v[104:107], v[168:171], v[202:205], v[104:107]
	v_mfma_f32_16x16x32_bf16 v[88:91], v[168:171], v[224:227], v[88:91]
	v_mfma_f32_16x16x32_bf16 v[80:83], v[176:179], v[224:227], v[80:83]
	v_mfma_f32_16x16x32_bf16 v[64:67], v[176:179], v[232:235], v[64:67]
	v_mfma_f32_16x16x32_bf16 v[72:75], v[168:171], v[232:235], v[72:75]
	v_mfma_f32_16x16x32_bf16 v[120:123], v[172:175], v[198:201], v[120:123]
	v_mfma_f32_16x16x32_bf16 v[112:115], v[180:183], v[198:201], v[112:115]
	v_mfma_f32_16x16x32_bf16 v[96:99], v[180:183], v[206:209], v[96:99]
	v_mfma_f32_16x16x32_bf16 v[104:107], v[172:175], v[206:209], v[104:107]
	v_mfma_f32_16x16x32_bf16 v[88:91], v[172:175], v[228:231], v[88:91]
	v_mfma_f32_16x16x32_bf16 v[80:83], v[180:183], v[228:231], v[80:83]
	v_mfma_f32_16x16x32_bf16 v[64:67], v[180:183], v[236:239], v[64:67]
	v_mfma_f32_16x16x32_bf16 v[72:75], v[172:175], v[236:239], v[72:75]
	s_setprio 0
	s_barrier
	s_add_i32 s29, s48, s50
	v_lshl_add_u64 v[216:217], v[210:211], 0, v[130:131]
	s_mov_b32 m0, s29
	ds_read_b128 v[194:197], v149 offset:16384
	ds_read_b128 v[198:201], v149 offset:17408
	ds_read_b128 v[202:205], v149 offset:18432
	ds_read_b128 v[206:209], v149 offset:19456
	ds_read_b128 v[224:227], v149 offset:20480
	ds_read_b128 v[228:231], v149 offset:21504
	ds_read_b128 v[232:235], v149 offset:22528
	ds_read_b128 v[236:239], v149 offset:23552
	global_load_lds_dwordx4 v[216:217], off
	v_lshl_add_u64 v[218:219], v[210:211], 0, v[134:135]
	s_add_i32 m0, s29, 0x2000
	v_lshl_add_u64 v[220:221], v[210:211], 0, s[72:73]
	s_add_i32 s28, s28, s50
	global_load_lds_dwordx4 v[218:219], off
	v_lshl_add_u64 v[240:241], v[220:221], 0, v[130:131]
	s_mov_b32 m0, s28
	v_lshl_add_u64 v[220:221], v[220:221], 0, v[134:135]
	global_load_lds_dwordx4 v[240:241], off
	s_add_i32 m0, s28, 0x2000
	v_lshl_add_u64 v[240:241], s[30:31], 0, v[132:133]
	global_load_lds_dwordx4 v[220:221], off
	v_lshl_add_u64 v[220:221], s[30:31], 0, v[128:129]
	s_mov_b32 m0, s19
	s_nop 0
	global_load_lds_dwordx4 v[220:221], off
	s_mov_b32 m0, s51
	s_nop 0
	global_load_lds_dwordx4 v[240:241], off
	s_waitcnt vmcnt(8)
	s_waitcnt lgkmcnt(0)
	s_barrier
	s_setprio 1
	s_waitcnt lgkmcnt(0)
	v_mfma_f32_16x16x32_bf16 v[60:63], v[152:155], v[194:197], v[60:63]
	v_mfma_f32_16x16x32_bf16 v[52:55], v[160:163], v[194:197], v[52:55]
	v_mfma_f32_16x16x32_bf16 v[36:39], v[160:163], v[202:205], v[36:39]
	v_mfma_f32_16x16x32_bf16 v[44:47], v[152:155], v[202:205], v[44:47]
	v_mfma_f32_16x16x32_bf16 v[28:31], v[152:155], v[224:227], v[28:31]
	v_mfma_f32_16x16x32_bf16 v[20:23], v[160:163], v[224:227], v[20:23]
	v_mfma_f32_16x16x32_bf16 v[4:7], v[160:163], v[232:235], v[4:7]
	v_mfma_f32_16x16x32_bf16 v[12:15], v[152:155], v[232:235], v[12:15]
	v_mfma_f32_16x16x32_bf16 v[60:63], v[156:159], v[198:201], v[60:63]
	v_mfma_f32_16x16x32_bf16 v[52:55], v[164:167], v[198:201], v[52:55]
	v_mfma_f32_16x16x32_bf16 v[36:39], v[164:167], v[206:209], v[36:39]
	v_mfma_f32_16x16x32_bf16 v[44:47], v[156:159], v[206:209], v[44:47]
	v_mfma_f32_16x16x32_bf16 v[28:31], v[156:159], v[228:231], v[28:31]
	v_mfma_f32_16x16x32_bf16 v[20:23], v[164:167], v[228:231], v[20:23]
	v_mfma_f32_16x16x32_bf16 v[4:7], v[164:167], v[236:239], v[4:7]
	v_mfma_f32_16x16x32_bf16 v[12:15], v[156:159], v[236:239], v[12:15]
	s_setprio 0
	s_setprio 1
	v_mfma_f32_16x16x32_bf16 v[56:59], v[168:171], v[194:197], v[56:59]
	v_mfma_f32_16x16x32_bf16 v[48:51], v[176:179], v[194:197], v[48:51]
	v_mfma_f32_16x16x32_bf16 v[32:35], v[176:179], v[202:205], v[32:35]
	v_mfma_f32_16x16x32_bf16 v[40:43], v[168:171], v[202:205], v[40:43]
	v_mfma_f32_16x16x32_bf16 v[24:27], v[168:171], v[224:227], v[24:27]
	v_mfma_f32_16x16x32_bf16 v[16:19], v[176:179], v[224:227], v[16:19]
	v_mfma_f32_16x16x32_bf16 v[0:3], v[176:179], v[232:235], v[0:3]
	v_mfma_f32_16x16x32_bf16 v[8:11], v[168:171], v[232:235], v[8:11]
	v_mfma_f32_16x16x32_bf16 v[56:59], v[172:175], v[198:201], v[56:59]
	v_mfma_f32_16x16x32_bf16 v[48:51], v[180:183], v[198:201], v[48:51]
	v_mfma_f32_16x16x32_bf16 v[32:35], v[180:183], v[206:209], v[32:35]
	v_mfma_f32_16x16x32_bf16 v[40:43], v[172:175], v[206:209], v[40:43]
	v_mfma_f32_16x16x32_bf16 v[24:27], v[172:175], v[228:231], v[24:27]
	v_mfma_f32_16x16x32_bf16 v[16:19], v[180:183], v[228:231], v[16:19]
	v_mfma_f32_16x16x32_bf16 v[0:3], v[180:183], v[236:239], v[0:3]
	v_mfma_f32_16x16x32_bf16 v[8:11], v[172:175], v[236:239], v[8:11]
	s_setprio 0
	s_barrier
	s_add_i32 s48, 0, 0x18000
	s_add_i32 s49, 0, 0x1c000
	v_add_u32_e32 v164, s48, v147
	v_add_u32_e32 v180, s49, v147
	ds_read_b128 v[152:155], v164
	ds_read_b128 v[156:159], v164 offset:1024
	ds_read_b128 v[160:163], v164 offset:2048
	ds_read_b128 v[164:167], v164 offset:3072
	ds_read_b128 v[168:171], v180
	ds_read_b128 v[172:175], v180 offset:1024
	ds_read_b128 v[176:179], v180 offset:2048
	ds_read_b128 v[180:183], v180 offset:3072
	s_add_u32 s28, s30, 0x80000
	s_addc_u32 s29, s31, 0
	s_mov_b32 m0, s52
	v_lshl_add_u64 v[242:243], s[28:29], 0, v[128:129]
	ds_read_b128 v[194:197], v149 offset:32768
	ds_read_b128 v[198:201], v149 offset:33792
	ds_read_b128 v[202:205], v149 offset:34816
	ds_read_b128 v[206:209], v149 offset:35840
	ds_read_b128 v[224:227], v149 offset:36864
	ds_read_b128 v[228:231], v149 offset:37888
	ds_read_b128 v[232:235], v149 offset:38912
	ds_read_b128 v[236:239], v149 offset:39936
	global_load_lds_dwordx4 v[242:243], off
	v_lshl_add_u64 v[242:243], s[28:29], 0, v[132:133]
	s_mov_b32 m0, s53
	s_nop 0
	global_load_lds_dwordx4 v[242:243], off
	s_waitcnt vmcnt(8)
	s_waitcnt lgkmcnt(0)
	s_barrier
	s_setprio 1
	s_waitcnt lgkmcnt(0)
	v_mfma_f32_16x16x32_bf16 v[124:127], v[152:155], v[194:197], v[124:127]
	v_mfma_f32_16x16x32_bf16 v[116:119], v[160:163], v[194:197], v[116:119]
	v_mfma_f32_16x16x32_bf16 v[100:103], v[160:163], v[202:205], v[100:103]
	v_mfma_f32_16x16x32_bf16 v[108:111], v[152:155], v[202:205], v[108:111]
	v_mfma_f32_16x16x32_bf16 v[92:95], v[152:155], v[224:227], v[92:95]
	v_mfma_f32_16x16x32_bf16 v[84:87], v[160:163], v[224:227], v[84:87]
	v_mfma_f32_16x16x32_bf16 v[68:71], v[160:163], v[232:235], v[68:71]
	v_mfma_f32_16x16x32_bf16 v[76:79], v[152:155], v[232:235], v[76:79]
	v_mfma_f32_16x16x32_bf16 v[124:127], v[156:159], v[198:201], v[124:127]
	v_mfma_f32_16x16x32_bf16 v[116:119], v[164:167], v[198:201], v[116:119]
	v_mfma_f32_16x16x32_bf16 v[100:103], v[164:167], v[206:209], v[100:103]
	v_mfma_f32_16x16x32_bf16 v[108:111], v[156:159], v[206:209], v[108:111]
	v_mfma_f32_16x16x32_bf16 v[92:95], v[156:159], v[228:231], v[92:95]
	v_mfma_f32_16x16x32_bf16 v[84:87], v[164:167], v[228:231], v[84:87]
	v_mfma_f32_16x16x32_bf16 v[68:71], v[164:167], v[236:239], v[68:71]
	v_mfma_f32_16x16x32_bf16 v[76:79], v[156:159], v[236:239], v[76:79]
	s_setprio 0
	s_setprio 1
	v_mfma_f32_16x16x32_bf16 v[120:123], v[168:171], v[194:197], v[120:123]
	v_mfma_f32_16x16x32_bf16 v[112:115], v[176:179], v[194:197], v[112:115]
	v_mfma_f32_16x16x32_bf16 v[96:99], v[176:179], v[202:205], v[96:99]
	v_mfma_f32_16x16x32_bf16 v[104:107], v[168:171], v[202:205], v[104:107]
	v_mfma_f32_16x16x32_bf16 v[88:91], v[168:171], v[224:227], v[88:91]
	v_mfma_f32_16x16x32_bf16 v[80:83], v[176:179], v[224:227], v[80:83]
	v_mfma_f32_16x16x32_bf16 v[64:67], v[176:179], v[232:235], v[64:67]
	v_mfma_f32_16x16x32_bf16 v[72:75], v[168:171], v[232:235], v[72:75]
	v_mfma_f32_16x16x32_bf16 v[120:123], v[172:175], v[198:201], v[120:123]
	v_mfma_f32_16x16x32_bf16 v[112:115], v[180:183], v[198:201], v[112:115]
	v_mfma_f32_16x16x32_bf16 v[96:99], v[180:183], v[206:209], v[96:99]
	v_mfma_f32_16x16x32_bf16 v[104:107], v[172:175], v[206:209], v[104:107]
	v_mfma_f32_16x16x32_bf16 v[88:91], v[172:175], v[228:231], v[88:91]
	v_mfma_f32_16x16x32_bf16 v[80:83], v[180:183], v[228:231], v[80:83]
	v_mfma_f32_16x16x32_bf16 v[64:67], v[180:183], v[236:239], v[64:67]
	v_mfma_f32_16x16x32_bf16 v[72:75], v[172:175], v[236:239], v[72:75]
	s_setprio 0
	s_barrier
	s_add_i32 s28, s48, s50
	v_lshl_add_u64 v[216:217], v[216:217], 0, s[68:69]
	s_mov_b32 m0, s28
	ds_read_b128 v[194:197], v149 offset:49152
	ds_read_b128 v[198:201], v149 offset:50176
	ds_read_b128 v[202:205], v149 offset:51200
	ds_read_b128 v[206:209], v149 offset:52224
	ds_read_b128 v[224:227], v149 offset:53248
	ds_read_b128 v[228:231], v149 offset:54272
	ds_read_b128 v[232:235], v149 offset:55296
	ds_read_b128 v[236:239], v149 offset:56320
	global_load_lds_dwordx4 v[216:217], off
	v_lshl_add_u64 v[216:217], v[218:219], 0, s[68:69]
	s_add_i32 m0, s28, 0x2000
	v_lshl_add_u64 v[210:211], v[210:211], 0, s[74:75]
	s_add_i32 s28, s49, s50
	global_load_lds_dwordx4 v[216:217], off
	v_lshl_add_u64 v[216:217], v[210:211], 0, v[130:131]
	s_mov_b32 m0, s28
	v_lshl_add_u64 v[210:211], v[210:211], 0, v[134:135]
	global_load_lds_dwordx4 v[216:217], off
	s_add_i32 m0, s28, 0x2000
	s_nop 0
	global_load_lds_dwordx4 v[210:211], off
	v_lshl_add_u64 v[210:211], v[220:221], 0, s[68:69]
	s_mov_b32 m0, s58
	s_nop 0
	global_load_lds_dwordx4 v[210:211], off
	v_lshl_add_u64 v[210:211], v[240:241], 0, s[68:69]
	s_mov_b32 m0, s59
	s_nop 0
	global_load_lds_dwordx4 v[210:211], off
	s_waitcnt vmcnt(8)
	s_waitcnt lgkmcnt(0)
	s_barrier
	s_setprio 1
	s_waitcnt lgkmcnt(0)
	v_mfma_f32_16x16x32_bf16 v[60:63], v[152:155], v[194:197], v[60:63]
	v_mfma_f32_16x16x32_bf16 v[52:55], v[160:163], v[194:197], v[52:55]
	v_mfma_f32_16x16x32_bf16 v[36:39], v[160:163], v[202:205], v[36:39]
	v_mfma_f32_16x16x32_bf16 v[44:47], v[152:155], v[202:205], v[44:47]
	v_mfma_f32_16x16x32_bf16 v[28:31], v[152:155], v[224:227], v[28:31]
	v_mfma_f32_16x16x32_bf16 v[20:23], v[160:163], v[224:227], v[20:23]
	v_mfma_f32_16x16x32_bf16 v[4:7], v[160:163], v[232:235], v[4:7]
	v_mfma_f32_16x16x32_bf16 v[12:15], v[152:155], v[232:235], v[12:15]
	v_mfma_f32_16x16x32_bf16 v[60:63], v[156:159], v[198:201], v[60:63]
	v_mfma_f32_16x16x32_bf16 v[52:55], v[164:167], v[198:201], v[52:55]
	v_mfma_f32_16x16x32_bf16 v[36:39], v[164:167], v[206:209], v[36:39]
	v_mfma_f32_16x16x32_bf16 v[44:47], v[156:159], v[206:209], v[44:47]
	v_mfma_f32_16x16x32_bf16 v[28:31], v[156:159], v[228:231], v[28:31]
	v_mfma_f32_16x16x32_bf16 v[20:23], v[164:167], v[228:231], v[20:23]
	v_mfma_f32_16x16x32_bf16 v[4:7], v[164:167], v[236:239], v[4:7]
	v_mfma_f32_16x16x32_bf16 v[12:15], v[156:159], v[236:239], v[12:15]
	s_setprio 0
	s_setprio 1
	v_mfma_f32_16x16x32_bf16 v[56:59], v[168:171], v[194:197], v[56:59]
	v_mfma_f32_16x16x32_bf16 v[48:51], v[176:179], v[194:197], v[48:51]
	v_mfma_f32_16x16x32_bf16 v[32:35], v[176:179], v[202:205], v[32:35]
	v_mfma_f32_16x16x32_bf16 v[40:43], v[168:171], v[202:205], v[40:43]
	v_mfma_f32_16x16x32_bf16 v[24:27], v[168:171], v[224:227], v[24:27]
	v_mfma_f32_16x16x32_bf16 v[16:19], v[176:179], v[224:227], v[16:19]
	v_mfma_f32_16x16x32_bf16 v[0:3], v[176:179], v[232:235], v[0:3]
	v_mfma_f32_16x16x32_bf16 v[8:11], v[168:171], v[232:235], v[8:11]
	v_mfma_f32_16x16x32_bf16 v[56:59], v[172:175], v[198:201], v[56:59]
	v_mfma_f32_16x16x32_bf16 v[48:51], v[180:183], v[198:201], v[48:51]
	v_mfma_f32_16x16x32_bf16 v[32:35], v[180:183], v[206:209], v[32:35]
	v_mfma_f32_16x16x32_bf16 v[40:43], v[172:175], v[206:209], v[40:43]
	v_mfma_f32_16x16x32_bf16 v[24:27], v[172:175], v[228:231], v[24:27]
	v_mfma_f32_16x16x32_bf16 v[16:19], v[180:183], v[228:231], v[16:19]
	v_mfma_f32_16x16x32_bf16 v[0:3], v[180:183], v[236:239], v[0:3]
	v_mfma_f32_16x16x32_bf16 v[8:11], v[172:175], v[236:239], v[8:11]
	s_setprio 0
	s_barrier
	s_add_i32 s17, s17, 2
	s_add_u32 s24, s24, 0x100
	s_addc_u32 s25, s25, 0
	s_cmp_gt_u32 s17, 29
	v_lshl_add_u64 v[144:145], v[144:145], 0, s[76:77]
	s_cbranch_scc0 .LBB0_1419
	s_and_b64 vcc, exec, s[6:7]
	s_cbranch_vccz .LBB0_1422
	s_barrier

.LBB0_1491:
	s_add_u32 s14, s12, 0x100
	s_addc_u32 s15, s13, 0
	s_add_i32 s28, 0, 0x10000
	s_cmp_eq_u32 s59, 40
	s_cselect_b32 s17, s53, s15
	s_cselect_b32 s16, s58, s14
	s_cselect_b64 vcc, -1, 0
	s_add_i32 s29, 0, 0x14000
	v_add_u32_e32 v164, s28, v147
	v_add_u32_e32 v180, s29, v147
	ds_read_b128 v[152:155], v164
	ds_read_b128 v[156:159], v164 offset:1024
	ds_read_b128 v[160:163], v164 offset:2048
	ds_read_b128 v[164:167], v164 offset:3072
	ds_read_b128 v[168:171], v180
	ds_read_b128 v[172:175], v180 offset:1024
	ds_read_b128 v[176:179], v180 offset:2048
	ds_read_b128 v[180:183], v180 offset:3072
	v_cndmask_b32_e32 v211, v145, v150, vcc
	v_cndmask_b32_e32 v210, v144, v151, vcc
	v_lshl_add_u64 v[216:217], s[12:13], 0, v[136:137]
	s_add_i32 m0, s40, 0xc000
	ds_read_b128 v[194:197], v149
	ds_read_b128 v[198:201], v149 offset:1024
	ds_read_b128 v[202:205], v149 offset:2048
	ds_read_b128 v[206:209], v149 offset:3072
	ds_read_b128 v[224:227], v149 offset:4096
	ds_read_b128 v[228:231], v149 offset:5120
	ds_read_b128 v[232:235], v149 offset:6144
	ds_read_b128 v[236:239], v149 offset:7168
	global_load_lds_dwordx4 v[216:217], off
	v_lshl_add_u64 v[216:217], s[12:13], 0, v[138:139]
	s_add_i32 m0, s40, 0xe000
	s_nop 0
	global_load_lds_dwordx4 v[216:217], off
	s_waitcnt vmcnt(8)
	s_waitcnt lgkmcnt(0)
	s_barrier
	s_setprio 1
	s_waitcnt lgkmcnt(0)
	v_mfma_f32_16x16x32_bf16 v[124:127], v[152:155], v[194:197], v[124:127]
	v_mfma_f32_16x16x32_bf16 v[120:123], v[160:163], v[194:197], v[120:123]
	v_mfma_f32_16x16x32_bf16 v[108:111], v[160:163], v[202:205], v[108:111]
	v_mfma_f32_16x16x32_bf16 v[116:119], v[152:155], v[202:205], v[116:119]
	v_mfma_f32_16x16x32_bf16 v[100:103], v[152:155], v[224:227], v[100:103]
	v_mfma_f32_16x16x32_bf16 v[92:95], v[160:163], v[224:227], v[92:95]
	v_mfma_f32_16x16x32_bf16 v[72:75], v[160:163], v[232:235], v[72:75]
	v_mfma_f32_16x16x32_bf16 v[80:83], v[152:155], v[232:235], v[80:83]
	v_mfma_f32_16x16x32_bf16 v[124:127], v[156:159], v[198:201], v[124:127]
	v_mfma_f32_16x16x32_bf16 v[120:123], v[164:167], v[198:201], v[120:123]
	v_mfma_f32_16x16x32_bf16 v[108:111], v[164:167], v[206:209], v[108:111]
	v_mfma_f32_16x16x32_bf16 v[116:119], v[156:159], v[206:209], v[116:119]
	v_mfma_f32_16x16x32_bf16 v[100:103], v[156:159], v[228:231], v[100:103]
	v_mfma_f32_16x16x32_bf16 v[92:95], v[164:167], v[228:231], v[92:95]
	v_mfma_f32_16x16x32_bf16 v[72:75], v[164:167], v[236:239], v[72:75]
	v_mfma_f32_16x16x32_bf16 v[80:83], v[156:159], v[236:239], v[80:83]
	s_setprio 0
	s_setprio 1
	v_mfma_f32_16x16x32_bf16 v[112:115], v[168:171], v[194:197], v[112:115]
	v_mfma_f32_16x16x32_bf16 v[104:107], v[176:179], v[194:197], v[104:107]
	v_mfma_f32_16x16x32_bf16 v[88:91], v[176:179], v[202:205], v[88:91]
	v_mfma_f32_16x16x32_bf16 v[96:99], v[168:171], v[202:205], v[96:99]
	v_mfma_f32_16x16x32_bf16 v[84:87], v[168:171], v[224:227], v[84:87]
	v_mfma_f32_16x16x32_bf16 v[76:79], v[176:179], v[224:227], v[76:79]
	v_mfma_f32_16x16x32_bf16 v[64:67], v[176:179], v[232:235], v[64:67]
	v_mfma_f32_16x16x32_bf16 v[68:71], v[168:171], v[232:235], v[68:71]
	v_mfma_f32_16x16x32_bf16 v[112:115], v[172:175], v[198:201], v[112:115]
	v_mfma_f32_16x16x32_bf16 v[104:107], v[180:183], v[198:201], v[104:107]
	v_mfma_f32_16x16x32_bf16 v[88:91], v[180:183], v[206:209], v[88:91]
	v_mfma_f32_16x16x32_bf16 v[96:99], v[172:175], v[206:209], v[96:99]
	v_mfma_f32_16x16x32_bf16 v[84:87], v[172:175], v[228:231], v[84:87]
	v_mfma_f32_16x16x32_bf16 v[76:79], v[180:183], v[228:231], v[76:79]
	v_mfma_f32_16x16x32_bf16 v[64:67], v[180:183], v[236:239], v[64:67]
	v_mfma_f32_16x16x32_bf16 v[68:71], v[172:175], v[236:239], v[68:71]
	s_setprio 0
	s_barrier
	s_add_i32 s12, s28, s30
	v_lshl_add_u64 v[216:217], v[210:211], 0, v[132:133]
	s_mov_b32 m0, s12
	ds_read_b128 v[194:197], v149 offset:16384
	ds_read_b128 v[198:201], v149 offset:17408
	ds_read_b128 v[202:205], v149 offset:18432
	ds_read_b128 v[206:209], v149 offset:19456
	ds_read_b128 v[224:227], v149 offset:20480
	ds_read_b128 v[228:231], v149 offset:21504
	ds_read_b128 v[232:235], v149 offset:22528
	ds_read_b128 v[236:239], v149 offset:23552
	global_load_lds_dwordx4 v[216:217], off
	v_lshl_add_u64 v[218:219], v[210:211], 0, v[128:129]
	s_add_i32 m0, s12, 0x2000
	v_lshl_add_u64 v[220:221], v[210:211], 0, s[72:73]
	s_add_i32 s12, s29, s30
	global_load_lds_dwordx4 v[218:219], off
	v_lshl_add_u64 v[240:241], v[220:221], 0, v[132:133]
	s_mov_b32 m0, s12
	v_lshl_add_u64 v[220:221], v[220:221], 0, v[128:129]
	global_load_lds_dwordx4 v[240:241], off
	s_add_i32 m0, s12, 0x2000
	v_lshl_add_u64 v[240:241], s[16:17], 0, v[130:131]
	global_load_lds_dwordx4 v[220:221], off
	v_lshl_add_u64 v[220:221], s[16:17], 0, v[134:135]
	s_mov_b32 m0, s40
	s_nop 0
	global_load_lds_dwordx4 v[220:221], off
	s_mov_b32 m0, s41
	s_nop 0
	global_load_lds_dwordx4 v[240:241], off
	s_waitcnt vmcnt(8)
	s_waitcnt lgkmcnt(0)
	s_barrier
	s_setprio 1
	s_waitcnt lgkmcnt(0)
	v_mfma_f32_16x16x32_bf16 v[60:63], v[152:155], v[194:197], v[60:63]
	v_mfma_f32_16x16x32_bf16 v[56:59], v[160:163], v[194:197], v[56:59]
	v_mfma_f32_16x16x32_bf16 v[44:47], v[160:163], v[202:205], v[44:47]
	v_mfma_f32_16x16x32_bf16 v[52:55], v[152:155], v[202:205], v[52:55]
	v_mfma_f32_16x16x32_bf16 v[36:39], v[152:155], v[224:227], v[36:39]
	v_mfma_f32_16x16x32_bf16 v[28:31], v[160:163], v[224:227], v[28:31]
	v_mfma_f32_16x16x32_bf16 v[12:15], v[160:163], v[232:235], v[12:15]
	v_mfma_f32_16x16x32_bf16 v[20:23], v[152:155], v[232:235], v[20:23]
	v_mfma_f32_16x16x32_bf16 v[60:63], v[156:159], v[198:201], v[60:63]
	v_mfma_f32_16x16x32_bf16 v[56:59], v[164:167], v[198:201], v[56:59]
	v_mfma_f32_16x16x32_bf16 v[44:47], v[164:167], v[206:209], v[44:47]
	v_mfma_f32_16x16x32_bf16 v[52:55], v[156:159], v[206:209], v[52:55]
	v_mfma_f32_16x16x32_bf16 v[36:39], v[156:159], v[228:231], v[36:39]
	v_mfma_f32_16x16x32_bf16 v[28:31], v[164:167], v[228:231], v[28:31]
	v_mfma_f32_16x16x32_bf16 v[12:15], v[164:167], v[236:239], v[12:15]
	v_mfma_f32_16x16x32_bf16 v[20:23], v[156:159], v[236:239], v[20:23]
	s_setprio 0
	s_setprio 1
	v_mfma_f32_16x16x32_bf16 v[48:51], v[168:171], v[194:197], v[48:51]
	v_mfma_f32_16x16x32_bf16 v[40:43], v[176:179], v[194:197], v[40:43]
	v_mfma_f32_16x16x32_bf16 v[24:27], v[176:179], v[202:205], v[24:27]
	v_mfma_f32_16x16x32_bf16 v[32:35], v[168:171], v[202:205], v[32:35]
	v_mfma_f32_16x16x32_bf16 v[16:19], v[168:171], v[224:227], v[16:19]
	v_mfma_f32_16x16x32_bf16 v[8:11], v[176:179], v[224:227], v[8:11]
	v_mfma_f32_16x16x32_bf16 v[0:3], v[176:179], v[232:235], v[0:3]
	v_mfma_f32_16x16x32_bf16 v[4:7], v[168:171], v[232:235], v[4:7]
	v_mfma_f32_16x16x32_bf16 v[48:51], v[172:175], v[198:201], v[48:51]
	v_mfma_f32_16x16x32_bf16 v[40:43], v[180:183], v[198:201], v[40:43]
	v_mfma_f32_16x16x32_bf16 v[24:27], v[180:183], v[206:209], v[24:27]
	v_mfma_f32_16x16x32_bf16 v[32:35], v[172:175], v[206:209], v[32:35]
	v_mfma_f32_16x16x32_bf16 v[16:19], v[172:175], v[228:231], v[16:19]
	v_mfma_f32_16x16x32_bf16 v[8:11], v[180:183], v[228:231], v[8:11]
	v_mfma_f32_16x16x32_bf16 v[0:3], v[180:183], v[236:239], v[0:3]
	v_mfma_f32_16x16x32_bf16 v[4:7], v[172:175], v[236:239], v[4:7]
	s_setprio 0
	s_barrier
	s_add_i32 s28, 0, 0x18000
	s_add_i32 s29, 0, 0x1c000
	v_add_u32_e32 v164, s28, v147
	v_add_u32_e32 v180, s29, v147
	ds_read_b128 v[152:155], v164
	ds_read_b128 v[156:159], v164 offset:1024
	ds_read_b128 v[160:163], v164 offset:2048
	ds_read_b128 v[164:167], v164 offset:3072
	ds_read_b128 v[168:171], v180
	ds_read_b128 v[172:175], v180 offset:1024
	ds_read_b128 v[176:179], v180 offset:2048
	ds_read_b128 v[180:183], v180 offset:3072
	s_add_u32 s12, s16, 0xb0000
	s_addc_u32 s13, s17, 0
	s_mov_b32 m0, s42
	v_lshl_add_u64 v[242:243], s[12:13], 0, v[134:135]
	ds_read_b128 v[194:197], v149 offset:32768
	ds_read_b128 v[198:201], v149 offset:33792
	ds_read_b128 v[202:205], v149 offset:34816
	ds_read_b128 v[206:209], v149 offset:35840
	ds_read_b128 v[224:227], v149 offset:36864
	ds_read_b128 v[228:231], v149 offset:37888
	ds_read_b128 v[232:235], v149 offset:38912
	ds_read_b128 v[236:239], v149 offset:39936
	global_load_lds_dwordx4 v[242:243], off
	v_lshl_add_u64 v[242:243], s[12:13], 0, v[130:131]
	s_mov_b32 m0, s43
	s_nop 0
	global_load_lds_dwordx4 v[242:243], off
	s_waitcnt vmcnt(8)
	s_waitcnt lgkmcnt(0)
	s_barrier
	s_setprio 1
	s_waitcnt lgkmcnt(0)
	v_mfma_f32_16x16x32_bf16 v[124:127], v[152:155], v[194:197], v[124:127]
	v_mfma_f32_16x16x32_bf16 v[120:123], v[160:163], v[194:197], v[120:123]
	v_mfma_f32_16x16x32_bf16 v[108:111], v[160:163], v[202:205], v[108:111]
	v_mfma_f32_16x16x32_bf16 v[116:119], v[152:155], v[202:205], v[116:119]
	v_mfma_f32_16x16x32_bf16 v[100:103], v[152:155], v[224:227], v[100:103]
	v_mfma_f32_16x16x32_bf16 v[92:95], v[160:163], v[224:227], v[92:95]
	v_mfma_f32_16x16x32_bf16 v[72:75], v[160:163], v[232:235], v[72:75]
	v_mfma_f32_16x16x32_bf16 v[80:83], v[152:155], v[232:235], v[80:83]
	v_mfma_f32_16x16x32_bf16 v[124:127], v[156:159], v[198:201], v[124:127]
	v_mfma_f32_16x16x32_bf16 v[120:123], v[164:167], v[198:201], v[120:123]
	v_mfma_f32_16x16x32_bf16 v[108:111], v[164:167], v[206:209], v[108:111]
	v_mfma_f32_16x16x32_bf16 v[116:119], v[156:159], v[206:209], v[116:119]
	v_mfma_f32_16x16x32_bf16 v[100:103], v[156:159], v[228:231], v[100:103]
	v_mfma_f32_16x16x32_bf16 v[92:95], v[164:167], v[228:231], v[92:95]
	v_mfma_f32_16x16x32_bf16 v[72:75], v[164:167], v[236:239], v[72:75]
	v_mfma_f32_16x16x32_bf16 v[80:83], v[156:159], v[236:239], v[80:83]
	s_setprio 0
	s_setprio 1
	v_mfma_f32_16x16x32_bf16 v[112:115], v[168:171], v[194:197], v[112:115]
	v_mfma_f32_16x16x32_bf16 v[104:107], v[176:179], v[194:197], v[104:107]
	v_mfma_f32_16x16x32_bf16 v[88:91], v[176:179], v[202:205], v[88:91]
	v_mfma_f32_16x16x32_bf16 v[96:99], v[168:171], v[202:205], v[96:99]
	v_mfma_f32_16x16x32_bf16 v[84:87], v[168:171], v[224:227], v[84:87]
	v_mfma_f32_16x16x32_bf16 v[76:79], v[176:179], v[224:227], v[76:79]
	v_mfma_f32_16x16x32_bf16 v[64:67], v[176:179], v[232:235], v[64:67]
	v_mfma_f32_16x16x32_bf16 v[68:71], v[168:171], v[232:235], v[68:71]
	v_mfma_f32_16x16x32_bf16 v[112:115], v[172:175], v[198:201], v[112:115]
	v_mfma_f32_16x16x32_bf16 v[104:107], v[180:183], v[198:201], v[104:107]
	v_mfma_f32_16x16x32_bf16 v[88:91], v[180:183], v[206:209], v[88:91]
	v_mfma_f32_16x16x32_bf16 v[96:99], v[172:175], v[206:209], v[96:99]
	v_mfma_f32_16x16x32_bf16 v[84:87], v[172:175], v[228:231], v[84:87]
	v_mfma_f32_16x16x32_bf16 v[76:79], v[180:183], v[228:231], v[76:79]
	v_mfma_f32_16x16x32_bf16 v[64:67], v[180:183], v[236:239], v[64:67]
	v_mfma_f32_16x16x32_bf16 v[68:71], v[172:175], v[236:239], v[68:71]
	s_setprio 0
	s_barrier
	s_add_i32 s12, s28, s30
	v_lshl_add_u64 v[216:217], v[216:217], 0, s[68:69]
	s_mov_b32 m0, s12
	ds_read_b128 v[194:197], v149 offset:49152
	ds_read_b128 v[198:201], v149 offset:50176
	ds_read_b128 v[202:205], v149 offset:51200
	ds_read_b128 v[206:209], v149 offset:52224
	ds_read_b128 v[224:227], v149 offset:53248
	ds_read_b128 v[228:231], v149 offset:54272
	ds_read_b128 v[232:235], v149 offset:55296
	ds_read_b128 v[236:239], v149 offset:56320
	global_load_lds_dwordx4 v[216:217], off
	v_lshl_add_u64 v[216:217], v[218:219], 0, s[68:69]
	s_add_i32 m0, s12, 0x2000
	v_lshl_add_u64 v[210:211], v[210:211], 0, s[74:75]
	s_add_i32 s12, s29, s30
	global_load_lds_dwordx4 v[216:217], off
	v_lshl_add_u64 v[216:217], v[210:211], 0, v[132:133]
	s_mov_b32 m0, s12
	v_lshl_add_u64 v[210:211], v[210:211], 0, v[128:129]
	global_load_lds_dwordx4 v[216:217], off
	s_add_i32 m0, s12, 0x2000
	s_nop 0
	global_load_lds_dwordx4 v[210:211], off
	v_lshl_add_u64 v[210:211], v[220:221], 0, s[68:69]
	s_mov_b32 m0, s44
	s_nop 0
	global_load_lds_dwordx4 v[210:211], off
	v_lshl_add_u64 v[210:211], v[240:241], 0, s[68:69]
	s_mov_b32 m0, s45
	s_nop 0
	global_load_lds_dwordx4 v[210:211], off
	s_waitcnt vmcnt(8)
	s_waitcnt lgkmcnt(0)
	s_barrier
	s_setprio 1
	s_waitcnt lgkmcnt(0)
	v_mfma_f32_16x16x32_bf16 v[60:63], v[152:155], v[194:197], v[60:63]
	v_mfma_f32_16x16x32_bf16 v[56:59], v[160:163], v[194:197], v[56:59]
	v_mfma_f32_16x16x32_bf16 v[44:47], v[160:163], v[202:205], v[44:47]
	v_mfma_f32_16x16x32_bf16 v[52:55], v[152:155], v[202:205], v[52:55]
	v_mfma_f32_16x16x32_bf16 v[36:39], v[152:155], v[224:227], v[36:39]
	v_mfma_f32_16x16x32_bf16 v[28:31], v[160:163], v[224:227], v[28:31]
	v_mfma_f32_16x16x32_bf16 v[12:15], v[160:163], v[232:235], v[12:15]
	v_mfma_f32_16x16x32_bf16 v[20:23], v[152:155], v[232:235], v[20:23]
	v_mfma_f32_16x16x32_bf16 v[60:63], v[156:159], v[198:201], v[60:63]
	v_mfma_f32_16x16x32_bf16 v[56:59], v[164:167], v[198:201], v[56:59]
	v_mfma_f32_16x16x32_bf16 v[44:47], v[164:167], v[206:209], v[44:47]
	v_mfma_f32_16x16x32_bf16 v[52:55], v[156:159], v[206:209], v[52:55]
	v_mfma_f32_16x16x32_bf16 v[36:39], v[156:159], v[228:231], v[36:39]
	v_mfma_f32_16x16x32_bf16 v[28:31], v[164:167], v[228:231], v[28:31]
	v_mfma_f32_16x16x32_bf16 v[12:15], v[164:167], v[236:239], v[12:15]
	v_mfma_f32_16x16x32_bf16 v[20:23], v[156:159], v[236:239], v[20:23]
	s_setprio 0
	s_setprio 1
	v_mfma_f32_16x16x32_bf16 v[48:51], v[168:171], v[194:197], v[48:51]
	v_mfma_f32_16x16x32_bf16 v[40:43], v[176:179], v[194:197], v[40:43]
	v_mfma_f32_16x16x32_bf16 v[24:27], v[176:179], v[202:205], v[24:27]
	v_mfma_f32_16x16x32_bf16 v[32:35], v[168:171], v[202:205], v[32:35]
	v_mfma_f32_16x16x32_bf16 v[16:19], v[168:171], v[224:227], v[16:19]
	v_mfma_f32_16x16x32_bf16 v[8:11], v[176:179], v[224:227], v[8:11]
	v_mfma_f32_16x16x32_bf16 v[0:3], v[176:179], v[232:235], v[0:3]
	v_mfma_f32_16x16x32_bf16 v[4:7], v[168:171], v[232:235], v[4:7]
	v_mfma_f32_16x16x32_bf16 v[48:51], v[172:175], v[198:201], v[48:51]
	v_mfma_f32_16x16x32_bf16 v[40:43], v[180:183], v[198:201], v[40:43]
	v_mfma_f32_16x16x32_bf16 v[24:27], v[180:183], v[206:209], v[24:27]
	v_mfma_f32_16x16x32_bf16 v[32:35], v[172:175], v[206:209], v[32:35]
	v_mfma_f32_16x16x32_bf16 v[16:19], v[172:175], v[228:231], v[16:19]
	v_mfma_f32_16x16x32_bf16 v[8:11], v[180:183], v[228:231], v[8:11]
	v_mfma_f32_16x16x32_bf16 v[0:3], v[180:183], v[236:239], v[0:3]
	v_mfma_f32_16x16x32_bf16 v[4:7], v[172:175], v[236:239], v[4:7]
	s_setprio 0
	s_barrier
	s_add_i32 s59, s59, 2
	v_lshl_add_u64 v[144:145], v[144:145], 0, s[60:61]
	s_cmp_gt_u32 s59, 41
	s_mov_b64 s[12:13], s[14:15]
	s_cbranch_scc0 .LBB0_1491
	s_mov_b64 s[14:15], 0xb0000
	s_and_b64 vcc, exec, s[6:7]
	s_cbranch_vccz .LBB0_1494
	s_barrier

.LBB0_1587:
	s_add_u32 s28, s24, 0xfff80080
	s_addc_u32 s29, s25, -1
	s_add_i32 s48, 0, 0x10000
	s_cmp_eq_u32 s51, 28
	s_cselect_b32 s39, s9, s29
	s_cselect_b32 s38, s11, s28
	s_cselect_b32 s31, s45, s50
	s_cselect_b32 s30, s46, s47
	s_add_i32 s49, 0, 0x14000
	v_add_u32_e32 v154, s48, v139
	v_add_u32_e32 v170, s49, v139
	ds_read_b128 v[142:145], v154
	ds_read_b128 v[146:149], v154 offset:1024
	ds_read_b128 v[150:153], v154 offset:2048
	ds_read_b128 v[154:157], v154 offset:3072
	ds_read_b128 v[158:161], v170
	ds_read_b128 v[162:165], v170 offset:1024
	ds_read_b128 v[166:169], v170 offset:2048
	ds_read_b128 v[170:173], v170 offset:3072
	v_lshl_add_u64 v[182:183], s[24:25], 0, v[134:135]
	s_add_i32 m0, s20, 0xc000
	ds_read_b128 v[174:177], v141
	ds_read_b128 v[178:181], v141 offset:1024
	ds_read_b128 v[194:197], v141 offset:2048
	ds_read_b128 v[198:201], v141 offset:3072
	ds_read_b128 v[202:205], v141 offset:4096
	ds_read_b128 v[206:209], v141 offset:5120
	ds_read_b128 v[224:227], v141 offset:6144
	ds_read_b128 v[228:231], v141 offset:7168
	global_load_lds_dwordx4 v[182:183], off
	v_lshl_add_u64 v[182:183], s[24:25], 0, v[136:137]
	s_add_i32 m0, s20, 0xe000
	s_nop 0
	global_load_lds_dwordx4 v[182:183], off
	s_waitcnt vmcnt(8)
	s_waitcnt lgkmcnt(0)
	s_barrier
	s_setprio 1
	s_waitcnt lgkmcnt(0)
	v_mfma_f32_16x16x32_bf16 v[124:127], v[142:145], v[174:177], v[124:127]
	v_mfma_f32_16x16x32_bf16 v[116:119], v[150:153], v[174:177], v[116:119]
	v_mfma_f32_16x16x32_bf16 v[100:103], v[150:153], v[194:197], v[100:103]
	v_mfma_f32_16x16x32_bf16 v[108:111], v[142:145], v[194:197], v[108:111]
	v_mfma_f32_16x16x32_bf16 v[92:95], v[142:145], v[202:205], v[92:95]
	v_mfma_f32_16x16x32_bf16 v[84:87], v[150:153], v[202:205], v[84:87]
	v_mfma_f32_16x16x32_bf16 v[68:71], v[150:153], v[224:227], v[68:71]
	v_mfma_f32_16x16x32_bf16 v[76:79], v[142:145], v[224:227], v[76:79]
	v_mfma_f32_16x16x32_bf16 v[124:127], v[146:149], v[178:181], v[124:127]
	v_mfma_f32_16x16x32_bf16 v[116:119], v[154:157], v[178:181], v[116:119]
	v_mfma_f32_16x16x32_bf16 v[100:103], v[154:157], v[198:201], v[100:103]
	v_mfma_f32_16x16x32_bf16 v[108:111], v[146:149], v[198:201], v[108:111]
	v_mfma_f32_16x16x32_bf16 v[92:95], v[146:149], v[206:209], v[92:95]
	v_mfma_f32_16x16x32_bf16 v[84:87], v[154:157], v[206:209], v[84:87]
	v_mfma_f32_16x16x32_bf16 v[68:71], v[154:157], v[228:231], v[68:71]
	v_mfma_f32_16x16x32_bf16 v[76:79], v[146:149], v[228:231], v[76:79]
	s_setprio 0
	s_setprio 1
	v_mfma_f32_16x16x32_bf16 v[120:123], v[158:161], v[174:177], v[120:123]
	v_mfma_f32_16x16x32_bf16 v[112:115], v[166:169], v[174:177], v[112:115]
	v_mfma_f32_16x16x32_bf16 v[96:99], v[166:169], v[194:197], v[96:99]
	v_mfma_f32_16x16x32_bf16 v[104:107], v[158:161], v[194:197], v[104:107]
	v_mfma_f32_16x16x32_bf16 v[88:91], v[158:161], v[202:205], v[88:91]
	v_mfma_f32_16x16x32_bf16 v[80:83], v[166:169], v[202:205], v[80:83]
	v_mfma_f32_16x16x32_bf16 v[64:67], v[166:169], v[224:227], v[64:67]
	v_mfma_f32_16x16x32_bf16 v[72:75], v[158:161], v[224:227], v[72:75]
	v_mfma_f32_16x16x32_bf16 v[120:123], v[162:165], v[178:181], v[120:123]
	v_mfma_f32_16x16x32_bf16 v[112:115], v[170:173], v[178:181], v[112:115]
	v_mfma_f32_16x16x32_bf16 v[96:99], v[170:173], v[198:201], v[96:99]
	v_mfma_f32_16x16x32_bf16 v[104:107], v[162:165], v[198:201], v[104:107]
	v_mfma_f32_16x16x32_bf16 v[88:91], v[162:165], v[206:209], v[88:91]
	v_mfma_f32_16x16x32_bf16 v[80:83], v[170:173], v[206:209], v[80:83]
	v_mfma_f32_16x16x32_bf16 v[64:67], v[170:173], v[228:231], v[64:67]
	v_mfma_f32_16x16x32_bf16 v[72:75], v[162:165], v[228:231], v[72:75]
	s_setprio 0
	s_barrier
	s_add_i32 s28, s48, s4
	v_lshl_add_u64 v[182:183], s[30:31], 0, v[184:185]
	s_mov_b32 m0, s28
	ds_read_b128 v[174:177], v141 offset:16384
	ds_read_b128 v[178:181], v141 offset:17408
	ds_read_b128 v[194:197], v141 offset:18432
	ds_read_b128 v[198:201], v141 offset:19456
	ds_read_b128 v[202:205], v141 offset:20480
	ds_read_b128 v[206:209], v141 offset:21504
	ds_read_b128 v[224:227], v141 offset:22528
	ds_read_b128 v[228:231], v141 offset:23552
	global_load_lds_dwordx4 v[182:183], off
	s_add_i32 m0, s28, 0x2000
	s_add_u32 s28, s30, 0x80000
	v_lshl_add_u64 v[210:211], s[30:31], 0, v[128:129]
	s_addc_u32 s29, s31, 0
	s_add_i32 s48, s49, s4
	global_load_lds_dwordx4 v[210:211], off
	v_lshl_add_u64 v[216:217], s[28:29], 0, v[184:185]
	s_mov_b32 m0, s48
	v_lshl_add_u64 v[218:219], s[38:39], 0, v[130:131]
	global_load_lds_dwordx4 v[216:217], off
	v_lshl_add_u64 v[216:217], s[28:29], 0, v[128:129]
	s_add_i32 m0, s48, 0x2000
	s_nop 0
	global_load_lds_dwordx4 v[216:217], off
	v_lshl_add_u64 v[216:217], s[38:39], 0, v[132:133]
	s_mov_b32 m0, s20
	s_nop 0
	global_load_lds_dwordx4 v[216:217], off
	s_mov_b32 m0, s21
	s_nop 0
	global_load_lds_dwordx4 v[218:219], off
	s_waitcnt vmcnt(8)
	s_waitcnt lgkmcnt(0)
	s_barrier
	s_setprio 1
	s_waitcnt lgkmcnt(0)
	v_mfma_f32_16x16x32_bf16 v[60:63], v[142:145], v[174:177], v[60:63]
	v_mfma_f32_16x16x32_bf16 v[52:55], v[150:153], v[174:177], v[52:55]
	v_mfma_f32_16x16x32_bf16 v[36:39], v[150:153], v[194:197], v[36:39]
	v_mfma_f32_16x16x32_bf16 v[44:47], v[142:145], v[194:197], v[44:47]
	v_mfma_f32_16x16x32_bf16 v[28:31], v[142:145], v[202:205], v[28:31]
	v_mfma_f32_16x16x32_bf16 v[20:23], v[150:153], v[202:205], v[20:23]
	v_mfma_f32_16x16x32_bf16 v[4:7], v[150:153], v[224:227], v[4:7]
	v_mfma_f32_16x16x32_bf16 v[12:15], v[142:145], v[224:227], v[12:15]
	v_mfma_f32_16x16x32_bf16 v[60:63], v[146:149], v[178:181], v[60:63]
	v_mfma_f32_16x16x32_bf16 v[52:55], v[154:157], v[178:181], v[52:55]
	v_mfma_f32_16x16x32_bf16 v[36:39], v[154:157], v[198:201], v[36:39]
	v_mfma_f32_16x16x32_bf16 v[44:47], v[146:149], v[198:201], v[44:47]
	v_mfma_f32_16x16x32_bf16 v[28:31], v[146:149], v[206:209], v[28:31]
	v_mfma_f32_16x16x32_bf16 v[20:23], v[154:157], v[206:209], v[20:23]
	v_mfma_f32_16x16x32_bf16 v[4:7], v[154:157], v[228:231], v[4:7]
	v_mfma_f32_16x16x32_bf16 v[12:15], v[146:149], v[228:231], v[12:15]
	s_setprio 0
	s_setprio 1
	v_mfma_f32_16x16x32_bf16 v[56:59], v[158:161], v[174:177], v[56:59]
	v_mfma_f32_16x16x32_bf16 v[48:51], v[166:169], v[174:177], v[48:51]
	v_mfma_f32_16x16x32_bf16 v[32:35], v[166:169], v[194:197], v[32:35]
	v_mfma_f32_16x16x32_bf16 v[40:43], v[158:161], v[194:197], v[40:43]
	v_mfma_f32_16x16x32_bf16 v[24:27], v[158:161], v[202:205], v[24:27]
	v_mfma_f32_16x16x32_bf16 v[16:19], v[166:169], v[202:205], v[16:19]
	v_mfma_f32_16x16x32_bf16 v[0:3], v[166:169], v[224:227], v[0:3]
	v_mfma_f32_16x16x32_bf16 v[8:11], v[158:161], v[224:227], v[8:11]
	v_mfma_f32_16x16x32_bf16 v[56:59], v[162:165], v[178:181], v[56:59]
	v_mfma_f32_16x16x32_bf16 v[48:51], v[170:173], v[178:181], v[48:51]
	v_mfma_f32_16x16x32_bf16 v[32:35], v[170:173], v[198:201], v[32:35]
	v_mfma_f32_16x16x32_bf16 v[40:43], v[162:165], v[198:201], v[40:43]
	v_mfma_f32_16x16x32_bf16 v[24:27], v[162:165], v[206:209], v[24:27]
	v_mfma_f32_16x16x32_bf16 v[16:19], v[170:173], v[206:209], v[16:19]
	v_mfma_f32_16x16x32_bf16 v[0:3], v[170:173], v[228:231], v[0:3]
	v_mfma_f32_16x16x32_bf16 v[8:11], v[162:165], v[228:231], v[8:11]
	s_setprio 0
	s_barrier
	s_add_i32 s48, 0, 0x18000
	s_add_i32 s49, 0, 0x1c000
	v_add_u32_e32 v154, s48, v139
	v_add_u32_e32 v170, s49, v139
	ds_read_b128 v[142:145], v154
	ds_read_b128 v[146:149], v154 offset:1024
	ds_read_b128 v[150:153], v154 offset:2048
	ds_read_b128 v[154:157], v154 offset:3072
	ds_read_b128 v[158:161], v170
	ds_read_b128 v[162:165], v170 offset:1024
	ds_read_b128 v[166:169], v170 offset:2048
	ds_read_b128 v[170:173], v170 offset:3072
	s_add_u32 s28, s38, 0x80000
	s_addc_u32 s29, s39, 0
	s_mov_b32 m0, s26
	v_lshl_add_u64 v[232:233], s[28:29], 0, v[132:133]
	ds_read_b128 v[174:177], v141 offset:32768
	ds_read_b128 v[178:181], v141 offset:33792
	ds_read_b128 v[194:197], v141 offset:34816
	ds_read_b128 v[198:201], v141 offset:35840
	ds_read_b128 v[202:205], v141 offset:36864
	ds_read_b128 v[206:209], v141 offset:37888
	ds_read_b128 v[224:227], v141 offset:38912
	ds_read_b128 v[228:231], v141 offset:39936
	global_load_lds_dwordx4 v[232:233], off
	v_lshl_add_u64 v[232:233], s[28:29], 0, v[130:131]
	s_mov_b32 m0, s27
	s_nop 0
	global_load_lds_dwordx4 v[232:233], off
	s_waitcnt vmcnt(8)
	s_waitcnt lgkmcnt(0)
	s_barrier
	s_setprio 1
	s_waitcnt lgkmcnt(0)
	v_mfma_f32_16x16x32_bf16 v[124:127], v[142:145], v[174:177], v[124:127]
	v_mfma_f32_16x16x32_bf16 v[116:119], v[150:153], v[174:177], v[116:119]
	v_mfma_f32_16x16x32_bf16 v[100:103], v[150:153], v[194:197], v[100:103]
	v_mfma_f32_16x16x32_bf16 v[108:111], v[142:145], v[194:197], v[108:111]
	v_mfma_f32_16x16x32_bf16 v[92:95], v[142:145], v[202:205], v[92:95]
	v_mfma_f32_16x16x32_bf16 v[84:87], v[150:153], v[202:205], v[84:87]
	v_mfma_f32_16x16x32_bf16 v[68:71], v[150:153], v[224:227], v[68:71]
	v_mfma_f32_16x16x32_bf16 v[76:79], v[142:145], v[224:227], v[76:79]
	v_mfma_f32_16x16x32_bf16 v[124:127], v[146:149], v[178:181], v[124:127]
	v_mfma_f32_16x16x32_bf16 v[116:119], v[154:157], v[178:181], v[116:119]
	v_mfma_f32_16x16x32_bf16 v[100:103], v[154:157], v[198:201], v[100:103]
	v_mfma_f32_16x16x32_bf16 v[108:111], v[146:149], v[198:201], v[108:111]
	v_mfma_f32_16x16x32_bf16 v[92:95], v[146:149], v[206:209], v[92:95]
	v_mfma_f32_16x16x32_bf16 v[84:87], v[154:157], v[206:209], v[84:87]
	v_mfma_f32_16x16x32_bf16 v[68:71], v[154:157], v[228:231], v[68:71]
	v_mfma_f32_16x16x32_bf16 v[76:79], v[146:149], v[228:231], v[76:79]
	s_setprio 0
	s_setprio 1
	v_mfma_f32_16x16x32_bf16 v[120:123], v[158:161], v[174:177], v[120:123]
	v_mfma_f32_16x16x32_bf16 v[112:115], v[166:169], v[174:177], v[112:115]
	v_mfma_f32_16x16x32_bf16 v[96:99], v[166:169], v[194:197], v[96:99]
	v_mfma_f32_16x16x32_bf16 v[104:107], v[158:161], v[194:197], v[104:107]
	v_mfma_f32_16x16x32_bf16 v[88:91], v[158:161], v[202:205], v[88:91]
	v_mfma_f32_16x16x32_bf16 v[80:83], v[166:169], v[202:205], v[80:83]
	v_mfma_f32_16x16x32_bf16 v[64:67], v[166:169], v[224:227], v[64:67]
	v_mfma_f32_16x16x32_bf16 v[72:75], v[158:161], v[224:227], v[72:75]
	v_mfma_f32_16x16x32_bf16 v[120:123], v[162:165], v[178:181], v[120:123]
	v_mfma_f32_16x16x32_bf16 v[112:115], v[170:173], v[178:181], v[112:115]
	v_mfma_f32_16x16x32_bf16 v[96:99], v[170:173], v[198:201], v[96:99]
	v_mfma_f32_16x16x32_bf16 v[104:107], v[162:165], v[198:201], v[104:107]
	v_mfma_f32_16x16x32_bf16 v[88:91], v[162:165], v[206:209], v[88:91]
	v_mfma_f32_16x16x32_bf16 v[80:83], v[170:173], v[206:209], v[80:83]
	v_mfma_f32_16x16x32_bf16 v[64:67], v[170:173], v[228:231], v[64:67]
	v_mfma_f32_16x16x32_bf16 v[72:75], v[162:165], v[228:231], v[72:75]
	s_setprio 0
	s_barrier
	s_add_i32 s28, s48, s4
	v_lshl_add_u64 v[182:183], v[182:183], 0, s[68:69]
	s_mov_b32 m0, s28
	ds_read_b128 v[174:177], v141 offset:49152
	ds_read_b128 v[178:181], v141 offset:50176
	ds_read_b128 v[194:197], v141 offset:51200
	ds_read_b128 v[198:201], v141 offset:52224
	ds_read_b128 v[202:205], v141 offset:53248
	ds_read_b128 v[206:209], v141 offset:54272
	ds_read_b128 v[224:227], v141 offset:55296
	ds_read_b128 v[228:231], v141 offset:56320
	global_load_lds_dwordx4 v[182:183], off
	s_add_i32 m0, s28, 0x2000
	s_add_u32 s28, s30, 0x80080
	v_lshl_add_u64 v[182:183], v[210:211], 0, s[68:69]
	s_addc_u32 s29, s31, 0
	s_add_i32 s30, s49, s4
	global_load_lds_dwordx4 v[182:183], off
	v_lshl_add_u64 v[182:183], s[28:29], 0, v[184:185]
	s_mov_b32 m0, s30
	s_nop 0
	global_load_lds_dwordx4 v[182:183], off
	v_lshl_add_u64 v[182:183], s[28:29], 0, v[128:129]
	s_add_i32 m0, s30, 0x2000
	s_nop 0
	global_load_lds_dwordx4 v[182:183], off
	v_lshl_add_u64 v[182:183], v[216:217], 0, s[68:69]
	s_mov_b32 m0, s40
	s_nop 0
	global_load_lds_dwordx4 v[182:183], off
	v_lshl_add_u64 v[182:183], v[218:219], 0, s[68:69]
	s_mov_b32 m0, s41
	s_nop 0
	global_load_lds_dwordx4 v[182:183], off
	s_waitcnt vmcnt(8)
	s_waitcnt lgkmcnt(0)
	s_barrier
	s_setprio 1
	s_waitcnt lgkmcnt(0)
	v_mfma_f32_16x16x32_bf16 v[60:63], v[142:145], v[174:177], v[60:63]
	v_mfma_f32_16x16x32_bf16 v[52:55], v[150:153], v[174:177], v[52:55]
	v_mfma_f32_16x16x32_bf16 v[36:39], v[150:153], v[194:197], v[36:39]
	v_mfma_f32_16x16x32_bf16 v[44:47], v[142:145], v[194:197], v[44:47]
	v_mfma_f32_16x16x32_bf16 v[28:31], v[142:145], v[202:205], v[28:31]
	v_mfma_f32_16x16x32_bf16 v[20:23], v[150:153], v[202:205], v[20:23]
	v_mfma_f32_16x16x32_bf16 v[4:7], v[150:153], v[224:227], v[4:7]
	v_mfma_f32_16x16x32_bf16 v[12:15], v[142:145], v[224:227], v[12:15]
	v_mfma_f32_16x16x32_bf16 v[60:63], v[146:149], v[178:181], v[60:63]
	v_mfma_f32_16x16x32_bf16 v[52:55], v[154:157], v[178:181], v[52:55]
	v_mfma_f32_16x16x32_bf16 v[36:39], v[154:157], v[198:201], v[36:39]
	v_mfma_f32_16x16x32_bf16 v[44:47], v[146:149], v[198:201], v[44:47]
	v_mfma_f32_16x16x32_bf16 v[28:31], v[146:149], v[206:209], v[28:31]
	v_mfma_f32_16x16x32_bf16 v[20:23], v[154:157], v[206:209], v[20:23]
	v_mfma_f32_16x16x32_bf16 v[4:7], v[154:157], v[228:231], v[4:7]
	v_mfma_f32_16x16x32_bf16 v[12:15], v[146:149], v[228:231], v[12:15]
	s_setprio 0
	s_setprio 1
	v_mfma_f32_16x16x32_bf16 v[56:59], v[158:161], v[174:177], v[56:59]
	v_mfma_f32_16x16x32_bf16 v[48:51], v[166:169], v[174:177], v[48:51]
	v_mfma_f32_16x16x32_bf16 v[32:35], v[166:169], v[194:197], v[32:35]
	v_mfma_f32_16x16x32_bf16 v[40:43], v[158:161], v[194:197], v[40:43]
	v_mfma_f32_16x16x32_bf16 v[24:27], v[158:161], v[202:205], v[24:27]
	v_mfma_f32_16x16x32_bf16 v[16:19], v[166:169], v[202:205], v[16:19]
	v_mfma_f32_16x16x32_bf16 v[0:3], v[166:169], v[224:227], v[0:3]
	v_mfma_f32_16x16x32_bf16 v[8:11], v[158:161], v[224:227], v[8:11]
	v_mfma_f32_16x16x32_bf16 v[56:59], v[162:165], v[178:181], v[56:59]
	v_mfma_f32_16x16x32_bf16 v[48:51], v[170:173], v[178:181], v[48:51]
	v_mfma_f32_16x16x32_bf16 v[32:35], v[170:173], v[198:201], v[32:35]
	v_mfma_f32_16x16x32_bf16 v[40:43], v[162:165], v[198:201], v[40:43]
	v_mfma_f32_16x16x32_bf16 v[24:27], v[162:165], v[206:209], v[24:27]
	v_mfma_f32_16x16x32_bf16 v[16:19], v[170:173], v[206:209], v[16:19]
	v_mfma_f32_16x16x32_bf16 v[0:3], v[170:173], v[228:231], v[0:3]
	v_mfma_f32_16x16x32_bf16 v[8:11], v[162:165], v[228:231], v[8:11]
	s_setprio 0
	s_barrier
	s_add_i32 s51, s51, 2
	s_add_u32 s24, s24, 0x100
	s_addc_u32 s25, s25, 0
	s_add_u32 s47, s47, 0x100
	s_addc_u32 s50, s50, 0
	s_cmp_gt_u32 s51, 29
	s_cbranch_scc0 .LBB0_1587
	s_and_b64 vcc, exec, s[6:7]
	s_cbranch_vccz .LBB0_1590
	s_barrier

.LBB0_1661:
	s_add_u32 s24, s18, 0x100
	s_addc_u32 s25, s19, 0
	s_add_i32 s28, 0, 0x10000
	s_cmpk_eq_i32 s61, 0x54
	s_cselect_b32 s39, s51, s25
	s_cselect_b32 s38, s52, s24
	s_cselect_b32 s31, s53, s60
	s_cselect_b32 s30, s58, s59
	s_add_i32 s29, 0, 0x14000
	s_waitcnt vmcnt(0)
	v_add_u32_e32 v84, s28, v163
	v_add_u32_e32 v170, s29, v163
	ds_read_b128 v[64:67], v84
	ds_read_b128 v[68:71], v84 offset:1024
	ds_read_b128 v[80:83], v84 offset:2048
	ds_read_b128 v[84:87], v84 offset:3072
	ds_read_b128 v[154:157], v170
	ds_read_b128 v[158:161], v170 offset:1024
	ds_read_b128 v[166:169], v170 offset:2048
	ds_read_b128 v[170:173], v170 offset:3072
	v_lshl_add_u64 v[182:183], s[18:19], 0, v[150:151]
	s_add_i32 m0, s20, 0xc000
	ds_read_b128 v[174:177], v165
	ds_read_b128 v[178:181], v165 offset:1024
	ds_read_b128 v[194:197], v165 offset:2048
	ds_read_b128 v[198:201], v165 offset:3072
	ds_read_b128 v[202:205], v165 offset:4096
	ds_read_b128 v[206:209], v165 offset:5120
	ds_read_b128 v[224:227], v165 offset:6144
	ds_read_b128 v[228:231], v165 offset:7168
	global_load_lds_dwordx4 v[182:183], off
	v_lshl_add_u64 v[182:183], s[18:19], 0, v[152:153]
	s_add_i32 m0, s20, 0xe000
	s_nop 0
	global_load_lds_dwordx4 v[182:183], off
	s_waitcnt vmcnt(8)
	s_waitcnt lgkmcnt(0)
	s_barrier
	s_setprio 1
	s_waitcnt lgkmcnt(0)
	v_mfma_f32_16x16x32_bf16 v[140:143], v[64:67], v[174:177], v[140:143]
	v_mfma_f32_16x16x32_bf16 v[136:139], v[80:83], v[174:177], v[136:139]
	v_mfma_f32_16x16x32_bf16 v[120:123], v[80:83], v[194:197], v[120:123]
	v_mfma_f32_16x16x32_bf16 v[124:127], v[64:67], v[194:197], v[124:127]
	v_mfma_f32_16x16x32_bf16 v[108:111], v[64:67], v[202:205], v[108:111]
	v_mfma_f32_16x16x32_bf16 v[104:107], v[80:83], v[202:205], v[104:107]
	v_mfma_f32_16x16x32_bf16 v[88:91], v[80:83], v[224:227], v[88:91]
	v_mfma_f32_16x16x32_bf16 v[92:95], v[64:67], v[224:227], v[92:95]
	v_mfma_f32_16x16x32_bf16 v[140:143], v[68:71], v[178:181], v[140:143]
	v_mfma_f32_16x16x32_bf16 v[136:139], v[84:87], v[178:181], v[136:139]
	v_mfma_f32_16x16x32_bf16 v[120:123], v[84:87], v[198:201], v[120:123]
	v_mfma_f32_16x16x32_bf16 v[124:127], v[68:71], v[198:201], v[124:127]
	v_mfma_f32_16x16x32_bf16 v[108:111], v[68:71], v[206:209], v[108:111]
	v_mfma_f32_16x16x32_bf16 v[104:107], v[84:87], v[206:209], v[104:107]
	v_mfma_f32_16x16x32_bf16 v[88:91], v[84:87], v[228:231], v[88:91]
	v_mfma_f32_16x16x32_bf16 v[92:95], v[68:71], v[228:231], v[92:95]
	s_setprio 0
	s_setprio 1
	v_mfma_f32_16x16x32_bf16 v[132:135], v[154:157], v[174:177], v[132:135]
	v_mfma_f32_16x16x32_bf16 v[128:131], v[166:169], v[174:177], v[128:131]
	v_mfma_f32_16x16x32_bf16 v[112:115], v[166:169], v[194:197], v[112:115]
	v_mfma_f32_16x16x32_bf16 v[116:119], v[154:157], v[194:197], v[116:119]
	v_mfma_f32_16x16x32_bf16 v[100:103], v[154:157], v[202:205], v[100:103]
	v_mfma_f32_16x16x32_bf16 v[96:99], v[166:169], v[202:205], v[96:99]
	v_mfma_f32_16x16x32_bf16 v[72:75], v[166:169], v[224:227], v[72:75]
	v_mfma_f32_16x16x32_bf16 v[76:79], v[154:157], v[224:227], v[76:79]
	v_mfma_f32_16x16x32_bf16 v[132:135], v[158:161], v[178:181], v[132:135]
	v_mfma_f32_16x16x32_bf16 v[128:131], v[170:173], v[178:181], v[128:131]
	v_mfma_f32_16x16x32_bf16 v[112:115], v[170:173], v[198:201], v[112:115]
	v_mfma_f32_16x16x32_bf16 v[116:119], v[158:161], v[198:201], v[116:119]
	v_mfma_f32_16x16x32_bf16 v[100:103], v[158:161], v[206:209], v[100:103]
	v_mfma_f32_16x16x32_bf16 v[96:99], v[170:173], v[206:209], v[96:99]
	v_mfma_f32_16x16x32_bf16 v[72:75], v[170:173], v[228:231], v[72:75]
	v_mfma_f32_16x16x32_bf16 v[76:79], v[158:161], v[228:231], v[76:79]
	s_setprio 0
	s_barrier
	s_add_i32 s18, s28, s4
	v_lshl_add_u64 v[182:183], s[30:31], 0, v[184:185]
	s_mov_b32 m0, s18
	ds_read_b128 v[174:177], v165 offset:16384
	ds_read_b128 v[178:181], v165 offset:17408
	ds_read_b128 v[194:197], v165 offset:18432
	ds_read_b128 v[198:201], v165 offset:19456
	ds_read_b128 v[202:205], v165 offset:20480
	ds_read_b128 v[206:209], v165 offset:21504
	ds_read_b128 v[224:227], v165 offset:22528
	ds_read_b128 v[228:231], v165 offset:23552
	global_load_lds_dwordx4 v[182:183], off
	s_add_i32 m0, s18, 0x2000
	s_add_u32 s18, s30, 0x160000
	v_lshl_add_u64 v[210:211], s[30:31], 0, v[144:145]
	s_addc_u32 s19, s31, 0
	s_add_i32 s28, s29, s4
	global_load_lds_dwordx4 v[210:211], off
	v_lshl_add_u64 v[216:217], s[18:19], 0, v[184:185]
	s_mov_b32 m0, s28
	v_lshl_add_u64 v[218:219], s[38:39], 0, v[146:147]
	global_load_lds_dwordx4 v[216:217], off
	v_lshl_add_u64 v[216:217], s[18:19], 0, v[144:145]
	s_add_i32 m0, s28, 0x2000
	s_nop 0
	global_load_lds_dwordx4 v[216:217], off
	v_lshl_add_u64 v[216:217], s[38:39], 0, v[148:149]
	s_mov_b32 m0, s20
	s_nop 0
	global_load_lds_dwordx4 v[216:217], off
	s_mov_b32 m0, s21
	s_nop 0
	global_load_lds_dwordx4 v[218:219], off
	s_waitcnt vmcnt(8)
	s_waitcnt lgkmcnt(0)
	s_barrier
	s_setprio 1
	s_waitcnt lgkmcnt(0)
	v_mfma_f32_16x16x32_bf16 v[60:63], v[64:67], v[174:177], v[60:63]
	v_mfma_f32_16x16x32_bf16 v[56:59], v[80:83], v[174:177], v[56:59]
	v_mfma_f32_16x16x32_bf16 v[40:43], v[80:83], v[194:197], v[40:43]
	v_mfma_f32_16x16x32_bf16 v[44:47], v[64:67], v[194:197], v[44:47]
	v_mfma_f32_16x16x32_bf16 v[28:31], v[64:67], v[202:205], v[28:31]
	v_mfma_f32_16x16x32_bf16 v[24:27], v[80:83], v[202:205], v[24:27]
	v_mfma_f32_16x16x32_bf16 v[8:11], v[80:83], v[224:227], v[8:11]
	v_mfma_f32_16x16x32_bf16 v[12:15], v[64:67], v[224:227], v[12:15]
	v_mfma_f32_16x16x32_bf16 v[60:63], v[68:71], v[178:181], v[60:63]
	v_mfma_f32_16x16x32_bf16 v[56:59], v[84:87], v[178:181], v[56:59]
	v_mfma_f32_16x16x32_bf16 v[40:43], v[84:87], v[198:201], v[40:43]
	v_mfma_f32_16x16x32_bf16 v[44:47], v[68:71], v[198:201], v[44:47]
	v_mfma_f32_16x16x32_bf16 v[28:31], v[68:71], v[206:209], v[28:31]
	v_mfma_f32_16x16x32_bf16 v[24:27], v[84:87], v[206:209], v[24:27]
	v_mfma_f32_16x16x32_bf16 v[8:11], v[84:87], v[228:231], v[8:11]
	v_mfma_f32_16x16x32_bf16 v[12:15], v[68:71], v[228:231], v[12:15]
	s_setprio 0
	s_setprio 1
	v_mfma_f32_16x16x32_bf16 v[52:55], v[154:157], v[174:177], v[52:55]
	v_mfma_f32_16x16x32_bf16 v[48:51], v[166:169], v[174:177], v[48:51]
	v_mfma_f32_16x16x32_bf16 v[32:35], v[166:169], v[194:197], v[32:35]
	v_mfma_f32_16x16x32_bf16 v[36:39], v[154:157], v[194:197], v[36:39]
	v_mfma_f32_16x16x32_bf16 v[20:23], v[154:157], v[202:205], v[20:23]
	v_mfma_f32_16x16x32_bf16 v[16:19], v[166:169], v[202:205], v[16:19]
	v_mfma_f32_16x16x32_bf16 v[0:3], v[166:169], v[224:227], v[0:3]
	v_mfma_f32_16x16x32_bf16 v[4:7], v[154:157], v[224:227], v[4:7]
	v_mfma_f32_16x16x32_bf16 v[52:55], v[158:161], v[178:181], v[52:55]
	v_mfma_f32_16x16x32_bf16 v[48:51], v[170:173], v[178:181], v[48:51]
	v_mfma_f32_16x16x32_bf16 v[32:35], v[170:173], v[198:201], v[32:35]
	v_mfma_f32_16x16x32_bf16 v[36:39], v[158:161], v[198:201], v[36:39]
	v_mfma_f32_16x16x32_bf16 v[20:23], v[158:161], v[206:209], v[20:23]
	v_mfma_f32_16x16x32_bf16 v[16:19], v[170:173], v[206:209], v[16:19]
	v_mfma_f32_16x16x32_bf16 v[0:3], v[170:173], v[228:231], v[0:3]
	v_mfma_f32_16x16x32_bf16 v[4:7], v[158:161], v[228:231], v[4:7]
	s_setprio 0
	s_barrier
	s_add_i32 s28, 0, 0x18000
	s_add_i32 s29, 0, 0x1c000
	v_add_u32_e32 v84, s28, v163
	v_add_u32_e32 v170, s29, v163
	ds_read_b128 v[64:67], v84
	ds_read_b128 v[68:71], v84 offset:1024
	ds_read_b128 v[80:83], v84 offset:2048
	ds_read_b128 v[84:87], v84 offset:3072
	ds_read_b128 v[154:157], v170
	ds_read_b128 v[158:161], v170 offset:1024
	ds_read_b128 v[166:169], v170 offset:2048
	ds_read_b128 v[170:173], v170 offset:3072
	s_add_u32 s18, s38, 0x160000
	s_addc_u32 s19, s39, 0
	s_mov_b32 m0, s26
	v_lshl_add_u64 v[232:233], s[18:19], 0, v[148:149]
	ds_read_b128 v[174:177], v165 offset:32768
	ds_read_b128 v[178:181], v165 offset:33792
	ds_read_b128 v[194:197], v165 offset:34816
	ds_read_b128 v[198:201], v165 offset:35840
	ds_read_b128 v[202:205], v165 offset:36864
	ds_read_b128 v[206:209], v165 offset:37888
	ds_read_b128 v[224:227], v165 offset:38912
	ds_read_b128 v[228:231], v165 offset:39936
	global_load_lds_dwordx4 v[232:233], off
	v_lshl_add_u64 v[232:233], s[18:19], 0, v[146:147]
	s_mov_b32 m0, s27
	s_nop 0
	global_load_lds_dwordx4 v[232:233], off
	s_waitcnt vmcnt(8)
	s_waitcnt lgkmcnt(0)
	s_barrier
	s_setprio 1
	s_waitcnt lgkmcnt(0)
	v_mfma_f32_16x16x32_bf16 v[140:143], v[64:67], v[174:177], v[140:143]
	v_mfma_f32_16x16x32_bf16 v[136:139], v[80:83], v[174:177], v[136:139]
	v_mfma_f32_16x16x32_bf16 v[120:123], v[80:83], v[194:197], v[120:123]
	v_mfma_f32_16x16x32_bf16 v[124:127], v[64:67], v[194:197], v[124:127]
	v_mfma_f32_16x16x32_bf16 v[108:111], v[64:67], v[202:205], v[108:111]
	v_mfma_f32_16x16x32_bf16 v[104:107], v[80:83], v[202:205], v[104:107]
	v_mfma_f32_16x16x32_bf16 v[88:91], v[80:83], v[224:227], v[88:91]
	v_mfma_f32_16x16x32_bf16 v[92:95], v[64:67], v[224:227], v[92:95]
	v_mfma_f32_16x16x32_bf16 v[140:143], v[68:71], v[178:181], v[140:143]
	v_mfma_f32_16x16x32_bf16 v[136:139], v[84:87], v[178:181], v[136:139]
	v_mfma_f32_16x16x32_bf16 v[120:123], v[84:87], v[198:201], v[120:123]
	v_mfma_f32_16x16x32_bf16 v[124:127], v[68:71], v[198:201], v[124:127]
	v_mfma_f32_16x16x32_bf16 v[108:111], v[68:71], v[206:209], v[108:111]
	v_mfma_f32_16x16x32_bf16 v[104:107], v[84:87], v[206:209], v[104:107]
	v_mfma_f32_16x16x32_bf16 v[88:91], v[84:87], v[228:231], v[88:91]
	v_mfma_f32_16x16x32_bf16 v[92:95], v[68:71], v[228:231], v[92:95]
	s_setprio 0
	s_setprio 1
	v_mfma_f32_16x16x32_bf16 v[132:135], v[154:157], v[174:177], v[132:135]
	v_mfma_f32_16x16x32_bf16 v[128:131], v[166:169], v[174:177], v[128:131]
	v_mfma_f32_16x16x32_bf16 v[112:115], v[166:169], v[194:197], v[112:115]
	v_mfma_f32_16x16x32_bf16 v[116:119], v[154:157], v[194:197], v[116:119]
	v_mfma_f32_16x16x32_bf16 v[100:103], v[154:157], v[202:205], v[100:103]
	v_mfma_f32_16x16x32_bf16 v[96:99], v[166:169], v[202:205], v[96:99]
	v_mfma_f32_16x16x32_bf16 v[72:75], v[166:169], v[224:227], v[72:75]
	v_mfma_f32_16x16x32_bf16 v[76:79], v[154:157], v[224:227], v[76:79]
	v_mfma_f32_16x16x32_bf16 v[132:135], v[158:161], v[178:181], v[132:135]
	v_mfma_f32_16x16x32_bf16 v[128:131], v[170:173], v[178:181], v[128:131]
	v_mfma_f32_16x16x32_bf16 v[112:115], v[170:173], v[198:201], v[112:115]
	v_mfma_f32_16x16x32_bf16 v[116:119], v[158:161], v[198:201], v[116:119]
	v_mfma_f32_16x16x32_bf16 v[100:103], v[158:161], v[206:209], v[100:103]
	v_mfma_f32_16x16x32_bf16 v[96:99], v[170:173], v[206:209], v[96:99]
	v_mfma_f32_16x16x32_bf16 v[72:75], v[170:173], v[228:231], v[72:75]
	v_mfma_f32_16x16x32_bf16 v[76:79], v[158:161], v[228:231], v[76:79]
	s_setprio 0
	s_barrier
	s_add_i32 s18, s28, s4
	v_lshl_add_u64 v[182:183], v[182:183], 0, s[68:69]
	s_mov_b32 m0, s18
	ds_read_b128 v[174:177], v165 offset:49152
	ds_read_b128 v[178:181], v165 offset:50176
	ds_read_b128 v[194:197], v165 offset:51200
	ds_read_b128 v[198:201], v165 offset:52224
	ds_read_b128 v[202:205], v165 offset:53248
	ds_read_b128 v[206:209], v165 offset:54272
	ds_read_b128 v[224:227], v165 offset:55296
	ds_read_b128 v[228:231], v165 offset:56320
	global_load_lds_dwordx4 v[182:183], off
	s_add_i32 m0, s18, 0x2000
	s_add_u32 s18, s30, 0x160080
	v_lshl_add_u64 v[182:183], v[210:211], 0, s[68:69]
	s_addc_u32 s19, s31, 0
	s_add_i32 s28, s29, s4
	global_load_lds_dwordx4 v[182:183], off
	v_lshl_add_u64 v[182:183], s[18:19], 0, v[184:185]
	s_mov_b32 m0, s28
	s_nop 0
	global_load_lds_dwordx4 v[182:183], off
	v_lshl_add_u64 v[182:183], s[18:19], 0, v[144:145]
	s_add_i32 m0, s28, 0x2000
	s_nop 0
	global_load_lds_dwordx4 v[182:183], off
	v_lshl_add_u64 v[182:183], v[216:217], 0, s[68:69]
	s_mov_b32 m0, s42
	s_nop 0
	global_load_lds_dwordx4 v[182:183], off
	v_lshl_add_u64 v[182:183], v[218:219], 0, s[68:69]
	s_mov_b32 m0, s43
	s_nop 0
	global_load_lds_dwordx4 v[182:183], off
	s_waitcnt vmcnt(8)
	s_waitcnt lgkmcnt(0)
	s_barrier
	s_setprio 1
	s_waitcnt lgkmcnt(0)
	v_mfma_f32_16x16x32_bf16 v[60:63], v[64:67], v[174:177], v[60:63]
	v_mfma_f32_16x16x32_bf16 v[56:59], v[80:83], v[174:177], v[56:59]
	v_mfma_f32_16x16x32_bf16 v[40:43], v[80:83], v[194:197], v[40:43]
	v_mfma_f32_16x16x32_bf16 v[44:47], v[64:67], v[194:197], v[44:47]
	v_mfma_f32_16x16x32_bf16 v[28:31], v[64:67], v[202:205], v[28:31]
	v_mfma_f32_16x16x32_bf16 v[24:27], v[80:83], v[202:205], v[24:27]
	v_mfma_f32_16x16x32_bf16 v[8:11], v[80:83], v[224:227], v[8:11]
	v_mfma_f32_16x16x32_bf16 v[12:15], v[64:67], v[224:227], v[12:15]
	v_mfma_f32_16x16x32_bf16 v[60:63], v[68:71], v[178:181], v[60:63]
	v_mfma_f32_16x16x32_bf16 v[56:59], v[84:87], v[178:181], v[56:59]
	v_mfma_f32_16x16x32_bf16 v[40:43], v[84:87], v[198:201], v[40:43]
	v_mfma_f32_16x16x32_bf16 v[44:47], v[68:71], v[198:201], v[44:47]
	v_mfma_f32_16x16x32_bf16 v[28:31], v[68:71], v[206:209], v[28:31]
	v_mfma_f32_16x16x32_bf16 v[24:27], v[84:87], v[206:209], v[24:27]
	v_mfma_f32_16x16x32_bf16 v[8:11], v[84:87], v[228:231], v[8:11]
	v_mfma_f32_16x16x32_bf16 v[12:15], v[68:71], v[228:231], v[12:15]
	s_setprio 0
	s_setprio 1
	v_mfma_f32_16x16x32_bf16 v[52:55], v[154:157], v[174:177], v[52:55]
	v_mfma_f32_16x16x32_bf16 v[48:51], v[166:169], v[174:177], v[48:51]
	v_mfma_f32_16x16x32_bf16 v[32:35], v[166:169], v[194:197], v[32:35]
	v_mfma_f32_16x16x32_bf16 v[36:39], v[154:157], v[194:197], v[36:39]
	v_mfma_f32_16x16x32_bf16 v[20:23], v[154:157], v[202:205], v[20:23]
	v_mfma_f32_16x16x32_bf16 v[16:19], v[166:169], v[202:205], v[16:19]
	v_mfma_f32_16x16x32_bf16 v[0:3], v[166:169], v[224:227], v[0:3]
	v_mfma_f32_16x16x32_bf16 v[4:7], v[154:157], v[224:227], v[4:7]
	v_mfma_f32_16x16x32_bf16 v[52:55], v[158:161], v[178:181], v[52:55]
	v_mfma_f32_16x16x32_bf16 v[48:51], v[170:173], v[178:181], v[48:51]
	v_mfma_f32_16x16x32_bf16 v[32:35], v[170:173], v[198:201], v[32:35]
	v_mfma_f32_16x16x32_bf16 v[36:39], v[158:161], v[198:201], v[36:39]
	v_mfma_f32_16x16x32_bf16 v[20:23], v[158:161], v[206:209], v[20:23]
	v_mfma_f32_16x16x32_bf16 v[16:19], v[170:173], v[206:209], v[16:19]
	v_mfma_f32_16x16x32_bf16 v[0:3], v[170:173], v[228:231], v[0:3]
	v_mfma_f32_16x16x32_bf16 v[4:7], v[158:161], v[228:231], v[4:7]
	s_setprio 0
	s_barrier
	s_add_i32 s61, s61, 2
	s_add_u32 s59, s59, 0x100
	s_addc_u32 s60, s60, 0
	s_cmpk_gt_u32 s61, 0x55
	s_mov_b64 s[18:19], s[24:25]
	s_cbranch_scc0 .LBB0_1661
	s_and_b64 vcc, exec, s[8:9]
	s_cbranch_vccz .LBB0_1664
	s_barrier

.LBB0_1741:
	s_add_u32 s38, s36, 0x100
	s_addc_u32 s39, s37, 0
	s_add_i32 s28, 0, 0x10000
	s_cmp_eq_u32 s59, 4
	s_cselect_b32 s43, s11, s39
	s_cselect_b32 s42, s50, s38
	s_cselect_b32 s41, s51, s58
	s_cselect_b32 s40, s52, s53
	s_add_i32 s48, 0, 0x14000
	v_add_u32_e32 v124, s28, v172
	v_add_u32_e32 v170, s48, v172
	ds_read_b128 v[112:115], v124
	ds_read_b128 v[116:119], v124 offset:1024
	ds_read_b128 v[120:123], v124 offset:2048
	ds_read_b128 v[124:127], v124 offset:3072
	ds_read_b128 v[176:179], v170
	ds_read_b128 v[180:183], v170 offset:1024
	ds_read_b128 v[194:197], v170 offset:2048
	ds_read_b128 v[198:201], v170 offset:3072
	v_lshl_add_u64 v[170:171], s[36:37], 0, v[166:167]
	s_add_i32 m0, s20, 0xc000
	ds_read_b128 v[202:205], v174
	ds_read_b128 v[206:209], v174 offset:1024
	ds_read_b128 v[224:227], v174 offset:2048
	ds_read_b128 v[228:231], v174 offset:3072
	ds_read_b128 v[232:235], v174 offset:4096
	ds_read_b128 v[236:239], v174 offset:5120
	ds_read_b128 v[240:243], v174 offset:6144
	ds_read_b128 v[244:247], v174 offset:7168
	global_load_lds_dwordx4 v[170:171], off
	v_lshl_add_u64 v[170:171], s[36:37], 0, v[168:169]
	s_add_i32 m0, s20, 0xe000
	s_nop 0
	global_load_lds_dwordx4 v[170:171], off
	s_waitcnt vmcnt(8)
	s_waitcnt lgkmcnt(0)
	s_barrier
	s_setprio 1
	s_waitcnt lgkmcnt(0)
	v_mfma_f32_16x16x32_bf16 v[140:143], v[112:115], v[202:205], v[140:143]
	v_mfma_f32_16x16x32_bf16 v[136:139], v[120:123], v[202:205], v[136:139]
	v_mfma_f32_16x16x32_bf16 v[104:107], v[120:123], v[224:227], v[104:107]
	v_mfma_f32_16x16x32_bf16 v[108:111], v[112:115], v[224:227], v[108:111]
	v_mfma_f32_16x16x32_bf16 v[92:95], v[112:115], v[232:235], v[92:95]
	v_mfma_f32_16x16x32_bf16 v[88:91], v[120:123], v[232:235], v[88:91]
	v_mfma_f32_16x16x32_bf16 v[72:75], v[120:123], v[240:243], v[72:75]
	v_mfma_f32_16x16x32_bf16 v[76:79], v[112:115], v[240:243], v[76:79]
	v_mfma_f32_16x16x32_bf16 v[140:143], v[116:119], v[206:209], v[140:143]
	v_mfma_f32_16x16x32_bf16 v[136:139], v[124:127], v[206:209], v[136:139]
	v_mfma_f32_16x16x32_bf16 v[104:107], v[124:127], v[228:231], v[104:107]
	v_mfma_f32_16x16x32_bf16 v[108:111], v[116:119], v[228:231], v[108:111]
	v_mfma_f32_16x16x32_bf16 v[92:95], v[116:119], v[236:239], v[92:95]
	v_mfma_f32_16x16x32_bf16 v[88:91], v[124:127], v[236:239], v[88:91]
	v_mfma_f32_16x16x32_bf16 v[72:75], v[124:127], v[244:247], v[72:75]
	v_mfma_f32_16x16x32_bf16 v[76:79], v[116:119], v[244:247], v[76:79]
	s_setprio 0
	s_setprio 1
	v_mfma_f32_16x16x32_bf16 v[132:135], v[176:179], v[202:205], v[132:135]
	v_mfma_f32_16x16x32_bf16 v[128:131], v[194:197], v[202:205], v[128:131]
	v_mfma_f32_16x16x32_bf16 v[96:99], v[194:197], v[224:227], v[96:99]
	v_mfma_f32_16x16x32_bf16 v[100:103], v[176:179], v[224:227], v[100:103]
	v_mfma_f32_16x16x32_bf16 v[84:87], v[176:179], v[232:235], v[84:87]
	v_mfma_f32_16x16x32_bf16 v[80:83], v[194:197], v[232:235], v[80:83]
	v_mfma_f32_16x16x32_bf16 v[64:67], v[194:197], v[240:243], v[64:67]
	v_mfma_f32_16x16x32_bf16 v[68:71], v[176:179], v[240:243], v[68:71]
	v_mfma_f32_16x16x32_bf16 v[132:135], v[180:183], v[206:209], v[132:135]
	v_mfma_f32_16x16x32_bf16 v[128:131], v[198:201], v[206:209], v[128:131]
	v_mfma_f32_16x16x32_bf16 v[96:99], v[198:201], v[228:231], v[96:99]
	v_mfma_f32_16x16x32_bf16 v[100:103], v[180:183], v[228:231], v[100:103]
	v_mfma_f32_16x16x32_bf16 v[84:87], v[180:183], v[236:239], v[84:87]
	v_mfma_f32_16x16x32_bf16 v[80:83], v[198:201], v[236:239], v[80:83]
	v_mfma_f32_16x16x32_bf16 v[64:67], v[198:201], v[244:247], v[64:67]
	v_mfma_f32_16x16x32_bf16 v[68:71], v[180:183], v[244:247], v[68:71]
	s_setprio 0
	s_barrier
	s_add_i32 s28, s28, s4
	v_lshl_add_u64 v[170:171], s[40:41], 0, v[184:185]
	s_mov_b32 m0, s28
	ds_read_b128 v[202:205], v174 offset:16384
	ds_read_b128 v[206:209], v174 offset:17408
	ds_read_b128 v[224:227], v174 offset:18432
	ds_read_b128 v[228:231], v174 offset:19456
	ds_read_b128 v[232:235], v174 offset:20480
	ds_read_b128 v[236:239], v174 offset:21504
	ds_read_b128 v[240:243], v174 offset:22528
	ds_read_b128 v[244:247], v174 offset:23552
	global_load_lds_dwordx4 v[170:171], off
	s_add_i32 m0, s28, 0x2000
	s_add_u32 s28, s40, 0x160000
	v_lshl_add_u64 v[210:211], s[40:41], 0, v[144:145]
	s_addc_u32 s29, s41, 0
	s_add_i32 s36, s48, s4
	global_load_lds_dwordx4 v[210:211], off
	v_lshl_add_u64 v[216:217], s[28:29], 0, v[184:185]
	s_mov_b32 m0, s36
	v_lshl_add_u64 v[218:219], s[42:43], 0, v[146:147]
	global_load_lds_dwordx4 v[216:217], off
	v_lshl_add_u64 v[216:217], s[28:29], 0, v[144:145]
	s_add_i32 m0, s36, 0x2000
	s_nop 0
	global_load_lds_dwordx4 v[216:217], off
	v_lshl_add_u64 v[216:217], s[42:43], 0, v[148:149]
	s_mov_b32 m0, s20
	s_nop 0
	global_load_lds_dwordx4 v[216:217], off
	s_mov_b32 m0, s21
	s_nop 0
	global_load_lds_dwordx4 v[218:219], off
	s_waitcnt vmcnt(8)
	s_waitcnt lgkmcnt(0)
	s_barrier
	s_setprio 1
	s_waitcnt lgkmcnt(0)
	v_mfma_f32_16x16x32_bf16 v[60:63], v[112:115], v[202:205], v[60:63]
	v_mfma_f32_16x16x32_bf16 v[56:59], v[120:123], v[202:205], v[56:59]
	v_mfma_f32_16x16x32_bf16 v[40:43], v[120:123], v[224:227], v[40:43]
	v_mfma_f32_16x16x32_bf16 v[44:47], v[112:115], v[224:227], v[44:47]
	v_mfma_f32_16x16x32_bf16 v[36:39], v[112:115], v[232:235], v[36:39]
	v_mfma_f32_16x16x32_bf16 v[28:31], v[120:123], v[232:235], v[28:31]
	v_mfma_f32_16x16x32_bf16 v[12:15], v[120:123], v[240:243], v[12:15]
	v_mfma_f32_16x16x32_bf16 v[20:23], v[112:115], v[240:243], v[20:23]
	v_mfma_f32_16x16x32_bf16 v[60:63], v[116:119], v[206:209], v[60:63]
	v_mfma_f32_16x16x32_bf16 v[56:59], v[124:127], v[206:209], v[56:59]
	v_mfma_f32_16x16x32_bf16 v[40:43], v[124:127], v[228:231], v[40:43]
	v_mfma_f32_16x16x32_bf16 v[44:47], v[116:119], v[228:231], v[44:47]
	v_mfma_f32_16x16x32_bf16 v[36:39], v[116:119], v[236:239], v[36:39]
	v_mfma_f32_16x16x32_bf16 v[28:31], v[124:127], v[236:239], v[28:31]
	v_mfma_f32_16x16x32_bf16 v[12:15], v[124:127], v[244:247], v[12:15]
	v_mfma_f32_16x16x32_bf16 v[20:23], v[116:119], v[244:247], v[20:23]
	s_setprio 0
	s_setprio 1
	v_mfma_f32_16x16x32_bf16 v[52:55], v[176:179], v[202:205], v[52:55]
	v_mfma_f32_16x16x32_bf16 v[48:51], v[194:197], v[202:205], v[48:51]
	v_mfma_f32_16x16x32_bf16 v[24:27], v[194:197], v[224:227], v[24:27]
	v_mfma_f32_16x16x32_bf16 v[32:35], v[176:179], v[224:227], v[32:35]
	v_mfma_f32_16x16x32_bf16 v[16:19], v[176:179], v[232:235], v[16:19]
	v_mfma_f32_16x16x32_bf16 v[8:11], v[194:197], v[232:235], v[8:11]
	v_mfma_f32_16x16x32_bf16 v[0:3], v[194:197], v[240:243], v[0:3]
	v_mfma_f32_16x16x32_bf16 v[4:7], v[176:179], v[240:243], v[4:7]
	v_mfma_f32_16x16x32_bf16 v[52:55], v[180:183], v[206:209], v[52:55]
	v_mfma_f32_16x16x32_bf16 v[48:51], v[198:201], v[206:209], v[48:51]
	v_mfma_f32_16x16x32_bf16 v[24:27], v[198:201], v[228:231], v[24:27]
	v_mfma_f32_16x16x32_bf16 v[32:35], v[180:183], v[228:231], v[32:35]
	v_mfma_f32_16x16x32_bf16 v[16:19], v[180:183], v[236:239], v[16:19]
	v_mfma_f32_16x16x32_bf16 v[8:11], v[198:201], v[236:239], v[8:11]
	v_mfma_f32_16x16x32_bf16 v[0:3], v[198:201], v[244:247], v[0:3]
	v_mfma_f32_16x16x32_bf16 v[4:7], v[180:183], v[244:247], v[4:7]
	s_setprio 0
	s_barrier
	s_add_i32 s36, 0, 0x18000
	s_add_i32 s37, 0, 0x1c000
	v_add_u32_e32 v124, s36, v172
	v_add_u32_e32 v175, s37, v172
	ds_read_b128 v[112:115], v124
	ds_read_b128 v[116:119], v124 offset:1024
	ds_read_b128 v[120:123], v124 offset:2048
	ds_read_b128 v[124:127], v124 offset:3072
	ds_read_b128 v[176:179], v175
	ds_read_b128 v[180:183], v175 offset:1024
	ds_read_b128 v[194:197], v175 offset:2048
	ds_read_b128 v[198:201], v175 offset:3072
	s_add_u32 s28, s42, 0x160000
	s_addc_u32 s29, s43, 0
	s_mov_b32 m0, s26
	v_lshl_add_u64 v[220:221], s[28:29], 0, v[148:149]
	ds_read_b128 v[202:205], v174 offset:32768
	ds_read_b128 v[206:209], v174 offset:33792
	ds_read_b128 v[224:227], v174 offset:34816
	ds_read_b128 v[228:231], v174 offset:35840
	ds_read_b128 v[232:235], v174 offset:36864
	ds_read_b128 v[236:239], v174 offset:37888
	ds_read_b128 v[240:243], v174 offset:38912
	ds_read_b128 v[244:247], v174 offset:39936
	global_load_lds_dwordx4 v[220:221], off
	v_lshl_add_u64 v[220:221], s[28:29], 0, v[146:147]
	s_mov_b32 m0, s27
	s_nop 0
	global_load_lds_dwordx4 v[220:221], off
	s_waitcnt vmcnt(8)
	s_waitcnt lgkmcnt(0)
	s_barrier
	s_setprio 1
	s_waitcnt lgkmcnt(0)
	v_mfma_f32_16x16x32_bf16 v[140:143], v[112:115], v[202:205], v[140:143]
	v_mfma_f32_16x16x32_bf16 v[136:139], v[120:123], v[202:205], v[136:139]
	v_mfma_f32_16x16x32_bf16 v[104:107], v[120:123], v[224:227], v[104:107]
	v_mfma_f32_16x16x32_bf16 v[108:111], v[112:115], v[224:227], v[108:111]
	v_mfma_f32_16x16x32_bf16 v[92:95], v[112:115], v[232:235], v[92:95]
	v_mfma_f32_16x16x32_bf16 v[88:91], v[120:123], v[232:235], v[88:91]
	v_mfma_f32_16x16x32_bf16 v[72:75], v[120:123], v[240:243], v[72:75]
	v_mfma_f32_16x16x32_bf16 v[76:79], v[112:115], v[240:243], v[76:79]
	v_mfma_f32_16x16x32_bf16 v[140:143], v[116:119], v[206:209], v[140:143]
	v_mfma_f32_16x16x32_bf16 v[136:139], v[124:127], v[206:209], v[136:139]
	v_mfma_f32_16x16x32_bf16 v[104:107], v[124:127], v[228:231], v[104:107]
	v_mfma_f32_16x16x32_bf16 v[108:111], v[116:119], v[228:231], v[108:111]
	v_mfma_f32_16x16x32_bf16 v[92:95], v[116:119], v[236:239], v[92:95]
	v_mfma_f32_16x16x32_bf16 v[88:91], v[124:127], v[236:239], v[88:91]
	v_mfma_f32_16x16x32_bf16 v[72:75], v[124:127], v[244:247], v[72:75]
	v_mfma_f32_16x16x32_bf16 v[76:79], v[116:119], v[244:247], v[76:79]
	s_setprio 0
	s_setprio 1
	v_mfma_f32_16x16x32_bf16 v[132:135], v[176:179], v[202:205], v[132:135]
	v_mfma_f32_16x16x32_bf16 v[128:131], v[194:197], v[202:205], v[128:131]
	v_mfma_f32_16x16x32_bf16 v[96:99], v[194:197], v[224:227], v[96:99]
	v_mfma_f32_16x16x32_bf16 v[100:103], v[176:179], v[224:227], v[100:103]
	v_mfma_f32_16x16x32_bf16 v[84:87], v[176:179], v[232:235], v[84:87]
	v_mfma_f32_16x16x32_bf16 v[80:83], v[194:197], v[232:235], v[80:83]
	v_mfma_f32_16x16x32_bf16 v[64:67], v[194:197], v[240:243], v[64:67]
	v_mfma_f32_16x16x32_bf16 v[68:71], v[176:179], v[240:243], v[68:71]
	v_mfma_f32_16x16x32_bf16 v[132:135], v[180:183], v[206:209], v[132:135]
	v_mfma_f32_16x16x32_bf16 v[128:131], v[198:201], v[206:209], v[128:131]
	v_mfma_f32_16x16x32_bf16 v[96:99], v[198:201], v[228:231], v[96:99]
	v_mfma_f32_16x16x32_bf16 v[100:103], v[180:183], v[228:231], v[100:103]
	v_mfma_f32_16x16x32_bf16 v[84:87], v[180:183], v[236:239], v[84:87]
	v_mfma_f32_16x16x32_bf16 v[80:83], v[198:201], v[236:239], v[80:83]
	v_mfma_f32_16x16x32_bf16 v[64:67], v[198:201], v[244:247], v[64:67]
	v_mfma_f32_16x16x32_bf16 v[68:71], v[180:183], v[244:247], v[68:71]
	s_setprio 0
	s_barrier
	s_add_i32 s28, s36, s4
	v_lshl_add_u64 v[170:171], v[170:171], 0, s[68:69]
	s_mov_b32 m0, s28
	ds_read_b128 v[202:205], v174 offset:49152
	ds_read_b128 v[206:209], v174 offset:50176
	ds_read_b128 v[224:227], v174 offset:51200
	ds_read_b128 v[228:231], v174 offset:52224
	ds_read_b128 v[232:235], v174 offset:53248
	ds_read_b128 v[236:239], v174 offset:54272
	ds_read_b128 v[240:243], v174 offset:55296
	ds_read_b128 v[244:247], v174 offset:56320
	global_load_lds_dwordx4 v[170:171], off
	s_add_i32 m0, s28, 0x2000
	s_add_u32 s28, s40, 0x160080
	v_lshl_add_u64 v[170:171], v[210:211], 0, s[68:69]
	s_addc_u32 s29, s41, 0
	s_add_i32 s36, s37, s4
	global_load_lds_dwordx4 v[170:171], off
	v_lshl_add_u64 v[170:171], s[28:29], 0, v[184:185]
	s_mov_b32 m0, s36
	s_nop 0
	global_load_lds_dwordx4 v[170:171], off
	v_lshl_add_u64 v[170:171], s[28:29], 0, v[144:145]
	s_add_i32 m0, s36, 0x2000
	s_nop 0
	global_load_lds_dwordx4 v[170:171], off
	v_lshl_add_u64 v[170:171], v[216:217], 0, s[68:69]
	s_mov_b32 m0, s44
	s_nop 0
	global_load_lds_dwordx4 v[170:171], off
	v_lshl_add_u64 v[170:171], v[218:219], 0, s[68:69]
	s_mov_b32 m0, s45
	s_nop 0
	global_load_lds_dwordx4 v[170:171], off
	s_waitcnt vmcnt(8)
	s_waitcnt lgkmcnt(0)
	s_barrier
	s_setprio 1
	s_waitcnt lgkmcnt(0)
	v_mfma_f32_16x16x32_bf16 v[60:63], v[112:115], v[202:205], v[60:63]
	v_mfma_f32_16x16x32_bf16 v[56:59], v[120:123], v[202:205], v[56:59]
	v_mfma_f32_16x16x32_bf16 v[40:43], v[120:123], v[224:227], v[40:43]
	v_mfma_f32_16x16x32_bf16 v[44:47], v[112:115], v[224:227], v[44:47]
	v_mfma_f32_16x16x32_bf16 v[36:39], v[112:115], v[232:235], v[36:39]
	v_mfma_f32_16x16x32_bf16 v[28:31], v[120:123], v[232:235], v[28:31]
	v_mfma_f32_16x16x32_bf16 v[12:15], v[120:123], v[240:243], v[12:15]
	v_mfma_f32_16x16x32_bf16 v[20:23], v[112:115], v[240:243], v[20:23]
	v_mfma_f32_16x16x32_bf16 v[60:63], v[116:119], v[206:209], v[60:63]
	v_mfma_f32_16x16x32_bf16 v[56:59], v[124:127], v[206:209], v[56:59]
	v_mfma_f32_16x16x32_bf16 v[40:43], v[124:127], v[228:231], v[40:43]
	v_mfma_f32_16x16x32_bf16 v[44:47], v[116:119], v[228:231], v[44:47]
	v_mfma_f32_16x16x32_bf16 v[36:39], v[116:119], v[236:239], v[36:39]
	v_mfma_f32_16x16x32_bf16 v[28:31], v[124:127], v[236:239], v[28:31]
	v_mfma_f32_16x16x32_bf16 v[12:15], v[124:127], v[244:247], v[12:15]
	v_mfma_f32_16x16x32_bf16 v[20:23], v[116:119], v[244:247], v[20:23]
	s_setprio 0
	s_setprio 1
	v_mfma_f32_16x16x32_bf16 v[52:55], v[176:179], v[202:205], v[52:55]
	v_mfma_f32_16x16x32_bf16 v[48:51], v[194:197], v[202:205], v[48:51]
	v_mfma_f32_16x16x32_bf16 v[24:27], v[194:197], v[224:227], v[24:27]
	v_mfma_f32_16x16x32_bf16 v[32:35], v[176:179], v[224:227], v[32:35]
	v_mfma_f32_16x16x32_bf16 v[16:19], v[176:179], v[232:235], v[16:19]
	v_mfma_f32_16x16x32_bf16 v[8:11], v[194:197], v[232:235], v[8:11]
	v_mfma_f32_16x16x32_bf16 v[0:3], v[194:197], v[240:243], v[0:3]
	v_mfma_f32_16x16x32_bf16 v[4:7], v[176:179], v[240:243], v[4:7]
	v_mfma_f32_16x16x32_bf16 v[52:55], v[180:183], v[206:209], v[52:55]
	v_mfma_f32_16x16x32_bf16 v[48:51], v[198:201], v[206:209], v[48:51]
	v_mfma_f32_16x16x32_bf16 v[24:27], v[198:201], v[228:231], v[24:27]
	v_mfma_f32_16x16x32_bf16 v[32:35], v[180:183], v[228:231], v[32:35]
	v_mfma_f32_16x16x32_bf16 v[16:19], v[180:183], v[236:239], v[16:19]
	v_mfma_f32_16x16x32_bf16 v[8:11], v[198:201], v[236:239], v[8:11]
	v_mfma_f32_16x16x32_bf16 v[0:3], v[198:201], v[244:247], v[0:3]
	v_mfma_f32_16x16x32_bf16 v[4:7], v[180:183], v[244:247], v[4:7]
	s_setprio 0
	s_barrier
	s_add_i32 s59, s59, 2
	s_add_u32 s53, s53, 0x100
	s_addc_u32 s58, s58, 0
	s_cmp_gt_u32 s59, 5
	s_mov_b64 s[36:37], s[38:39]
	s_cbranch_scc0 .LBB0_1741
	s_and_b64 vcc, exec, s[8:9]
	s_cbranch_vccz .LBB0_1744
	s_barrier
